# LoRA GEMMs: first (only) K-loop iteration peeled with SrcC = 0, zeroing moves removed
# speedup vs baseline: 1.0488x; 1.0026x over previous
; #define PG8_STAGE(bufoff, goff, voff) do { _Pragma("unroll") for (int _i = 0; _i < 2; ++_i) \
;         __builtin_amdgcn_raw_ptr_buffer_load_lds(rsrc, (PG8_LAS void*)(lds + (bufoff) + ldsw + _i * 8192), 16, (int)(voff), (int)((goff) + _i * p1##voff), 0, 0); } while (0)
; #define PG8_LDA(dst, b, h) do { _Pragma("unroll") for (int m = 0; m < 4; ++m) dst[m] = PG8_LD8(lds + PG8_SA(b, h) + aoff + m * 2048); } while (0)
; #define PG8_LDB(dst, b, h) do { _Pragma("unroll") for (int n = 0; n < 2; ++n) dst[n] = PG8_LD8(lds + PG8_SB(b, h) + boff + n * 2048); } while (0)
; #define PG8_WAIT_V(n) asm volatile("s_waitcnt vmcnt(" #n ")" ::: "memory")
; #define PG8_WAIT_L(n) asm volatile("s_waitcnt lgkmcnt(" #n ")" ::: "memory")
; #define PG8_BAR __builtin_amdgcn_s_barrier()
; #define PG8_SCHED __builtin_amdgcn_sched_barrier(0)
; template <class Epi, class Sched, bool ALIGN_EPI, bool F8 = false, int F8SC = F8_SCALES>
; __device__ __forceinline__ void gemm_phase(PG8_LAS unsigned char* lds, const __amdgpu_buffer_rsrc_t rsrc, const int lda, const int ldb, const int K, const Sched& S, const Epi& E) {
;     ...
;         for (int t = 0; t < nt; t += 2) {
;             const bool last = (t == nt - 2);
;             const unsigned a1 = cA + (unsigned)(t + 1) * kstep;
;             const unsigned a2 = last ? nA : cA + (unsigned)(t + 2) * kstep, b2 = last ? nB : cB + (unsigned)(t + 2) * kstep;
;             const unsigned a3 = a2 + kstep, b3 = b2 + kstep;
;             PG8_LDB(B0, 0, 0); PG8_LDB(B1, 0, 1); PG8_SCHED; PG8_LDA(At, 0, 0); PG8_STAGE(PG8_SA(1, 1), a1 + hsA, voffA);
;             PG8_WAIT_V(8); PG8_WAIT_L(0); PG8_BAR; PG8_MMA(0, 0, At, B0); PG8_MMA(0, 1, At, B1); PG8_BAR; PG8_SCHED;
;             PG8_LDA(At, 0, 1); PG8_STAGE(PG8_SB(0, 0), b2, voffB); PG8_STAGE(PG8_SB(0, 1), b2 + hsB, voffB); PG8_STAGE(PG8_SA(0, 0), a2, voffA);
;             PG8_WAIT_V(8); PG8_WAIT_L(0); PG8_BAR; PG8_MMA(1, 0, At, B0); PG8_MMA(1, 1, At, B1); PG8_BAR; PG8_SCHED;
.LBB0_968:
	s_add_i32 s43, s42, 0x20080
	s_mov_b32 s44, 0
	s_mov_b64 s[6:7], -1
	s_mov_b64 s[14:15], 0
	s_waitcnt vmcnt(23)
	s_waitcnt vmcnt(22)
	ds_read_b128 v[82:85], v157
	ds_read_b128 v[90:93], v157 offset:1024
	ds_read_b128 v[98:101], v157 offset:2048
	ds_read_b128 v[106:109], v157 offset:3072
	ds_read_b128 v[150:153], v158
	ds_read_b128 v[162:165], v158 offset:1024
	ds_read_b128 v[166:169], v158 offset:2048
	ds_read_b128 v[170:173], v158 offset:3072
	s_add_i32 s45, s44, 0x100
	s_add_i32 s48, s45, s42
	s_and_b64 s[46:47], s[14:15], exec
	s_cselect_b32 s50, s37, s48
	s_add_i32 s46, s45, s41
	s_add_i32 s45, s50, 0x80
	s_and_b64 s[14:15], s[14:15], exec
	s_cselect_b32 s53, s38, s46
	s_add_i32 s56, s43, s44
	s_add_i32 s44, s53, 0x10080
	s_add_i32 s15, s53, 0x18080
	s_add_i32 s14, s50, 0x10080
	s_add_i32 s57, s56, 0x10000
	s_add_i32 s55, s53, 0x8000
	s_add_i32 s54, s53, 0x10000
	s_add_i32 s52, s53, 0x18000
	s_add_i32 s51, s50, 0x10000
	s_add_i32 s49, s50, 0x20000
	s_add_i32 s48, s50, 0x30000
	s_add_i32 s47, s53, 0x80
	s_add_i32 s46, s53, 0x8080
	s_mov_b32 s80, s96
	s_mov_b32 m0, s31
	ds_read_b128 v[174:177], v159
	ds_read_b128 v[178:181], v159 offset:1024
	ds_read_b128 v[182:185], v159 offset:2048
	ds_read_b128 v[186:189], v159 offset:3072
	ds_read_b128 v[190:193], v159 offset:4096
	ds_read_b128 v[194:197], v159 offset:5120
	ds_read_b128 v[198:201], v159 offset:6144
	ds_read_b128 v[202:205], v159 offset:7168
	buffer_load_dwordx4 v1, s[80:83], s56 offen lds
	s_mov_b32 m0, s33
	s_nop 0
	buffer_load_dwordx4 v1, s[80:83], s57 offen lds
	s_waitcnt vmcnt(8)
	s_waitcnt lgkmcnt(0)
	s_barrier
	s_setprio 1
	s_waitcnt lgkmcnt(7)
	v_mfma_f32_16x16x32_bf16 v[142:145], v[82:85], v[174:177], 0
	v_mfma_f32_16x16x32_bf16 v[138:141], v[98:101], v[174:177], 0
	s_waitcnt lgkmcnt(5)
	v_mfma_f32_16x16x32_bf16 v[126:129], v[82:85], v[182:185], 0
	v_mfma_f32_16x16x32_bf16 v[122:125], v[98:101], v[182:185], 0
	s_waitcnt lgkmcnt(3)
	v_mfma_f32_16x16x32_bf16 v[110:113], v[82:85], v[190:193], 0
	v_mfma_f32_16x16x32_bf16 v[102:105], v[98:101], v[190:193], 0
	s_waitcnt lgkmcnt(1)
	v_mfma_f32_16x16x32_bf16 v[78:81], v[82:85], v[198:201], 0
	v_mfma_f32_16x16x32_bf16 v[74:77], v[98:101], v[198:201], 0
	v_mfma_f32_16x16x32_bf16 v[142:145], v[90:93], v[178:181], v[142:145]
	v_mfma_f32_16x16x32_bf16 v[138:141], v[106:109], v[178:181], v[138:141]
	v_mfma_f32_16x16x32_bf16 v[126:129], v[90:93], v[186:189], v[126:129]
	v_mfma_f32_16x16x32_bf16 v[122:125], v[106:109], v[186:189], v[122:125]
	v_mfma_f32_16x16x32_bf16 v[110:113], v[90:93], v[194:197], v[110:113]
	v_mfma_f32_16x16x32_bf16 v[102:105], v[106:109], v[194:197], v[102:105]
	s_waitcnt lgkmcnt(0)
	v_mfma_f32_16x16x32_bf16 v[78:81], v[90:93], v[202:205], v[78:81]
	v_mfma_f32_16x16x32_bf16 v[74:77], v[106:109], v[202:205], v[74:77]
	s_setprio 0
	s_setprio 1
	v_mfma_f32_16x16x32_bf16 v[134:137], v[150:153], v[174:177], 0
	v_mfma_f32_16x16x32_bf16 v[130:133], v[166:169], v[174:177], 0
	v_mfma_f32_16x16x32_bf16 v[118:121], v[150:153], v[182:185], 0
	v_mfma_f32_16x16x32_bf16 v[114:117], v[166:169], v[182:185], 0
	v_mfma_f32_16x16x32_bf16 v[94:97], v[150:153], v[190:193], 0
	v_mfma_f32_16x16x32_bf16 v[86:89], v[166:169], v[190:193], 0
	v_mfma_f32_16x16x32_bf16 v[70:73], v[150:153], v[198:201], 0
	v_mfma_f32_16x16x32_bf16 v[66:69], v[166:169], v[198:201], 0
	v_mfma_f32_16x16x32_bf16 v[134:137], v[162:165], v[178:181], v[134:137]
	v_mfma_f32_16x16x32_bf16 v[130:133], v[170:173], v[178:181], v[130:133]
	v_mfma_f32_16x16x32_bf16 v[118:121], v[162:165], v[186:189], v[118:121]
	v_mfma_f32_16x16x32_bf16 v[114:117], v[170:173], v[186:189], v[114:117]
	v_mfma_f32_16x16x32_bf16 v[94:97], v[162:165], v[194:197], v[94:97]
	v_mfma_f32_16x16x32_bf16 v[86:89], v[170:173], v[194:197], v[86:89]
	v_mfma_f32_16x16x32_bf16 v[70:73], v[162:165], v[202:205], v[70:73]
	v_mfma_f32_16x16x32_bf16 v[66:69], v[170:173], v[202:205], v[66:69]
	s_setprio 0
	s_barrier
	s_mov_b32 m0, s17
	ds_read_b128 v[174:177], v159 offset:16384
	ds_read_b128 v[178:181], v159 offset:17408
	ds_read_b128 v[182:185], v159 offset:18432
	ds_read_b128 v[186:189], v159 offset:19456
	ds_read_b128 v[190:193], v159 offset:20480
	ds_read_b128 v[194:197], v159 offset:21504
	ds_read_b128 v[198:201], v159 offset:22528
	ds_read_b128 v[202:205], v159 offset:23552
	buffer_load_dwordx4 v156, s[80:83], s53 offen lds
	s_mov_b32 m0, s18
	s_nop 0
	buffer_load_dwordx4 v156, s[80:83], s55 offen lds
	s_mov_b32 m0, s19
	s_nop 0
	buffer_load_dwordx4 v156, s[80:83], s54 offen lds
	s_mov_b32 m0, s20
	s_nop 0
	buffer_load_dwordx4 v156, s[80:83], s52 offen lds
	s_mov_b32 m0, s16
	s_nop 0
	buffer_load_dwordx4 v1, s[80:83], s50 offen lds
	s_mov_b32 m0, s21
	s_nop 0
	buffer_load_dwordx4 v1, s[80:83], s51 offen lds
	s_waitcnt vmcnt(8)
	s_waitcnt lgkmcnt(0)
	s_barrier
; #define PG8_STAGE(bufoff, goff, voff) do { _Pragma("unroll") for (int _i = 0; _i < 2; ++_i) \
;         __builtin_amdgcn_raw_ptr_buffer_load_lds(rsrc, (PG8_LAS void*)(lds + (bufoff) + ldsw + _i * 8192), 16, (int)(voff), (int)((goff) + _i * p1##voff), 0, 0); } while (0)
; #define PG8_LDA(dst, b, h) do { _Pragma("unroll") for (int m = 0; m < 4; ++m) dst[m] = PG8_LD8(lds + PG8_SA(b, h) + aoff + m * 2048); } while (0)
; #define PG8_LDB(dst, b, h) do { _Pragma("unroll") for (int n = 0; n < 2; ++n) dst[n] = PG8_LD8(lds + PG8_SB(b, h) + boff + n * 2048); } while (0)
; #define PG8_WAIT_V(n) asm volatile("s_waitcnt vmcnt(" #n ")" ::: "memory")
; #define PG8_WAIT_L(n) asm volatile("s_waitcnt lgkmcnt(" #n ")" ::: "memory")
; #define PG8_BAR __builtin_amdgcn_s_barrier()
; #define PG8_SCHED __builtin_amdgcn_sched_barrier(0)
; template <class Epi, class Sched, bool ALIGN_EPI, bool F8 = false, int F8SC = F8_SCALES>
; __device__ __forceinline__ void gemm_phase(PG8_LAS unsigned char* lds, const __amdgpu_buffer_rsrc_t rsrc, const int lda, const int ldb, const int K, const Sched& S, const Epi& E) {
;     ...
;             PG8_WAIT_V(8); PG8_WAIT_L(0); PG8_BAR; PG8_MMA(0, 0, At, B0); PG8_MMA(0, 1, At, B1); PG8_BAR; PG8_SCHED;
;             PG8_LDA(At, 0, 1); PG8_STAGE(PG8_SB(0, 0), b2, voffB); PG8_STAGE(PG8_SB(0, 1), b2 + hsB, voffB); PG8_STAGE(PG8_SA(0, 0), a2, voffA);
;             PG8_WAIT_V(8); PG8_WAIT_L(0); PG8_BAR; PG8_MMA(1, 0, At, B0); PG8_MMA(1, 1, At, B1); PG8_BAR; PG8_SCHED;
;             PG8_LDB(B0, 1, 0); PG8_LDB(B1, 1, 1); PG8_SCHED; PG8_LDA(At, 1, 0); PG8_STAGE(PG8_SA(0, 1), a2 + hsA, voffA);
;             PG8_WAIT_V(8); PG8_WAIT_L(0); PG8_BAR; PG8_MMA(0, 0, At, B0); PG8_MMA(0, 1, At, B1); PG8_BAR; PG8_SCHED;
	s_setprio 1
	s_waitcnt lgkmcnt(7)
	v_mfma_f32_16x16x32_bf16 v[62:65], v[82:85], v[174:177], 0
	v_mfma_f32_16x16x32_bf16 v[58:61], v[98:101], v[174:177], 0
	s_waitcnt lgkmcnt(5)
	v_mfma_f32_16x16x32_bf16 v[46:49], v[82:85], v[182:185], 0
	v_mfma_f32_16x16x32_bf16 v[42:45], v[98:101], v[182:185], 0
	s_waitcnt lgkmcnt(3)
	v_mfma_f32_16x16x32_bf16 v[30:33], v[82:85], v[190:193], 0
	v_mfma_f32_16x16x32_bf16 v[26:29], v[98:101], v[190:193], 0
	s_waitcnt lgkmcnt(1)
	v_mfma_f32_16x16x32_bf16 v[14:17], v[82:85], v[198:201], 0
	v_mfma_f32_16x16x32_bf16 v[10:13], v[98:101], v[198:201], 0
	v_mfma_f32_16x16x32_bf16 v[62:65], v[90:93], v[178:181], v[62:65]
	v_mfma_f32_16x16x32_bf16 v[58:61], v[106:109], v[178:181], v[58:61]
	v_mfma_f32_16x16x32_bf16 v[46:49], v[90:93], v[186:189], v[46:49]
	v_mfma_f32_16x16x32_bf16 v[42:45], v[106:109], v[186:189], v[42:45]
	v_mfma_f32_16x16x32_bf16 v[30:33], v[90:93], v[194:197], v[30:33]
	v_mfma_f32_16x16x32_bf16 v[26:29], v[106:109], v[194:197], v[26:29]
	s_waitcnt lgkmcnt(0)
	v_mfma_f32_16x16x32_bf16 v[14:17], v[90:93], v[202:205], v[14:17]
	v_mfma_f32_16x16x32_bf16 v[10:13], v[106:109], v[202:205], v[10:13]
	s_setprio 0
	s_setprio 1
	v_mfma_f32_16x16x32_bf16 v[54:57], v[150:153], v[174:177], 0
	v_mfma_f32_16x16x32_bf16 v[50:53], v[166:169], v[174:177], 0
	v_mfma_f32_16x16x32_bf16 v[38:41], v[150:153], v[182:185], 0
	v_mfma_f32_16x16x32_bf16 v[34:37], v[166:169], v[182:185], 0
	v_mfma_f32_16x16x32_bf16 v[22:25], v[150:153], v[190:193], 0
	v_mfma_f32_16x16x32_bf16 v[18:21], v[166:169], v[190:193], 0
	v_mfma_f32_16x16x32_bf16 v[6:9], v[150:153], v[198:201], 0
	v_mfma_f32_16x16x32_bf16 v[2:5], v[166:169], v[198:201], 0
	v_mfma_f32_16x16x32_bf16 v[54:57], v[162:165], v[178:181], v[54:57]
	v_mfma_f32_16x16x32_bf16 v[50:53], v[170:173], v[178:181], v[50:53]
	v_mfma_f32_16x16x32_bf16 v[38:41], v[162:165], v[186:189], v[38:41]
	v_mfma_f32_16x16x32_bf16 v[34:37], v[170:173], v[186:189], v[34:37]
	v_mfma_f32_16x16x32_bf16 v[22:25], v[162:165], v[194:197], v[22:25]
	v_mfma_f32_16x16x32_bf16 v[18:21], v[170:173], v[194:197], v[18:21]
	v_mfma_f32_16x16x32_bf16 v[6:9], v[162:165], v[202:205], v[6:9]
	v_mfma_f32_16x16x32_bf16 v[2:5], v[170:173], v[202:205], v[2:5]
	s_setprio 0
	s_barrier
	ds_read_b128 v[82:85], v160
	ds_read_b128 v[90:93], v160 offset:1024
	ds_read_b128 v[98:101], v160 offset:2048
	ds_read_b128 v[106:109], v160 offset:3072
	ds_read_b128 v[150:153], v161
	ds_read_b128 v[162:165], v161 offset:1024
	ds_read_b128 v[166:169], v161 offset:2048
	ds_read_b128 v[170:173], v161 offset:3072
	s_mov_b32 m0, s22
	ds_read_b128 v[174:177], v159 offset:32768
	ds_read_b128 v[178:181], v159 offset:33792
	ds_read_b128 v[182:185], v159 offset:34816
	ds_read_b128 v[186:189], v159 offset:35840
	ds_read_b128 v[190:193], v159 offset:36864
	ds_read_b128 v[194:197], v159 offset:37888
	ds_read_b128 v[198:201], v159 offset:38912
	ds_read_b128 v[202:205], v159 offset:39936
	buffer_load_dwordx4 v1, s[80:83], s49 offen lds
	s_mov_b32 m0, s23
	s_nop 0
	buffer_load_dwordx4 v1, s[80:83], s48 offen lds
	s_waitcnt vmcnt(8)
	s_waitcnt lgkmcnt(0)
	s_barrier
	s_setprio 1
	s_waitcnt lgkmcnt(7)
	v_mfma_f32_16x16x32_bf16 v[142:145], v[82:85], v[174:177], v[142:145]
	v_mfma_f32_16x16x32_bf16 v[138:141], v[98:101], v[174:177], v[138:141]
	s_waitcnt lgkmcnt(5)
	v_mfma_f32_16x16x32_bf16 v[126:129], v[82:85], v[182:185], v[126:129]
	v_mfma_f32_16x16x32_bf16 v[122:125], v[98:101], v[182:185], v[122:125]
	s_waitcnt lgkmcnt(3)
	v_mfma_f32_16x16x32_bf16 v[110:113], v[82:85], v[190:193], v[110:113]
	v_mfma_f32_16x16x32_bf16 v[102:105], v[98:101], v[190:193], v[102:105]
	s_waitcnt lgkmcnt(1)
	v_mfma_f32_16x16x32_bf16 v[78:81], v[82:85], v[198:201], v[78:81]
	v_mfma_f32_16x16x32_bf16 v[74:77], v[98:101], v[198:201], v[74:77]
	v_mfma_f32_16x16x32_bf16 v[142:145], v[90:93], v[178:181], v[142:145]
	v_mfma_f32_16x16x32_bf16 v[138:141], v[106:109], v[178:181], v[138:141]
	v_mfma_f32_16x16x32_bf16 v[126:129], v[90:93], v[186:189], v[126:129]
	v_mfma_f32_16x16x32_bf16 v[122:125], v[106:109], v[186:189], v[122:125]
	v_mfma_f32_16x16x32_bf16 v[110:113], v[90:93], v[194:197], v[110:113]
	v_mfma_f32_16x16x32_bf16 v[102:105], v[106:109], v[194:197], v[102:105]
	s_waitcnt lgkmcnt(0)
	v_mfma_f32_16x16x32_bf16 v[78:81], v[90:93], v[202:205], v[78:81]
	v_mfma_f32_16x16x32_bf16 v[74:77], v[106:109], v[202:205], v[74:77]
	s_setprio 0
	s_setprio 1
	v_mfma_f32_16x16x32_bf16 v[134:137], v[150:153], v[174:177], v[134:137]
	v_mfma_f32_16x16x32_bf16 v[130:133], v[166:169], v[174:177], v[130:133]
	v_mfma_f32_16x16x32_bf16 v[118:121], v[150:153], v[182:185], v[118:121]
	v_mfma_f32_16x16x32_bf16 v[114:117], v[166:169], v[182:185], v[114:117]
	v_mfma_f32_16x16x32_bf16 v[94:97], v[150:153], v[190:193], v[94:97]
	v_mfma_f32_16x16x32_bf16 v[86:89], v[166:169], v[190:193], v[86:89]
	v_mfma_f32_16x16x32_bf16 v[70:73], v[150:153], v[198:201], v[70:73]
	v_mfma_f32_16x16x32_bf16 v[66:69], v[166:169], v[198:201], v[66:69]
	v_mfma_f32_16x16x32_bf16 v[134:137], v[162:165], v[178:181], v[134:137]
	v_mfma_f32_16x16x32_bf16 v[130:133], v[170:173], v[178:181], v[130:133]
	v_mfma_f32_16x16x32_bf16 v[118:121], v[162:165], v[186:189], v[118:121]
	v_mfma_f32_16x16x32_bf16 v[114:117], v[170:173], v[186:189], v[114:117]
	v_mfma_f32_16x16x32_bf16 v[94:97], v[162:165], v[194:197], v[94:97]
	v_mfma_f32_16x16x32_bf16 v[86:89], v[170:173], v[194:197], v[86:89]
	v_mfma_f32_16x16x32_bf16 v[70:73], v[162:165], v[202:205], v[70:73]
	v_mfma_f32_16x16x32_bf16 v[66:69], v[170:173], v[202:205], v[66:69]
	s_setprio 0
	s_barrier
; #define PG8_STAGE(bufoff, goff, voff) do { _Pragma("unroll") for (int _i = 0; _i < 2; ++_i) \
;         __builtin_amdgcn_raw_ptr_buffer_load_lds(rsrc, (PG8_LAS void*)(lds + (bufoff) + ldsw + _i * 8192), 16, (int)(voff), (int)((goff) + _i * p1##voff), 0, 0); } while (0)
; #define PG8_LDA(dst, b, h) do { _Pragma("unroll") for (int m = 0; m < 4; ++m) dst[m] = PG8_LD8(lds + PG8_SA(b, h) + aoff + m * 2048); } while (0)
; #define PG8_WAIT_V(n) asm volatile("s_waitcnt vmcnt(" #n ")" ::: "memory")
; #define PG8_WAIT_L(n) asm volatile("s_waitcnt lgkmcnt(" #n ")" ::: "memory")
; #define PG8_BAR __builtin_amdgcn_s_barrier()
; #define PG8_SCHED __builtin_amdgcn_sched_barrier(0)
; template <class Epi, class Sched, bool ALIGN_EPI, bool F8 = false, int F8SC = F8_SCALES>
; __device__ __forceinline__ void gemm_phase(PG8_LAS unsigned char* lds, const __amdgpu_buffer_rsrc_t rsrc, const int lda, const int ldb, const int K, const Sched& S, const Epi& E) {
;     ...
;             PG8_LDA(At, 1, 1); PG8_STAGE(PG8_SB(1, 0), b3, voffB); PG8_STAGE(PG8_SB(1, 1), b3 + hsB, voffB); PG8_STAGE(PG8_SA(1, 0), a3, voffA);
;             PG8_WAIT_V(8); PG8_WAIT_L(0); PG8_BAR; PG8_MMA(1, 0, At, B0); PG8_MMA(1, 1, At, B1); PG8_BAR; PG8_SCHED;
;         }
	s_mov_b32 m0, s25
	ds_read_b128 v[174:177], v159 offset:49152
	ds_read_b128 v[178:181], v159 offset:50176
	ds_read_b128 v[182:185], v159 offset:51200
	ds_read_b128 v[186:189], v159 offset:52224
	ds_read_b128 v[190:193], v159 offset:53248
	ds_read_b128 v[194:197], v159 offset:54272
	ds_read_b128 v[198:201], v159 offset:55296
	ds_read_b128 v[202:205], v159 offset:56320
	buffer_load_dwordx4 v156, s[80:83], s47 offen lds
	s_mov_b32 m0, s26
	s_nop 0
	buffer_load_dwordx4 v156, s[80:83], s46 offen lds
	s_mov_b32 m0, s29
	s_nop 0
	buffer_load_dwordx4 v156, s[80:83], s44 offen lds
	s_mov_b32 m0, s30
	s_nop 0
	buffer_load_dwordx4 v156, s[80:83], s15 offen lds
	s_mov_b32 m0, s27
	s_nop 0
	buffer_load_dwordx4 v1, s[80:83], s45 offen lds
	s_mov_b32 m0, s28
	s_nop 0
	buffer_load_dwordx4 v1, s[80:83], s14 offen lds
	s_waitcnt vmcnt(8)
	s_waitcnt lgkmcnt(0)
	s_barrier
	s_setprio 1
	s_waitcnt lgkmcnt(7)
	v_mfma_f32_16x16x32_bf16 v[62:65], v[82:85], v[174:177], v[62:65]
	v_mfma_f32_16x16x32_bf16 v[58:61], v[98:101], v[174:177], v[58:61]
	s_waitcnt lgkmcnt(5)
	v_mfma_f32_16x16x32_bf16 v[46:49], v[82:85], v[182:185], v[46:49]
	v_mfma_f32_16x16x32_bf16 v[42:45], v[98:101], v[182:185], v[42:45]
	s_waitcnt lgkmcnt(3)
	v_mfma_f32_16x16x32_bf16 v[30:33], v[82:85], v[190:193], v[30:33]
	v_mfma_f32_16x16x32_bf16 v[26:29], v[98:101], v[190:193], v[26:29]
	s_waitcnt lgkmcnt(1)
	v_mfma_f32_16x16x32_bf16 v[14:17], v[82:85], v[198:201], v[14:17]
	v_mfma_f32_16x16x32_bf16 v[10:13], v[98:101], v[198:201], v[10:13]
	v_mfma_f32_16x16x32_bf16 v[62:65], v[90:93], v[178:181], v[62:65]
	v_mfma_f32_16x16x32_bf16 v[58:61], v[106:109], v[178:181], v[58:61]
	v_mfma_f32_16x16x32_bf16 v[46:49], v[90:93], v[186:189], v[46:49]
	v_mfma_f32_16x16x32_bf16 v[42:45], v[106:109], v[186:189], v[42:45]
	v_mfma_f32_16x16x32_bf16 v[30:33], v[90:93], v[194:197], v[30:33]
	v_mfma_f32_16x16x32_bf16 v[26:29], v[106:109], v[194:197], v[26:29]
	s_waitcnt lgkmcnt(0)
	v_mfma_f32_16x16x32_bf16 v[14:17], v[90:93], v[202:205], v[14:17]
	v_mfma_f32_16x16x32_bf16 v[10:13], v[106:109], v[202:205], v[10:13]
	s_setprio 0
	s_setprio 1
	v_mfma_f32_16x16x32_bf16 v[54:57], v[150:153], v[174:177], v[54:57]
	v_mfma_f32_16x16x32_bf16 v[50:53], v[166:169], v[174:177], v[50:53]
	v_mfma_f32_16x16x32_bf16 v[38:41], v[150:153], v[182:185], v[38:41]
	v_mfma_f32_16x16x32_bf16 v[34:37], v[166:169], v[182:185], v[34:37]
	v_mfma_f32_16x16x32_bf16 v[22:25], v[150:153], v[190:193], v[22:25]
	v_mfma_f32_16x16x32_bf16 v[18:21], v[166:169], v[190:193], v[18:21]
	v_mfma_f32_16x16x32_bf16 v[6:9], v[150:153], v[198:201], v[6:9]
	v_mfma_f32_16x16x32_bf16 v[2:5], v[166:169], v[198:201], v[2:5]
	v_mfma_f32_16x16x32_bf16 v[54:57], v[162:165], v[178:181], v[54:57]
	v_mfma_f32_16x16x32_bf16 v[50:53], v[170:173], v[178:181], v[50:53]
	v_mfma_f32_16x16x32_bf16 v[38:41], v[162:165], v[186:189], v[38:41]
	v_mfma_f32_16x16x32_bf16 v[34:37], v[170:173], v[186:189], v[34:37]
	v_mfma_f32_16x16x32_bf16 v[22:25], v[162:165], v[194:197], v[22:25]
	v_mfma_f32_16x16x32_bf16 v[18:21], v[170:173], v[194:197], v[18:21]
	v_mfma_f32_16x16x32_bf16 v[6:9], v[162:165], v[202:205], v[6:9]
	v_mfma_f32_16x16x32_bf16 v[2:5], v[170:173], v[202:205], v[2:5]
	s_setprio 0
	s_barrier
	s_andn2_b64 vcc, exec, s[6:7]
	s_mov_b64 s[14:15], -1
	s_mov_b64 s[6:7], 0
	s_movk_i32 s44, 0x100
	s_cbranch_vccz .LBB0_969
	s_branch .Lpeel_after_969
.LBB0_969:
	ds_read_b128 v[82:85], v157
	ds_read_b128 v[90:93], v157 offset:1024
	ds_read_b128 v[98:101], v157 offset:2048
	ds_read_b128 v[106:109], v157 offset:3072
	ds_read_b128 v[150:153], v158
	ds_read_b128 v[162:165], v158 offset:1024
	ds_read_b128 v[166:169], v158 offset:2048
	ds_read_b128 v[170:173], v158 offset:3072
	s_add_i32 s45, s44, 0x100
	s_add_i32 s48, s45, s42
	s_and_b64 s[46:47], s[14:15], exec
	s_cselect_b32 s50, s37, s48
	s_add_i32 s46, s45, s41
	s_add_i32 s45, s50, 0x80
	s_and_b64 s[14:15], s[14:15], exec
	s_cselect_b32 s53, s38, s46
	s_add_i32 s56, s43, s44
	s_add_i32 s44, s53, 0x10080
	s_add_i32 s15, s53, 0x18080
	s_add_i32 s14, s50, 0x10080
	s_add_i32 s57, s56, 0x10000
	s_add_i32 s55, s53, 0x8000
	s_add_i32 s54, s53, 0x10000
	s_add_i32 s52, s53, 0x18000
	s_add_i32 s51, s50, 0x10000
	s_add_i32 s49, s50, 0x20000
	s_add_i32 s48, s50, 0x30000
	s_add_i32 s47, s53, 0x80
	s_add_i32 s46, s53, 0x8080
	s_mov_b32 s80, s96
	s_mov_b32 m0, s31
	ds_read_b128 v[174:177], v159
	ds_read_b128 v[178:181], v159 offset:1024
	ds_read_b128 v[182:185], v159 offset:2048
	ds_read_b128 v[186:189], v159 offset:3072
	ds_read_b128 v[190:193], v159 offset:4096
	ds_read_b128 v[194:197], v159 offset:5120
	ds_read_b128 v[198:201], v159 offset:6144
	ds_read_b128 v[202:205], v159 offset:7168
	buffer_load_dwordx4 v1, s[80:83], s56 offen lds
	s_mov_b32 m0, s33
	s_nop 0
	buffer_load_dwordx4 v1, s[80:83], s57 offen lds
	s_waitcnt vmcnt(8)
	s_waitcnt lgkmcnt(0)
	s_barrier
; #define PG8_STAGE(bufoff, goff, voff) do { _Pragma("unroll") for (int _i = 0; _i < 2; ++_i) \
;         __builtin_amdgcn_raw_ptr_buffer_load_lds(rsrc, (PG8_LAS void*)(lds + (bufoff) + ldsw + _i * 8192), 16, (int)(voff), (int)((goff) + _i * p1##voff), 0, 0); } while (0)
; #define PG8_LDA(dst, b, h) do { _Pragma("unroll") for (int m = 0; m < 4; ++m) dst[m] = PG8_LD8(lds + PG8_SA(b, h) + aoff + m * 2048); } while (0)
; #define PG8_LDB(dst, b, h) do { _Pragma("unroll") for (int n = 0; n < 2; ++n) dst[n] = PG8_LD8(lds + PG8_SB(b, h) + boff + n * 2048); } while (0)
; #define PG8_WAIT_V(n) asm volatile("s_waitcnt vmcnt(" #n ")" ::: "memory")
; #define PG8_WAIT_L(n) asm volatile("s_waitcnt lgkmcnt(" #n ")" ::: "memory")
; #define PG8_BAR __builtin_amdgcn_s_barrier()
; #define PG8_SCHED __builtin_amdgcn_sched_barrier(0)
; template <class Epi, class Sched, bool ALIGN_EPI, bool F8 = false, int F8SC = F8_SCALES>
; __device__ __forceinline__ void gemm_phase(PG8_LAS unsigned char* lds, const __amdgpu_buffer_rsrc_t rsrc, const int lda, const int ldb, const int K, const Sched& S, const Epi& E) {
;     ...
;             PG8_WAIT_V(8); PG8_WAIT_L(0); PG8_BAR; PG8_MMA(0, 0, At, B0); PG8_MMA(0, 1, At, B1); PG8_BAR; PG8_SCHED;
;             PG8_LDA(At, 0, 1); PG8_STAGE(PG8_SB(0, 0), b2, voffB); PG8_STAGE(PG8_SB(0, 1), b2 + hsB, voffB); PG8_STAGE(PG8_SA(0, 0), a2, voffA);
;             PG8_WAIT_V(8); PG8_WAIT_L(0); PG8_BAR; PG8_MMA(1, 0, At, B0); PG8_MMA(1, 1, At, B1); PG8_BAR; PG8_SCHED;
;             PG8_LDB(B0, 1, 0); PG8_LDB(B1, 1, 1); PG8_SCHED; PG8_LDA(At, 1, 0); PG8_STAGE(PG8_SA(0, 1), a2 + hsA, voffA);
;             PG8_WAIT_V(8); PG8_WAIT_L(0); PG8_BAR; PG8_MMA(0, 0, At, B0); PG8_MMA(0, 1, At, B1); PG8_BAR; PG8_SCHED;
	s_setprio 1
	s_waitcnt lgkmcnt(7)
	v_mfma_f32_16x16x32_bf16 v[142:145], v[82:85], v[174:177], v[142:145]
	v_mfma_f32_16x16x32_bf16 v[138:141], v[98:101], v[174:177], v[138:141]
	s_waitcnt lgkmcnt(5)
	v_mfma_f32_16x16x32_bf16 v[126:129], v[82:85], v[182:185], v[126:129]
	v_mfma_f32_16x16x32_bf16 v[122:125], v[98:101], v[182:185], v[122:125]
	s_waitcnt lgkmcnt(3)
	v_mfma_f32_16x16x32_bf16 v[110:113], v[82:85], v[190:193], v[110:113]
	v_mfma_f32_16x16x32_bf16 v[102:105], v[98:101], v[190:193], v[102:105]
	s_waitcnt lgkmcnt(1)
	v_mfma_f32_16x16x32_bf16 v[78:81], v[82:85], v[198:201], v[78:81]
	v_mfma_f32_16x16x32_bf16 v[74:77], v[98:101], v[198:201], v[74:77]
	v_mfma_f32_16x16x32_bf16 v[142:145], v[90:93], v[178:181], v[142:145]
	v_mfma_f32_16x16x32_bf16 v[138:141], v[106:109], v[178:181], v[138:141]
	v_mfma_f32_16x16x32_bf16 v[126:129], v[90:93], v[186:189], v[126:129]
	v_mfma_f32_16x16x32_bf16 v[122:125], v[106:109], v[186:189], v[122:125]
	v_mfma_f32_16x16x32_bf16 v[110:113], v[90:93], v[194:197], v[110:113]
	v_mfma_f32_16x16x32_bf16 v[102:105], v[106:109], v[194:197], v[102:105]
	s_waitcnt lgkmcnt(0)
	v_mfma_f32_16x16x32_bf16 v[78:81], v[90:93], v[202:205], v[78:81]
	v_mfma_f32_16x16x32_bf16 v[74:77], v[106:109], v[202:205], v[74:77]
	s_setprio 0
	s_setprio 1
	v_mfma_f32_16x16x32_bf16 v[134:137], v[150:153], v[174:177], v[134:137]
	v_mfma_f32_16x16x32_bf16 v[130:133], v[166:169], v[174:177], v[130:133]
	v_mfma_f32_16x16x32_bf16 v[118:121], v[150:153], v[182:185], v[118:121]
	v_mfma_f32_16x16x32_bf16 v[114:117], v[166:169], v[182:185], v[114:117]
	v_mfma_f32_16x16x32_bf16 v[94:97], v[150:153], v[190:193], v[94:97]
	v_mfma_f32_16x16x32_bf16 v[86:89], v[166:169], v[190:193], v[86:89]
	v_mfma_f32_16x16x32_bf16 v[70:73], v[150:153], v[198:201], v[70:73]
	v_mfma_f32_16x16x32_bf16 v[66:69], v[166:169], v[198:201], v[66:69]
	v_mfma_f32_16x16x32_bf16 v[134:137], v[162:165], v[178:181], v[134:137]
	v_mfma_f32_16x16x32_bf16 v[130:133], v[170:173], v[178:181], v[130:133]
	v_mfma_f32_16x16x32_bf16 v[118:121], v[162:165], v[186:189], v[118:121]
	v_mfma_f32_16x16x32_bf16 v[114:117], v[170:173], v[186:189], v[114:117]
	v_mfma_f32_16x16x32_bf16 v[94:97], v[162:165], v[194:197], v[94:97]
	v_mfma_f32_16x16x32_bf16 v[86:89], v[170:173], v[194:197], v[86:89]
	v_mfma_f32_16x16x32_bf16 v[70:73], v[162:165], v[202:205], v[70:73]
	v_mfma_f32_16x16x32_bf16 v[66:69], v[170:173], v[202:205], v[66:69]
	s_setprio 0
	s_barrier
	s_mov_b32 m0, s17
	ds_read_b128 v[174:177], v159 offset:16384
	ds_read_b128 v[178:181], v159 offset:17408
	ds_read_b128 v[182:185], v159 offset:18432
	ds_read_b128 v[186:189], v159 offset:19456
	ds_read_b128 v[190:193], v159 offset:20480
	ds_read_b128 v[194:197], v159 offset:21504
	ds_read_b128 v[198:201], v159 offset:22528
	ds_read_b128 v[202:205], v159 offset:23552
	buffer_load_dwordx4 v156, s[80:83], s53 offen lds
	s_mov_b32 m0, s18
	s_nop 0
	buffer_load_dwordx4 v156, s[80:83], s55 offen lds
	s_mov_b32 m0, s19
	s_nop 0
	buffer_load_dwordx4 v156, s[80:83], s54 offen lds
	s_mov_b32 m0, s20
	s_nop 0
	buffer_load_dwordx4 v156, s[80:83], s52 offen lds
	s_mov_b32 m0, s16
	s_nop 0
	buffer_load_dwordx4 v1, s[80:83], s50 offen lds
	s_mov_b32 m0, s21
	s_nop 0
	buffer_load_dwordx4 v1, s[80:83], s51 offen lds
	s_waitcnt vmcnt(8)
	s_waitcnt lgkmcnt(0)
	s_barrier
	s_setprio 1
	s_waitcnt lgkmcnt(7)
	v_mfma_f32_16x16x32_bf16 v[62:65], v[82:85], v[174:177], v[62:65]
	v_mfma_f32_16x16x32_bf16 v[58:61], v[98:101], v[174:177], v[58:61]
	s_waitcnt lgkmcnt(5)
	v_mfma_f32_16x16x32_bf16 v[46:49], v[82:85], v[182:185], v[46:49]
	v_mfma_f32_16x16x32_bf16 v[42:45], v[98:101], v[182:185], v[42:45]
	s_waitcnt lgkmcnt(3)
	v_mfma_f32_16x16x32_bf16 v[30:33], v[82:85], v[190:193], v[30:33]
	v_mfma_f32_16x16x32_bf16 v[26:29], v[98:101], v[190:193], v[26:29]
	s_waitcnt lgkmcnt(1)
	v_mfma_f32_16x16x32_bf16 v[14:17], v[82:85], v[198:201], v[14:17]
	v_mfma_f32_16x16x32_bf16 v[10:13], v[98:101], v[198:201], v[10:13]
	v_mfma_f32_16x16x32_bf16 v[62:65], v[90:93], v[178:181], v[62:65]
	v_mfma_f32_16x16x32_bf16 v[58:61], v[106:109], v[178:181], v[58:61]
	v_mfma_f32_16x16x32_bf16 v[46:49], v[90:93], v[186:189], v[46:49]
	v_mfma_f32_16x16x32_bf16 v[42:45], v[106:109], v[186:189], v[42:45]
	v_mfma_f32_16x16x32_bf16 v[30:33], v[90:93], v[194:197], v[30:33]
	v_mfma_f32_16x16x32_bf16 v[26:29], v[106:109], v[194:197], v[26:29]
	s_waitcnt lgkmcnt(0)
	v_mfma_f32_16x16x32_bf16 v[14:17], v[90:93], v[202:205], v[14:17]
	v_mfma_f32_16x16x32_bf16 v[10:13], v[106:109], v[202:205], v[10:13]
	s_setprio 0
	s_setprio 1
	v_mfma_f32_16x16x32_bf16 v[54:57], v[150:153], v[174:177], v[54:57]
	v_mfma_f32_16x16x32_bf16 v[50:53], v[166:169], v[174:177], v[50:53]
	v_mfma_f32_16x16x32_bf16 v[38:41], v[150:153], v[182:185], v[38:41]
	v_mfma_f32_16x16x32_bf16 v[34:37], v[166:169], v[182:185], v[34:37]
	v_mfma_f32_16x16x32_bf16 v[22:25], v[150:153], v[190:193], v[22:25]
	v_mfma_f32_16x16x32_bf16 v[18:21], v[166:169], v[190:193], v[18:21]
	v_mfma_f32_16x16x32_bf16 v[6:9], v[150:153], v[198:201], v[6:9]
	v_mfma_f32_16x16x32_bf16 v[2:5], v[166:169], v[198:201], v[2:5]
	v_mfma_f32_16x16x32_bf16 v[54:57], v[162:165], v[178:181], v[54:57]
	v_mfma_f32_16x16x32_bf16 v[50:53], v[170:173], v[178:181], v[50:53]
	v_mfma_f32_16x16x32_bf16 v[38:41], v[162:165], v[186:189], v[38:41]
	v_mfma_f32_16x16x32_bf16 v[34:37], v[170:173], v[186:189], v[34:37]
	v_mfma_f32_16x16x32_bf16 v[22:25], v[162:165], v[194:197], v[22:25]
	v_mfma_f32_16x16x32_bf16 v[18:21], v[170:173], v[194:197], v[18:21]
	v_mfma_f32_16x16x32_bf16 v[6:9], v[162:165], v[202:205], v[6:9]
	v_mfma_f32_16x16x32_bf16 v[2:5], v[170:173], v[202:205], v[2:5]
	s_setprio 0
	s_barrier
; #define PG8_STAGE(bufoff, goff, voff) do { _Pragma("unroll") for (int _i = 0; _i < 2; ++_i) \
;         __builtin_amdgcn_raw_ptr_buffer_load_lds(rsrc, (PG8_LAS void*)(lds + (bufoff) + ldsw + _i * 8192), 16, (int)(voff), (int)((goff) + _i * p1##voff), 0, 0); } while (0)
; #define PG8_LDA(dst, b, h) do { _Pragma("unroll") for (int m = 0; m < 4; ++m) dst[m] = PG8_LD8(lds + PG8_SA(b, h) + aoff + m * 2048); } while (0)
; #define PG8_LDB(dst, b, h) do { _Pragma("unroll") for (int n = 0; n < 2; ++n) dst[n] = PG8_LD8(lds + PG8_SB(b, h) + boff + n * 2048); } while (0)
; #define PG8_WAIT_V(n) asm volatile("s_waitcnt vmcnt(" #n ")" ::: "memory")
; #define PG8_WAIT_L(n) asm volatile("s_waitcnt lgkmcnt(" #n ")" ::: "memory")
; #define PG8_BAR __builtin_amdgcn_s_barrier()
; #define PG8_SCHED __builtin_amdgcn_sched_barrier(0)
; template <class Epi, class Sched, bool ALIGN_EPI, bool F8 = false, int F8SC = F8_SCALES>
; __device__ __forceinline__ void gemm_phase(PG8_LAS unsigned char* lds, const __amdgpu_buffer_rsrc_t rsrc, const int lda, const int ldb, const int K, const Sched& S, const Epi& E) {
;     ...
;             PG8_LDB(B0, 1, 0); PG8_LDB(B1, 1, 1); PG8_SCHED; PG8_LDA(At, 1, 0); PG8_STAGE(PG8_SA(0, 1), a2 + hsA, voffA);
;             PG8_WAIT_V(8); PG8_WAIT_L(0); PG8_BAR; PG8_MMA(0, 0, At, B0); PG8_MMA(0, 1, At, B1); PG8_BAR; PG8_SCHED;
;             PG8_LDA(At, 1, 1); PG8_STAGE(PG8_SB(1, 0), b3, voffB); PG8_STAGE(PG8_SB(1, 1), b3 + hsB, voffB); PG8_STAGE(PG8_SA(1, 0), a3, voffA);
;             PG8_WAIT_V(8); PG8_WAIT_L(0); PG8_BAR; PG8_MMA(1, 0, At, B0); PG8_MMA(1, 1, At, B1); PG8_BAR; PG8_SCHED;
;         }
	ds_read_b128 v[82:85], v160
	ds_read_b128 v[90:93], v160 offset:1024
	ds_read_b128 v[98:101], v160 offset:2048
	ds_read_b128 v[106:109], v160 offset:3072
	ds_read_b128 v[150:153], v161
	ds_read_b128 v[162:165], v161 offset:1024
	ds_read_b128 v[166:169], v161 offset:2048
	ds_read_b128 v[170:173], v161 offset:3072
	s_mov_b32 m0, s22
	ds_read_b128 v[174:177], v159 offset:32768
	ds_read_b128 v[178:181], v159 offset:33792
	ds_read_b128 v[182:185], v159 offset:34816
	ds_read_b128 v[186:189], v159 offset:35840
	ds_read_b128 v[190:193], v159 offset:36864
	ds_read_b128 v[194:197], v159 offset:37888
	ds_read_b128 v[198:201], v159 offset:38912
	ds_read_b128 v[202:205], v159 offset:39936
	buffer_load_dwordx4 v1, s[80:83], s49 offen lds
	s_mov_b32 m0, s23
	s_nop 0
	buffer_load_dwordx4 v1, s[80:83], s48 offen lds
	s_waitcnt vmcnt(8)
	s_waitcnt lgkmcnt(0)
	s_barrier
	s_setprio 1
	s_waitcnt lgkmcnt(7)
	v_mfma_f32_16x16x32_bf16 v[142:145], v[82:85], v[174:177], v[142:145]
	v_mfma_f32_16x16x32_bf16 v[138:141], v[98:101], v[174:177], v[138:141]
	s_waitcnt lgkmcnt(5)
	v_mfma_f32_16x16x32_bf16 v[126:129], v[82:85], v[182:185], v[126:129]
	v_mfma_f32_16x16x32_bf16 v[122:125], v[98:101], v[182:185], v[122:125]
	s_waitcnt lgkmcnt(3)
	v_mfma_f32_16x16x32_bf16 v[110:113], v[82:85], v[190:193], v[110:113]
	v_mfma_f32_16x16x32_bf16 v[102:105], v[98:101], v[190:193], v[102:105]
	s_waitcnt lgkmcnt(1)
	v_mfma_f32_16x16x32_bf16 v[78:81], v[82:85], v[198:201], v[78:81]
	v_mfma_f32_16x16x32_bf16 v[74:77], v[98:101], v[198:201], v[74:77]
	v_mfma_f32_16x16x32_bf16 v[142:145], v[90:93], v[178:181], v[142:145]
	v_mfma_f32_16x16x32_bf16 v[138:141], v[106:109], v[178:181], v[138:141]
	v_mfma_f32_16x16x32_bf16 v[126:129], v[90:93], v[186:189], v[126:129]
	v_mfma_f32_16x16x32_bf16 v[122:125], v[106:109], v[186:189], v[122:125]
	v_mfma_f32_16x16x32_bf16 v[110:113], v[90:93], v[194:197], v[110:113]
	v_mfma_f32_16x16x32_bf16 v[102:105], v[106:109], v[194:197], v[102:105]
	s_waitcnt lgkmcnt(0)
	v_mfma_f32_16x16x32_bf16 v[78:81], v[90:93], v[202:205], v[78:81]
	v_mfma_f32_16x16x32_bf16 v[74:77], v[106:109], v[202:205], v[74:77]
	s_setprio 0
	s_setprio 1
	v_mfma_f32_16x16x32_bf16 v[134:137], v[150:153], v[174:177], v[134:137]
	v_mfma_f32_16x16x32_bf16 v[130:133], v[166:169], v[174:177], v[130:133]
	v_mfma_f32_16x16x32_bf16 v[118:121], v[150:153], v[182:185], v[118:121]
	v_mfma_f32_16x16x32_bf16 v[114:117], v[166:169], v[182:185], v[114:117]
	v_mfma_f32_16x16x32_bf16 v[94:97], v[150:153], v[190:193], v[94:97]
	v_mfma_f32_16x16x32_bf16 v[86:89], v[166:169], v[190:193], v[86:89]
	v_mfma_f32_16x16x32_bf16 v[70:73], v[150:153], v[198:201], v[70:73]
	v_mfma_f32_16x16x32_bf16 v[66:69], v[166:169], v[198:201], v[66:69]
	v_mfma_f32_16x16x32_bf16 v[134:137], v[162:165], v[178:181], v[134:137]
	v_mfma_f32_16x16x32_bf16 v[130:133], v[170:173], v[178:181], v[130:133]
	v_mfma_f32_16x16x32_bf16 v[118:121], v[162:165], v[186:189], v[118:121]
	v_mfma_f32_16x16x32_bf16 v[114:117], v[170:173], v[186:189], v[114:117]
	v_mfma_f32_16x16x32_bf16 v[94:97], v[162:165], v[194:197], v[94:97]
	v_mfma_f32_16x16x32_bf16 v[86:89], v[170:173], v[194:197], v[86:89]
	v_mfma_f32_16x16x32_bf16 v[70:73], v[162:165], v[202:205], v[70:73]
	v_mfma_f32_16x16x32_bf16 v[66:69], v[170:173], v[202:205], v[66:69]
	s_setprio 0
	s_barrier
	s_mov_b32 m0, s25
	ds_read_b128 v[174:177], v159 offset:49152
	ds_read_b128 v[178:181], v159 offset:50176
	ds_read_b128 v[182:185], v159 offset:51200
	ds_read_b128 v[186:189], v159 offset:52224
	ds_read_b128 v[190:193], v159 offset:53248
	ds_read_b128 v[194:197], v159 offset:54272
	ds_read_b128 v[198:201], v159 offset:55296
	ds_read_b128 v[202:205], v159 offset:56320
	buffer_load_dwordx4 v156, s[80:83], s47 offen lds
	s_mov_b32 m0, s26
	s_nop 0
	buffer_load_dwordx4 v156, s[80:83], s46 offen lds
	s_mov_b32 m0, s29
	s_nop 0
	buffer_load_dwordx4 v156, s[80:83], s44 offen lds
	s_mov_b32 m0, s30
	s_nop 0
	buffer_load_dwordx4 v156, s[80:83], s15 offen lds
	s_mov_b32 m0, s27
	s_nop 0
	buffer_load_dwordx4 v1, s[80:83], s45 offen lds
	s_mov_b32 m0, s28
	s_nop 0
	buffer_load_dwordx4 v1, s[80:83], s14 offen lds
	s_waitcnt vmcnt(8)
	s_waitcnt lgkmcnt(0)
	s_barrier
	s_setprio 1
	s_waitcnt lgkmcnt(7)
	v_mfma_f32_16x16x32_bf16 v[62:65], v[82:85], v[174:177], v[62:65]
	v_mfma_f32_16x16x32_bf16 v[58:61], v[98:101], v[174:177], v[58:61]
	s_waitcnt lgkmcnt(5)
	v_mfma_f32_16x16x32_bf16 v[46:49], v[82:85], v[182:185], v[46:49]
	v_mfma_f32_16x16x32_bf16 v[42:45], v[98:101], v[182:185], v[42:45]
	s_waitcnt lgkmcnt(3)
	v_mfma_f32_16x16x32_bf16 v[30:33], v[82:85], v[190:193], v[30:33]
	v_mfma_f32_16x16x32_bf16 v[26:29], v[98:101], v[190:193], v[26:29]
	s_waitcnt lgkmcnt(1)
	v_mfma_f32_16x16x32_bf16 v[14:17], v[82:85], v[198:201], v[14:17]
	v_mfma_f32_16x16x32_bf16 v[10:13], v[98:101], v[198:201], v[10:13]
	v_mfma_f32_16x16x32_bf16 v[62:65], v[90:93], v[178:181], v[62:65]
	v_mfma_f32_16x16x32_bf16 v[58:61], v[106:109], v[178:181], v[58:61]
	v_mfma_f32_16x16x32_bf16 v[46:49], v[90:93], v[186:189], v[46:49]
	v_mfma_f32_16x16x32_bf16 v[42:45], v[106:109], v[186:189], v[42:45]
	v_mfma_f32_16x16x32_bf16 v[30:33], v[90:93], v[194:197], v[30:33]
	v_mfma_f32_16x16x32_bf16 v[26:29], v[106:109], v[194:197], v[26:29]
	s_waitcnt lgkmcnt(0)
	v_mfma_f32_16x16x32_bf16 v[14:17], v[90:93], v[202:205], v[14:17]
	v_mfma_f32_16x16x32_bf16 v[10:13], v[106:109], v[202:205], v[10:13]
	s_setprio 0
	s_setprio 1
	v_mfma_f32_16x16x32_bf16 v[54:57], v[150:153], v[174:177], v[54:57]
	v_mfma_f32_16x16x32_bf16 v[50:53], v[166:169], v[174:177], v[50:53]
	v_mfma_f32_16x16x32_bf16 v[38:41], v[150:153], v[182:185], v[38:41]
	v_mfma_f32_16x16x32_bf16 v[34:37], v[166:169], v[182:185], v[34:37]
	v_mfma_f32_16x16x32_bf16 v[22:25], v[150:153], v[190:193], v[22:25]
	v_mfma_f32_16x16x32_bf16 v[18:21], v[166:169], v[190:193], v[18:21]
	v_mfma_f32_16x16x32_bf16 v[6:9], v[150:153], v[198:201], v[6:9]
	v_mfma_f32_16x16x32_bf16 v[2:5], v[166:169], v[198:201], v[2:5]
	v_mfma_f32_16x16x32_bf16 v[54:57], v[162:165], v[178:181], v[54:57]
	v_mfma_f32_16x16x32_bf16 v[50:53], v[170:173], v[178:181], v[50:53]
	v_mfma_f32_16x16x32_bf16 v[38:41], v[162:165], v[186:189], v[38:41]
	v_mfma_f32_16x16x32_bf16 v[34:37], v[170:173], v[186:189], v[34:37]
	v_mfma_f32_16x16x32_bf16 v[22:25], v[162:165], v[194:197], v[22:25]
	v_mfma_f32_16x16x32_bf16 v[18:21], v[170:173], v[194:197], v[18:21]
	v_mfma_f32_16x16x32_bf16 v[6:9], v[162:165], v[202:205], v[6:9]
	v_mfma_f32_16x16x32_bf16 v[2:5], v[170:173], v[202:205], v[2:5]
	s_setprio 0
	s_barrier
	s_andn2_b64 vcc, exec, s[6:7]
	s_mov_b64 s[14:15], -1
	s_mov_b64 s[6:7], 0
	s_movk_i32 s44, 0x100
	s_cbranch_vccz .LBB0_969
; __device__ __forceinline__ float fsigmoid(float x) { return __builtin_amdgcn_rcpf(1.0f + __expf(-x)); }
; #define PG8_BAR __builtin_amdgcn_s_barrier()
; #define EPI_ROWLOOP _Pragma("unroll") for (int ai = 0; ai < 2; ++ai) _Pragma("unroll") for (int m = 0; m < 4; ++m)
; template <class Epi, class Sched, bool ALIGN_EPI, bool F8 = false, int F8SC = F8_SCALES>
; __device__ __forceinline__ void gemm_phase(PG8_LAS unsigned char* lds, const __amdgpu_buffer_rsrc_t rsrc, const int lda, const int ldb, const int K, const Sched& S, const Epi& E) {
;     ...
;         if constexpr (ALIGN_EPI) { if (wr == 0) PG8_BAR; }
;     __device__ __forceinline__ bool operator()(f32x4 (&acc)[2][2][4][2], const Unit& u, int wr, int wc, int fr, int fq) const {
;         const int row0 = u.pm * BM + wr * 64 + fr, col0 = u.pn * BM + wc * 32 + 8 * fq;
;         f32x4 pv[2][2];
; #pragma unroll
;         for (int bj = 0; bj < 2; ++bj)
; #pragma unroll
;             for (int n = 0; n < 2; ++n) pv[bj][n] = *(const f32x4*)(par + col0 + bj * HALF + 4 * n);
;         EPI_ROWLOOP { float* rowp = OUT + (size_t)(row0 + ai * HALF + m * 16) * RW + col0;
; #pragma unroll
;             for (int bj = 0; bj < 2; ++bj)
; #pragma unroll
;                 for (int n = 0; n < 2; ++n) { f32x4 v = acc[ai][bj][m][n] + pv[bj][n];
; #pragma unroll
;                     for (int j = 0; j < 4; ++j) {
;                         if (ISDEC) v[j] = -0.60653065971263342f * fsigmoid(v[j]);
;                         else v[j] = fsigmoid(v[j]); }
;                     *(f32x4*)(rowp + bj * HALF + 4 * n) = v; } }
.Lpeel_after_969:
	s_and_b64 vcc, exec, s[10:11]
	s_cbranch_vccz .LBB0_972
	s_barrier
.LBB0_972:
	v_mov_b32_e32 v150, v0
	s_lshl_b32 s7, s40, 8
	v_readfirstlane_b32 s6, v150
	s_lshr_b32 s14, s6, 1
	s_and_b32 s14, s14, 0x60
	s_or_b32 s7, s14, s7
	v_lshrrev_b32_e32 v82, 1, v150
	v_and_or_b32 v82, v82, 24, s7
	v_ashrrev_i32_e32 v83, 31, v82
	v_readlane_b32 s40, v254, 5
	v_lshlrev_b64 v[152:153], 2, v[82:83]
	v_readlane_b32 s48, v254, 13
	v_readlane_b32 s49, v254, 14
	s_ashr_i32 s6, s6, 2
	s_lshl_b32 s7, s39, 8
	v_lshl_add_u64 v[82:83], s[48:49], 0, v[152:153]
	global_load_dwordx4 v[106:109], v[82:83], off
	global_load_dwordx4 v[98:101], v[82:83], off offset:16
	global_load_dwordx4 v[90:93], v[82:83], off offset:512
	s_nop 0
	global_load_dwordx4 v[82:85], v[82:83], off offset:528
	s_andn2_b32 s6, s6, 63
	s_add_i32 s6, s6, s7
	v_and_or_b32 v154, v150, 15, s6
	v_ashrrev_i32_e32 v155, 31, v154
	v_lshlrev_b64 v[150:151], 12, v[154:155]
	v_lshl_add_u64 v[150:151], s[0:1], 0, v[150:151]
	v_lshl_add_u64 v[150:151], v[150:151], 0, v[152:153]
	s_mov_b64 s[6:7], 0x80000
	v_readlane_b32 s41, v254, 6
	v_readlane_b32 s42, v254, 7
	v_readlane_b32 s43, v254, 8
	v_readlane_b32 s44, v254, 9
	v_readlane_b32 s45, v254, 10
	v_readlane_b32 s46, v254, 11
	v_readlane_b32 s47, v254, 12
	v_readlane_b32 s50, v254, 15
	v_readlane_b32 s51, v254, 16
	v_readlane_b32 s52, v254, 17
	v_readlane_b32 s53, v254, 18
	v_readlane_b32 s54, v254, 19
	v_readlane_b32 s55, v254, 20
	s_waitcnt vmcnt(3)
	v_pk_add_f32 v[144:145], v[144:145], v[108:109]
	v_pk_add_f32 v[142:143], v[142:143], v[106:107]
	s_waitcnt vmcnt(2)
	v_pk_add_f32 v[140:141], v[140:141], v[100:101]
	v_pk_add_f32 v[138:139], v[138:139], v[98:99]
	s_waitcnt vmcnt(0)
	v_pk_add_f32 v[132:133], v[132:133], v[84:85]
	v_pk_add_f32 v[130:131], v[130:131], v[82:83]
	v_mul_f32_e32 v142, 0xbfb8aa3b, v142
	v_mul_f32_e32 v143, 0xbfb8aa3b, v143
	v_mul_f32_e32 v144, 0xbfb8aa3b, v144
	v_mul_f32_e32 v145, 0xbfb8aa3b, v145
	v_pk_add_f32 v[136:137], v[136:137], v[92:93]
	v_pk_add_f32 v[134:135], v[134:135], v[90:91]
	v_mul_f32_e32 v138, 0xbfb8aa3b, v138
	v_mul_f32_e32 v139, 0xbfb8aa3b, v139
	v_mul_f32_e32 v140, 0xbfb8aa3b, v140
	v_mul_f32_e32 v141, 0xbfb8aa3b, v141
	v_mul_f32_e32 v130, 0xbfb8aa3b, v130
	v_mul_f32_e32 v131, 0xbfb8aa3b, v131
	v_mul_f32_e32 v132, 0xbfb8aa3b, v132
	v_mul_f32_e32 v133, 0xbfb8aa3b, v133
	v_exp_f32_e32 v142, v142
	v_exp_f32_e32 v143, v143
	v_exp_f32_e32 v144, v144
	v_exp_f32_e32 v145, v145
	v_mul_f32_e32 v134, 0xbfb8aa3b, v134
	v_mul_f32_e32 v135, 0xbfb8aa3b, v135
	v_mul_f32_e32 v136, 0xbfb8aa3b, v136
	v_mul_f32_e32 v137, 0xbfb8aa3b, v137
	v_exp_f32_e32 v138, v138
	v_exp_f32_e32 v139, v139
	v_exp_f32_e32 v140, v140
	v_exp_f32_e32 v141, v141
	v_exp_f32_e32 v130, v130
	v_exp_f32_e32 v131, v131
	v_exp_f32_e32 v132, v132
	v_exp_f32_e32 v133, v133
	v_exp_f32_e32 v134, v134
	v_exp_f32_e32 v135, v135
	v_exp_f32_e32 v136, v136
	v_exp_f32_e32 v137, v137
	v_add_f32_e32 v142, 1.0, v142
	v_add_f32_e32 v143, 1.0, v143
	v_add_f32_e32 v144, 1.0, v144
	v_add_f32_e32 v145, 1.0, v145
	v_add_f32_e32 v138, 1.0, v138
	v_add_f32_e32 v139, 1.0, v139
	v_add_f32_e32 v140, 1.0, v140
	v_add_f32_e32 v141, 1.0, v141
	v_add_f32_e32 v165, 1.0, v130
	v_add_f32_e32 v166, 1.0, v131
	v_add_f32_e32 v167, 1.0, v132
	v_add_f32_e32 v168, 1.0, v133
	v_rcp_f32_e32 v130, v142
	v_rcp_f32_e32 v131, v143
	v_rcp_f32_e32 v132, v144
	v_rcp_f32_e32 v133, v145
	v_pk_add_f32 v[126:127], v[126:127], v[106:107]
	v_add_f32_e32 v155, 1.0, v134
	v_add_f32_e32 v162, 1.0, v135
	v_add_f32_e32 v163, 1.0, v136
	v_add_f32_e32 v164, 1.0, v137
	v_rcp_f32_e32 v134, v138
	v_rcp_f32_e32 v135, v139
	v_rcp_f32_e32 v136, v140
	v_rcp_f32_e32 v137, v141
	v_rcp_f32_e32 v142, v165
	v_rcp_f32_e32 v144, v167
	v_rcp_f32_e32 v145, v168
	v_rcp_f32_e32 v143, v166
	v_mul_f32_e32 v126, 0xbfb8aa3b, v126
	v_exp_f32_e32 v126, v126
	v_pk_mul_f32 v[132:133], v[132:133], s[12:13] op_sel_hi:[1,0]
	v_pk_mul_f32 v[130:131], v[130:131], s[12:13] op_sel_hi:[1,0]
	v_pk_mul_f32 v[136:137], v[136:137], s[12:13] op_sel_hi:[1,0]
	v_pk_mul_f32 v[134:135], v[134:135], s[12:13] op_sel_hi:[1,0]
	global_store_dwordx4 v[150:151], v[130:133], off
	global_store_dwordx4 v[150:151], v[134:137], off offset:16
	v_pk_add_f32 v[128:129], v[128:129], v[108:109]
	v_pk_mul_f32 v[132:133], v[144:145], s[12:13] op_sel_hi:[1,0]
	v_pk_mul_f32 v[130:131], v[142:143], s[12:13] op_sel_hi:[1,0]
	global_store_dwordx4 v[150:151], v[130:133], off offset:528
	v_pk_add_f32 v[122:123], v[122:123], v[98:99]
	v_pk_add_f32 v[124:125], v[124:125], v[100:101]
	v_add_f32_e32 v132, 1.0, v126
	v_mul_f32_e32 v126, 0xbfb8aa3b, v127
	v_mul_f32_e32 v127, 0xbfb8aa3b, v128
	v_mul_f32_e32 v128, 0xbfb8aa3b, v129
	v_exp_f32_e32 v127, v127
	v_exp_f32_e32 v128, v128
	v_exp_f32_e32 v129, v126
	v_or_b32_e32 v130, 16, v154
	v_add_f32_e32 v126, 1.0, v127
	v_add_f32_e32 v127, 1.0, v128
	v_add_f32_e32 v128, 1.0, v129
	v_rcp_f32_e32 v126, v126
	v_rcp_f32_e32 v127, v127
	v_rcp_f32_e32 v132, v132
	v_rcp_f32_e32 v133, v128
	v_mul_f32_e32 v122, 0xbfb8aa3b, v122
	v_ashrrev_i32_e32 v131, 31, v130
	v_exp_f32_e32 v122, v122
	v_lshlrev_b64 v[130:131], 12, v[130:131]
	v_lshl_add_u64 v[130:131], s[0:1], 0, v[130:131]
	v_lshl_add_u64 v[130:131], v[130:131], 0, v[152:153]
	v_pk_mul_f32 v[128:129], v[126:127], s[12:13] op_sel_hi:[1,0]
	v_pk_mul_f32 v[126:127], v[132:133], s[12:13] op_sel_hi:[1,0]
	global_store_dwordx4 v[130:131], v[126:129], off
	v_pk_add_f32 v[118:119], v[118:119], v[90:91]
	v_pk_add_f32 v[120:121], v[120:121], v[92:93]
	v_add_f32_e32 v126, 1.0, v122
	v_mul_f32_e32 v122, 0xbfb8aa3b, v123
	v_mul_f32_e32 v123, 0xbfb8aa3b, v124
	v_mul_f32_e32 v124, 0xbfb8aa3b, v125
; __device__ __forceinline__ float fsigmoid(float x) { return __builtin_amdgcn_rcpf(1.0f + __expf(-x)); }
; #define EPI_ROWLOOP _Pragma("unroll") for (int ai = 0; ai < 2; ++ai) _Pragma("unroll") for (int m = 0; m < 4; ++m)
;     __device__ __forceinline__ bool operator()(f32x4 (&acc)[2][2][4][2], const Unit& u, int wr, int wc, int fr, int fq) const {
;     ...
;         EPI_ROWLOOP { float* rowp = OUT + (size_t)(row0 + ai * HALF + m * 16) * RW + col0;
; #pragma unroll
;             for (int bj = 0; bj < 2; ++bj)
; #pragma unroll
;                 for (int n = 0; n < 2; ++n) { f32x4 v = acc[ai][bj][m][n] + pv[bj][n];
; #pragma unroll
;                     for (int j = 0; j < 4; ++j) {
;                         if (ISDEC) v[j] = -0.60653065971263342f * fsigmoid(v[j]);
;                         else v[j] = fsigmoid(v[j]); }
;                     *(f32x4*)(rowp + bj * HALF + 4 * n) = v; } }
	v_exp_f32_e32 v123, v123
	v_exp_f32_e32 v124, v124
	v_exp_f32_e32 v125, v122
	v_mul_f32_e32 v118, 0xbfb8aa3b, v118
	v_add_f32_e32 v122, 1.0, v123
	v_add_f32_e32 v123, 1.0, v124
	v_add_f32_e32 v124, 1.0, v125
	v_rcp_f32_e32 v122, v122
	v_rcp_f32_e32 v123, v123
	v_rcp_f32_e32 v126, v126
	v_rcp_f32_e32 v127, v124
	v_exp_f32_e32 v118, v118
	v_pk_mul_f32 v[124:125], v[122:123], s[12:13] op_sel_hi:[1,0]
	v_pk_add_f32 v[116:117], v[116:117], v[84:85]
	v_pk_mul_f32 v[122:123], v[126:127], s[12:13] op_sel_hi:[1,0]
	v_add_f32_e32 v118, 1.0, v118
	global_store_dwordx4 v[130:131], v[122:125], off offset:16
	v_pk_add_f32 v[114:115], v[114:115], v[82:83]
	v_mul_f32_e32 v116, 0xbfb8aa3b, v116
	v_rcp_f32_e32 v122, v118
	v_mul_f32_e32 v118, 0xbfb8aa3b, v119
	v_mul_f32_e32 v119, 0xbfb8aa3b, v120
	v_mul_f32_e32 v120, 0xbfb8aa3b, v121
	v_exp_f32_e32 v118, v118
	v_exp_f32_e32 v119, v119
	v_exp_f32_e32 v120, v120
	v_mul_f32_e32 v114, 0xbfb8aa3b, v114
	v_mul_f32_e32 v115, 0xbfb8aa3b, v115
	v_exp_f32_e32 v116, v116
	v_mul_f32_e32 v117, 0xbfb8aa3b, v117
	v_exp_f32_e32 v114, v114
	v_exp_f32_e32 v115, v115
	v_exp_f32_e32 v117, v117
	v_add_f32_e32 v121, 1.0, v118
	v_add_f32_e32 v118, 1.0, v119
	v_add_f32_e32 v119, 1.0, v120
	v_add_f32_e32 v116, 1.0, v116
	v_pk_add_f32 v[86:87], v[86:87], v[82:83]
	v_pk_add_f32 v[88:89], v[88:89], v[84:85]
	v_rcp_f32_e32 v118, v118
	v_rcp_f32_e32 v119, v119
	v_rcp_f32_e32 v123, v121
	v_add_f32_e32 v114, 1.0, v114
	v_add_f32_e32 v115, 1.0, v115
	v_rcp_f32_e32 v120, v116
	v_add_f32_e32 v116, 1.0, v117
	v_mul_f32_e32 v86, 0xbfb8aa3b, v86
	v_mul_f32_e32 v87, 0xbfb8aa3b, v87
	v_mul_f32_e32 v88, 0xbfb8aa3b, v88
	v_mul_f32_e32 v89, 0xbfb8aa3b, v89
	v_rcp_f32_e32 v114, v114
	v_rcp_f32_e32 v121, v116
	v_rcp_f32_e32 v115, v115
	v_exp_f32_e32 v86, v86
	v_exp_f32_e32 v87, v87
	v_exp_f32_e32 v88, v88
	v_exp_f32_e32 v89, v89
	v_pk_mul_f32 v[118:119], v[118:119], s[12:13] op_sel_hi:[1,0]
	v_pk_mul_f32 v[116:117], v[122:123], s[12:13] op_sel_hi:[1,0]
	global_store_dwordx4 v[130:131], v[116:119], off offset:512
	v_pk_mul_f32 v[114:115], v[114:115], s[12:13] op_sel_hi:[1,0]
	v_add_f32_e32 v86, 1.0, v86
	v_pk_mul_f32 v[116:117], v[120:121], s[12:13] op_sel_hi:[1,0]
	v_add_f32_e32 v87, 1.0, v87
	v_add_f32_e32 v88, 1.0, v88
	v_add_f32_e32 v89, 1.0, v89
	v_pk_add_f32 v[78:79], v[78:79], v[106:107]
	global_store_dwordx4 v[130:131], v[114:117], off offset:528
	v_rcp_f32_e32 v86, v86
	v_rcp_f32_e32 v88, v88
	v_or_b32_e32 v114, 32, v154
	v_rcp_f32_e32 v89, v89
	v_rcp_f32_e32 v87, v87
	v_mul_f32_e32 v78, 0xbfb8aa3b, v78
	v_ashrrev_i32_e32 v115, 31, v114
	v_exp_f32_e32 v78, v78
	v_lshlrev_b64 v[114:115], 12, v[114:115]
	v_lshl_add_u64 v[114:115], s[0:1], 0, v[114:115]
	v_lshl_add_u64 v[114:115], v[114:115], 0, v[152:153]
	v_pk_mul_f32 v[88:89], v[88:89], s[12:13] op_sel_hi:[1,0]
	v_pk_mul_f32 v[86:87], v[86:87], s[12:13] op_sel_hi:[1,0]
	v_pk_add_f32 v[80:81], v[80:81], v[108:109]
	global_store_dwordx4 v[114:115], v[86:89], off offset:528
	v_pk_add_f32 v[74:75], v[74:75], v[98:99]
	v_pk_add_f32 v[76:77], v[76:77], v[100:101]
	v_add_f32_e32 v88, 1.0, v78
	v_mul_f32_e32 v78, 0xbfb8aa3b, v79
	v_mul_f32_e32 v79, 0xbfb8aa3b, v80
	v_mul_f32_e32 v80, 0xbfb8aa3b, v81
	v_exp_f32_e32 v79, v79
	v_exp_f32_e32 v80, v80
	v_exp_f32_e32 v81, v78
	v_mul_f32_e32 v74, 0xbfb8aa3b, v74
	v_add_f32_e32 v78, 1.0, v79
	v_add_f32_e32 v79, 1.0, v80
	v_add_f32_e32 v80, 1.0, v81
	v_or_b32_e32 v86, 48, v154
	v_rcp_f32_e32 v78, v78
	v_rcp_f32_e32 v79, v79
	v_rcp_f32_e32 v88, v88
	v_rcp_f32_e32 v89, v80
	v_exp_f32_e32 v74, v74
	v_ashrrev_i32_e32 v87, 31, v86
	v_lshlrev_b64 v[86:87], 12, v[86:87]
	v_lshl_add_u64 v[86:87], s[0:1], 0, v[86:87]
	v_lshl_add_u64 v[86:87], v[86:87], 0, v[152:153]
	v_pk_mul_f32 v[80:81], v[78:79], s[12:13] op_sel_hi:[1,0]
	v_pk_mul_f32 v[78:79], v[88:89], s[12:13] op_sel_hi:[1,0]
	v_add_f32_e32 v74, 1.0, v74
	v_pk_add_f32 v[72:73], v[72:73], v[92:93]
	global_store_dwordx4 v[86:87], v[78:81], off
	v_pk_add_f32 v[70:71], v[70:71], v[90:91]
	v_mul_f32_e32 v72, 0xbfb8aa3b, v72
	v_rcp_f32_e32 v78, v74
	v_mul_f32_e32 v74, 0xbfb8aa3b, v75
	v_mul_f32_e32 v75, 0xbfb8aa3b, v76
	v_mul_f32_e32 v76, 0xbfb8aa3b, v77
	v_exp_f32_e32 v74, v74
	v_exp_f32_e32 v75, v75
	v_exp_f32_e32 v76, v76
	v_mul_f32_e32 v70, 0xbfb8aa3b, v70
	v_mul_f32_e32 v71, 0xbfb8aa3b, v71
	v_exp_f32_e32 v72, v72
	v_mul_f32_e32 v73, 0xbfb8aa3b, v73
	v_exp_f32_e32 v70, v70
	v_exp_f32_e32 v71, v71
	v_exp_f32_e32 v73, v73
	v_add_f32_e32 v77, 1.0, v74
	v_add_f32_e32 v74, 1.0, v75
	v_add_f32_e32 v75, 1.0, v76
	v_add_f32_e32 v72, 1.0, v72
	v_rcp_f32_e32 v74, v74
	v_rcp_f32_e32 v75, v75
	v_rcp_f32_e32 v79, v77
	v_add_f32_e32 v70, 1.0, v70
	v_add_f32_e32 v71, 1.0, v71
	v_rcp_f32_e32 v76, v72
	v_add_f32_e32 v72, 1.0, v73
	v_rcp_f32_e32 v70, v70
	v_rcp_f32_e32 v77, v72
	v_rcp_f32_e32 v71, v71
	v_pk_mul_f32 v[74:75], v[74:75], s[12:13] op_sel_hi:[1,0]
	v_pk_mul_f32 v[72:73], v[78:79], s[12:13] op_sel_hi:[1,0]
	v_pk_add_f32 v[66:67], v[66:67], v[82:83]
	global_store_dwordx4 v[86:87], v[72:75], off offset:16
	v_pk_mul_f32 v[70:71], v[70:71], s[12:13] op_sel_hi:[1,0]
	v_mul_f32_e32 v66, 0xbfb8aa3b, v66
	v_pk_mul_f32 v[72:73], v[76:77], s[12:13] op_sel_hi:[1,0]
	global_store_dwordx4 v[86:87], v[70:73], off offset:512
	v_pk_add_f32 v[62:63], v[62:63], v[106:107]
	v_pk_add_f32 v[64:65], v[64:65], v[108:109]
	v_exp_f32_e32 v70, v66
	v_mul_f32_e32 v66, 0xbfb8aa3b, v67
	v_exp_f32_e32 v71, v66
	v_pk_add_f32 v[66:67], v[68:69], v[84:85]
	v_mul_f32_e32 v62, 0xbfb8aa3b, v62
	v_mul_f32_e32 v66, 0xbfb8aa3b, v66
	v_mul_f32_e32 v67, 0xbfb8aa3b, v67
	v_exp_f32_e32 v66, v66
	v_exp_f32_e32 v67, v67
	v_mul_f32_e32 v63, 0xbfb8aa3b, v63
; __device__ __forceinline__ float fsigmoid(float x) { return __builtin_amdgcn_rcpf(1.0f + __expf(-x)); }
; #define EPI_ROWLOOP _Pragma("unroll") for (int ai = 0; ai < 2; ++ai) _Pragma("unroll") for (int m = 0; m < 4; ++m)
;     __device__ __forceinline__ bool operator()(f32x4 (&acc)[2][2][4][2], const Unit& u, int wr, int wc, int fr, int fq) const {
;     ...
;         EPI_ROWLOOP { float* rowp = OUT + (size_t)(row0 + ai * HALF + m * 16) * RW + col0;
; #pragma unroll
;             for (int bj = 0; bj < 2; ++bj)
; #pragma unroll
;                 for (int n = 0; n < 2; ++n) { f32x4 v = acc[ai][bj][m][n] + pv[bj][n];
; #pragma unroll
;                     for (int j = 0; j < 4; ++j) {
;                         if (ISDEC) v[j] = -0.60653065971263342f * fsigmoid(v[j]);
;                         else v[j] = fsigmoid(v[j]); }
;                     *(f32x4*)(rowp + bj * HALF + 4 * n) = v; } }
	v_mul_f32_e32 v64, 0xbfb8aa3b, v64
	v_mul_f32_e32 v65, 0xbfb8aa3b, v65
	v_add_f32_e32 v68, 1.0, v70
	v_exp_f32_e32 v62, v62
	v_exp_f32_e32 v63, v63
	v_exp_f32_e32 v64, v64
	v_exp_f32_e32 v65, v65
	v_rcp_f32_e32 v70, v68
	v_add_f32_e32 v68, 1.0, v71
	v_add_f32_e32 v66, 1.0, v66
	v_add_f32_e32 v67, 1.0, v67
	v_rcp_f32_e32 v71, v68
	v_rcp_f32_e32 v66, v66
	v_rcp_f32_e32 v67, v67
	v_pk_add_f32 v[58:59], v[58:59], v[98:99]
	v_add_f32_e32 v62, 1.0, v62
	v_add_f32_e32 v63, 1.0, v63
	v_add_f32_e32 v64, 1.0, v64
	v_add_f32_e32 v65, 1.0, v65
	v_mul_f32_e32 v58, 0xbfb8aa3b, v58
	v_rcp_f32_e32 v62, v62
	v_rcp_f32_e32 v64, v64
	v_rcp_f32_e32 v65, v65
	v_rcp_f32_e32 v63, v63
	v_exp_f32_e32 v58, v58
	v_pk_mul_f32 v[68:69], v[66:67], s[12:13] op_sel_hi:[1,0]
	v_pk_mul_f32 v[66:67], v[70:71], s[12:13] op_sel_hi:[1,0]
	global_store_dwordx4 v[86:87], v[66:69], off offset:528
	v_pk_mul_f32 v[64:65], v[64:65], s[12:13] op_sel_hi:[1,0]
	v_pk_mul_f32 v[62:63], v[62:63], s[12:13] op_sel_hi:[1,0]
	v_lshl_add_u64 v[66:67], v[150:151], 0, s[6:7]
	s_mov_b32 s6, 0x80000
	v_add_co_u32_e32 v68, vcc, s6, v150
	v_pk_add_f32 v[60:61], v[60:61], v[100:101]
	s_nop 0
	v_addc_co_u32_e32 v69, vcc, 0, v151, vcc
	v_add_f32_e32 v58, 1.0, v58
	v_pk_add_f32 v[56:57], v[56:57], v[92:93]
	global_store_dwordx4 v[68:69], v[62:65], off
	v_pk_add_f32 v[54:55], v[54:55], v[90:91]
	v_mul_f32_e32 v56, 0xbfb8aa3b, v56
	v_rcp_f32_e32 v62, v58
	v_mul_f32_e32 v58, 0xbfb8aa3b, v59
	v_mul_f32_e32 v59, 0xbfb8aa3b, v60
	v_mul_f32_e32 v60, 0xbfb8aa3b, v61
	v_exp_f32_e32 v58, v58
	v_exp_f32_e32 v59, v59
	v_exp_f32_e32 v60, v60
	v_mul_f32_e32 v54, 0xbfb8aa3b, v54
	v_mul_f32_e32 v55, 0xbfb8aa3b, v55
	v_exp_f32_e32 v56, v56
	v_mul_f32_e32 v57, 0xbfb8aa3b, v57
	v_exp_f32_e32 v54, v54
	v_exp_f32_e32 v55, v55
	v_exp_f32_e32 v57, v57
	v_add_f32_e32 v61, 1.0, v58
	v_add_f32_e32 v58, 1.0, v59
	v_add_f32_e32 v59, 1.0, v60
	v_add_f32_e32 v56, 1.0, v56
	v_rcp_f32_e32 v58, v58
	v_rcp_f32_e32 v59, v59
	v_rcp_f32_e32 v63, v61
	v_add_f32_e32 v54, 1.0, v54
	v_add_f32_e32 v55, 1.0, v55
	v_rcp_f32_e32 v60, v56
	v_add_f32_e32 v56, 1.0, v57
	v_rcp_f32_e32 v54, v54
	v_rcp_f32_e32 v61, v56
	v_rcp_f32_e32 v55, v55
	v_pk_mul_f32 v[58:59], v[58:59], s[12:13] op_sel_hi:[1,0]
	v_pk_mul_f32 v[56:57], v[62:63], s[12:13] op_sel_hi:[1,0]
	v_pk_add_f32 v[50:51], v[50:51], v[82:83]
	global_store_dwordx4 v[66:67], v[56:59], off offset:16
	v_pk_mul_f32 v[54:55], v[54:55], s[12:13] op_sel_hi:[1,0]
	v_mul_f32_e32 v50, 0xbfb8aa3b, v50
	v_pk_mul_f32 v[56:57], v[60:61], s[12:13] op_sel_hi:[1,0]
	global_store_dwordx4 v[66:67], v[54:57], off offset:512
	v_pk_add_f32 v[46:47], v[46:47], v[106:107]
	v_pk_add_f32 v[48:49], v[48:49], v[108:109]
	v_exp_f32_e32 v54, v50
	v_mul_f32_e32 v50, 0xbfb8aa3b, v51
	v_exp_f32_e32 v55, v50
	v_pk_add_f32 v[50:51], v[52:53], v[84:85]
	v_mul_f32_e32 v46, 0xbfb8aa3b, v46
	v_mul_f32_e32 v50, 0xbfb8aa3b, v50
	v_mul_f32_e32 v51, 0xbfb8aa3b, v51
	v_exp_f32_e32 v50, v50
	v_exp_f32_e32 v51, v51
	v_mul_f32_e32 v47, 0xbfb8aa3b, v47
	v_mul_f32_e32 v48, 0xbfb8aa3b, v48
	v_mul_f32_e32 v49, 0xbfb8aa3b, v49
	v_add_f32_e32 v52, 1.0, v54
	v_exp_f32_e32 v46, v46
	v_exp_f32_e32 v47, v47
	v_exp_f32_e32 v48, v48
	v_exp_f32_e32 v49, v49
	v_rcp_f32_e32 v54, v52
	v_add_f32_e32 v52, 1.0, v55
	v_add_f32_e32 v50, 1.0, v50
	v_add_f32_e32 v51, 1.0, v51
	v_rcp_f32_e32 v55, v52
	v_rcp_f32_e32 v50, v50
	v_rcp_f32_e32 v51, v51
	v_pk_add_f32 v[42:43], v[42:43], v[98:99]
	v_add_f32_e32 v46, 1.0, v46
	v_add_f32_e32 v47, 1.0, v47
	v_add_f32_e32 v48, 1.0, v48
	v_add_f32_e32 v49, 1.0, v49
	v_mul_f32_e32 v42, 0xbfb8aa3b, v42
	v_rcp_f32_e32 v46, v46
	v_rcp_f32_e32 v48, v48
	v_rcp_f32_e32 v49, v49
	v_rcp_f32_e32 v47, v47
	v_exp_f32_e32 v42, v42
	v_pk_mul_f32 v[52:53], v[50:51], s[12:13] op_sel_hi:[1,0]
	v_pk_mul_f32 v[50:51], v[54:55], s[12:13] op_sel_hi:[1,0]
	s_mov_b64 s[6:7], 0x90000
	global_store_dwordx4 v[66:67], v[50:53], off offset:528
	v_pk_mul_f32 v[48:49], v[48:49], s[12:13] op_sel_hi:[1,0]
	v_pk_mul_f32 v[46:47], v[46:47], s[12:13] op_sel_hi:[1,0]
	v_lshl_add_u64 v[50:51], v[150:151], 0, s[6:7]
	s_mov_b32 s6, 0x90000
	v_add_co_u32_e32 v52, vcc, s6, v150
	v_pk_add_f32 v[44:45], v[44:45], v[100:101]
	s_nop 0
	v_addc_co_u32_e32 v53, vcc, 0, v151, vcc
	v_add_f32_e32 v42, 1.0, v42
	v_pk_add_f32 v[40:41], v[40:41], v[92:93]
	global_store_dwordx4 v[52:53], v[46:49], off
	v_pk_add_f32 v[38:39], v[38:39], v[90:91]
	v_mul_f32_e32 v40, 0xbfb8aa3b, v40
	v_rcp_f32_e32 v46, v42
	v_mul_f32_e32 v42, 0xbfb8aa3b, v43
	v_mul_f32_e32 v43, 0xbfb8aa3b, v44
	v_mul_f32_e32 v44, 0xbfb8aa3b, v45
	v_exp_f32_e32 v42, v42
	v_exp_f32_e32 v43, v43
	v_exp_f32_e32 v44, v44
	v_mul_f32_e32 v38, 0xbfb8aa3b, v38
	v_mul_f32_e32 v39, 0xbfb8aa3b, v39
	v_exp_f32_e32 v40, v40
	v_mul_f32_e32 v41, 0xbfb8aa3b, v41
	v_exp_f32_e32 v38, v38
	v_exp_f32_e32 v39, v39
	v_exp_f32_e32 v41, v41
	v_add_f32_e32 v45, 1.0, v42
	v_add_f32_e32 v42, 1.0, v43
	v_add_f32_e32 v43, 1.0, v44
	v_add_f32_e32 v40, 1.0, v40
	v_rcp_f32_e32 v42, v42
	v_rcp_f32_e32 v43, v43
	v_rcp_f32_e32 v47, v45
	v_add_f32_e32 v38, 1.0, v38
	v_add_f32_e32 v39, 1.0, v39
	v_rcp_f32_e32 v44, v40
	v_add_f32_e32 v40, 1.0, v41
	v_rcp_f32_e32 v38, v38
	v_rcp_f32_e32 v45, v40
	v_rcp_f32_e32 v39, v39
	v_pk_mul_f32 v[42:43], v[42:43], s[12:13] op_sel_hi:[1,0]
	v_pk_mul_f32 v[40:41], v[46:47], s[12:13] op_sel_hi:[1,0]
	v_pk_add_f32 v[34:35], v[34:35], v[82:83]
	global_store_dwordx4 v[50:51], v[40:43], off offset:16
	v_pk_mul_f32 v[38:39], v[38:39], s[12:13] op_sel_hi:[1,0]
	v_mul_f32_e32 v34, 0xbfb8aa3b, v34
	v_pk_mul_f32 v[40:41], v[44:45], s[12:13] op_sel_hi:[1,0]
	global_store_dwordx4 v[50:51], v[38:41], off offset:512
; __device__ __forceinline__ float fsigmoid(float x) { return __builtin_amdgcn_rcpf(1.0f + __expf(-x)); }
; #define EPI_ROWLOOP _Pragma("unroll") for (int ai = 0; ai < 2; ++ai) _Pragma("unroll") for (int m = 0; m < 4; ++m)
;     __device__ __forceinline__ bool operator()(f32x4 (&acc)[2][2][4][2], const Unit& u, int wr, int wc, int fr, int fq) const {
;     ...
;         EPI_ROWLOOP { float* rowp = OUT + (size_t)(row0 + ai * HALF + m * 16) * RW + col0;
; #pragma unroll
;             for (int bj = 0; bj < 2; ++bj)
; #pragma unroll
;                 for (int n = 0; n < 2; ++n) { f32x4 v = acc[ai][bj][m][n] + pv[bj][n];
; #pragma unroll
;                     for (int j = 0; j < 4; ++j) {
;                         if (ISDEC) v[j] = -0.60653065971263342f * fsigmoid(v[j]);
;                         else v[j] = fsigmoid(v[j]); }
;                     *(f32x4*)(rowp + bj * HALF + 4 * n) = v; } }
	v_pk_add_f32 v[30:31], v[30:31], v[106:107]
	v_pk_add_f32 v[32:33], v[32:33], v[108:109]
	v_exp_f32_e32 v38, v34
	v_mul_f32_e32 v34, 0xbfb8aa3b, v35
	v_exp_f32_e32 v39, v34
	v_pk_add_f32 v[34:35], v[36:37], v[84:85]
	v_mul_f32_e32 v30, 0xbfb8aa3b, v30
	v_mul_f32_e32 v34, 0xbfb8aa3b, v34
	v_mul_f32_e32 v35, 0xbfb8aa3b, v35
	v_exp_f32_e32 v34, v34
	v_exp_f32_e32 v35, v35
	v_mul_f32_e32 v31, 0xbfb8aa3b, v31
	v_mul_f32_e32 v32, 0xbfb8aa3b, v32
	v_mul_f32_e32 v33, 0xbfb8aa3b, v33
	v_add_f32_e32 v36, 1.0, v38
	v_exp_f32_e32 v30, v30
	v_exp_f32_e32 v31, v31
	v_exp_f32_e32 v32, v32
	v_exp_f32_e32 v33, v33
	v_rcp_f32_e32 v38, v36
	v_add_f32_e32 v36, 1.0, v39
	v_add_f32_e32 v34, 1.0, v34
	v_add_f32_e32 v35, 1.0, v35
	v_rcp_f32_e32 v39, v36
	v_rcp_f32_e32 v34, v34
	v_rcp_f32_e32 v35, v35
	v_pk_add_f32 v[26:27], v[26:27], v[98:99]
	v_add_f32_e32 v30, 1.0, v30
	v_add_f32_e32 v31, 1.0, v31
	v_add_f32_e32 v32, 1.0, v32
	v_add_f32_e32 v33, 1.0, v33
	v_mul_f32_e32 v26, 0xbfb8aa3b, v26
	v_rcp_f32_e32 v30, v30
	v_rcp_f32_e32 v32, v32
	v_rcp_f32_e32 v33, v33
	v_rcp_f32_e32 v31, v31
	v_exp_f32_e32 v26, v26
	v_pk_mul_f32 v[36:37], v[34:35], s[12:13] op_sel_hi:[1,0]
	v_pk_mul_f32 v[34:35], v[38:39], s[12:13] op_sel_hi:[1,0]
	s_mov_b64 s[6:7], 0xa0000
	global_store_dwordx4 v[50:51], v[34:37], off offset:528
	v_pk_mul_f32 v[32:33], v[32:33], s[12:13] op_sel_hi:[1,0]
	v_pk_mul_f32 v[30:31], v[30:31], s[12:13] op_sel_hi:[1,0]
	v_lshl_add_u64 v[34:35], v[150:151], 0, s[6:7]
	s_mov_b32 s6, 0xa0000
	v_add_co_u32_e32 v36, vcc, s6, v150
	v_pk_add_f32 v[28:29], v[28:29], v[100:101]
	s_nop 0
	v_addc_co_u32_e32 v37, vcc, 0, v151, vcc
	v_add_f32_e32 v26, 1.0, v26
	v_pk_add_f32 v[24:25], v[24:25], v[92:93]
	global_store_dwordx4 v[36:37], v[30:33], off
	v_pk_add_f32 v[22:23], v[22:23], v[90:91]
	v_mul_f32_e32 v24, 0xbfb8aa3b, v24
	v_rcp_f32_e32 v30, v26
	v_mul_f32_e32 v26, 0xbfb8aa3b, v27
	v_mul_f32_e32 v27, 0xbfb8aa3b, v28
	v_mul_f32_e32 v28, 0xbfb8aa3b, v29
	v_exp_f32_e32 v26, v26
	v_exp_f32_e32 v27, v27
	v_exp_f32_e32 v28, v28
	v_mul_f32_e32 v22, 0xbfb8aa3b, v22
	v_mul_f32_e32 v23, 0xbfb8aa3b, v23
	v_exp_f32_e32 v24, v24
	v_mul_f32_e32 v25, 0xbfb8aa3b, v25
	v_exp_f32_e32 v22, v22
	v_exp_f32_e32 v23, v23
	v_exp_f32_e32 v25, v25
	v_add_f32_e32 v29, 1.0, v26
	v_add_f32_e32 v26, 1.0, v27
	v_add_f32_e32 v27, 1.0, v28
	v_add_f32_e32 v24, 1.0, v24
	v_rcp_f32_e32 v26, v26
	v_rcp_f32_e32 v27, v27
	v_rcp_f32_e32 v31, v29
	v_add_f32_e32 v22, 1.0, v22
	v_add_f32_e32 v23, 1.0, v23
	v_rcp_f32_e32 v28, v24
	v_add_f32_e32 v24, 1.0, v25
	v_rcp_f32_e32 v22, v22
	v_rcp_f32_e32 v29, v24
	v_rcp_f32_e32 v23, v23
	v_pk_mul_f32 v[26:27], v[26:27], s[12:13] op_sel_hi:[1,0]
	v_pk_mul_f32 v[24:25], v[30:31], s[12:13] op_sel_hi:[1,0]
	v_pk_add_f32 v[18:19], v[18:19], v[82:83]
	global_store_dwordx4 v[34:35], v[24:27], off offset:16
	v_pk_mul_f32 v[22:23], v[22:23], s[12:13] op_sel_hi:[1,0]
	v_mul_f32_e32 v18, 0xbfb8aa3b, v18
	v_pk_mul_f32 v[24:25], v[28:29], s[12:13] op_sel_hi:[1,0]
	global_store_dwordx4 v[34:35], v[22:25], off offset:512
	v_pk_add_f32 v[14:15], v[14:15], v[106:107]
	v_pk_add_f32 v[16:17], v[16:17], v[108:109]
	v_exp_f32_e32 v22, v18
	v_mul_f32_e32 v18, 0xbfb8aa3b, v19
	v_exp_f32_e32 v23, v18
	v_pk_add_f32 v[18:19], v[20:21], v[84:85]
	v_mul_f32_e32 v14, 0xbfb8aa3b, v14
	v_mul_f32_e32 v18, 0xbfb8aa3b, v18
	v_mul_f32_e32 v19, 0xbfb8aa3b, v19
	v_exp_f32_e32 v18, v18
	v_exp_f32_e32 v19, v19
	v_mul_f32_e32 v15, 0xbfb8aa3b, v15
	v_mul_f32_e32 v16, 0xbfb8aa3b, v16
	v_mul_f32_e32 v17, 0xbfb8aa3b, v17
	v_add_f32_e32 v20, 1.0, v22
	v_exp_f32_e32 v14, v14
	v_exp_f32_e32 v15, v15
	v_exp_f32_e32 v16, v16
	v_exp_f32_e32 v17, v17
	v_rcp_f32_e32 v22, v20
	v_add_f32_e32 v20, 1.0, v23
	v_add_f32_e32 v18, 1.0, v18
	v_add_f32_e32 v19, 1.0, v19
	v_rcp_f32_e32 v23, v20
	v_rcp_f32_e32 v18, v18
	v_rcp_f32_e32 v19, v19
	v_add_f32_e32 v14, 1.0, v14
	v_add_f32_e32 v15, 1.0, v15
	v_add_f32_e32 v16, 1.0, v16
	v_add_f32_e32 v17, 1.0, v17
	v_pk_add_f32 v[10:11], v[10:11], v[98:99]
	v_pk_add_f32 v[110:111], v[110:111], v[106:107]
	v_rcp_f32_e32 v14, v14
	v_rcp_f32_e32 v16, v16
	v_rcp_f32_e32 v17, v17
	v_rcp_f32_e32 v15, v15
	v_mul_f32_e32 v10, 0xbfb8aa3b, v10
	v_mul_f32_e32 v110, 0xbfb8aa3b, v110
	v_pk_mul_f32 v[20:21], v[18:19], s[12:13] op_sel_hi:[1,0]
	v_pk_mul_f32 v[18:19], v[22:23], s[12:13] op_sel_hi:[1,0]
	s_mov_b64 s[6:7], 0xb0000
	v_exp_f32_e32 v10, v10
	v_exp_f32_e32 v110, v110
	global_store_dwordx4 v[34:35], v[18:21], off offset:528
	v_pk_mul_f32 v[16:17], v[16:17], s[12:13] op_sel_hi:[1,0]
	v_pk_mul_f32 v[14:15], v[14:15], s[12:13] op_sel_hi:[1,0]
	v_lshl_add_u64 v[18:19], v[150:151], 0, s[6:7]
	s_mov_b32 s6, 0xb0000
; __device__ __forceinline__ float fsigmoid(float x) { return __builtin_amdgcn_rcpf(1.0f + __expf(-x)); }
; #define PG8_BAR __builtin_amdgcn_s_barrier()
; #define PG8_ZERO() do { _Pragma("unroll") for (int a = 0; a < 2; ++a) _Pragma("unroll") for (int b = 0; b < 2; ++b) _Pragma("unroll") for (int m = 0; m < 4; ++m) _Pragma("unroll") for (int n = 0; n < 2; ++n) acc[a][b][m][n] = (f32x4){0.f, 0.f, 0.f, 0.f}; } while (0)
; #define EPI_ROWLOOP _Pragma("unroll") for (int ai = 0; ai < 2; ++ai) _Pragma("unroll") for (int m = 0; m < 4; ++m)
; template <class Epi, class Sched, bool ALIGN_EPI, bool F8 = false, int F8SC = F8_SCALES>
; __device__ __forceinline__ void gemm_phase(PG8_LAS unsigned char* lds, const __amdgpu_buffer_rsrc_t rsrc, const int lda, const int ldb, const int K, const Sched& S, const Epi& E) {
;     ...
;         if (!has_next) break;
;         if (!keep) PG8_ZERO();
;         cur = nxt; cA = nA; cB = nB; ++ui;
;         if constexpr (ALIGN_EPI) { if (wr == 1) PG8_BAR; }
;     __device__ __forceinline__ bool operator()(f32x4 (&acc)[2][2][4][2], const Unit& u, int wr, int wc, int fr, int fq) const {
;     ...
;         EPI_ROWLOOP { float* rowp = OUT + (size_t)(row0 + ai * HALF + m * 16) * RW + col0;
; #pragma unroll
;             for (int bj = 0; bj < 2; ++bj)
; #pragma unroll
;                 for (int n = 0; n < 2; ++n) { f32x4 v = acc[ai][bj][m][n] + pv[bj][n];
; #pragma unroll
;                     for (int j = 0; j < 4; ++j) {
;                         if (ISDEC) v[j] = -0.60653065971263342f * fsigmoid(v[j]);
;                         else v[j] = fsigmoid(v[j]); }
;                     *(f32x4*)(rowp + bj * HALF + 4 * n) = v; } }
	v_add_co_u32_e32 v20, vcc, s6, v150
	v_pk_add_f32 v[12:13], v[12:13], v[100:101]
	s_nop 0
	v_addc_co_u32_e32 v21, vcc, 0, v151, vcc
	v_pk_add_f32 v[112:113], v[112:113], v[108:109]
	global_store_dwordx4 v[20:21], v[14:17], off
	v_add_f32_e32 v116, 1.0, v110
	v_mul_f32_e32 v110, 0xbfb8aa3b, v111
	v_add_f32_e32 v14, 1.0, v10
	v_mul_f32_e32 v10, 0xbfb8aa3b, v11
	v_mul_f32_e32 v11, 0xbfb8aa3b, v12
	v_mul_f32_e32 v12, 0xbfb8aa3b, v13
	v_mul_f32_e32 v111, 0xbfb8aa3b, v112
	v_mul_f32_e32 v112, 0xbfb8aa3b, v113
	v_exp_f32_e32 v11, v11
	v_exp_f32_e32 v12, v12
	v_exp_f32_e32 v13, v10
	v_exp_f32_e32 v111, v111
	v_exp_f32_e32 v112, v112
	v_exp_f32_e32 v113, v110
	v_pk_add_f32 v[6:7], v[6:7], v[90:91]
	v_add_f32_e32 v10, 1.0, v11
	v_add_f32_e32 v11, 1.0, v12
	v_add_f32_e32 v12, 1.0, v13
	v_mul_f32_e32 v6, 0xbfb8aa3b, v6
	v_add_f32_e32 v110, 1.0, v111
	v_add_f32_e32 v111, 1.0, v112
	v_add_f32_e32 v112, 1.0, v113
	v_pk_add_f32 v[102:103], v[102:103], v[98:99]
	v_rcp_f32_e32 v10, v10
	v_rcp_f32_e32 v11, v11
	v_rcp_f32_e32 v14, v14
	v_rcp_f32_e32 v15, v12
	v_exp_f32_e32 v6, v6
	v_rcp_f32_e32 v110, v110
	v_rcp_f32_e32 v111, v111
	v_rcp_f32_e32 v116, v116
	v_rcp_f32_e32 v117, v112
	v_mul_f32_e32 v102, 0xbfb8aa3b, v102
	v_exp_f32_e32 v102, v102
	v_pk_mul_f32 v[12:13], v[10:11], s[12:13] op_sel_hi:[1,0]
	v_pk_mul_f32 v[10:11], v[14:15], s[12:13] op_sel_hi:[1,0]
	v_pk_add_f32 v[8:9], v[8:9], v[92:93]
	v_add_f32_e32 v6, 1.0, v6
	v_pk_add_f32 v[4:5], v[4:5], v[84:85]
	v_pk_mul_f32 v[112:113], v[110:111], s[12:13] op_sel_hi:[1,0]
	v_pk_mul_f32 v[110:111], v[116:117], s[12:13] op_sel_hi:[1,0]
	v_pk_add_f32 v[104:105], v[104:105], v[100:101]
	v_pk_add_f32 v[94:95], v[94:95], v[90:91]
	v_pk_add_f32 v[96:97], v[96:97], v[92:93]
	global_store_dwordx4 v[18:19], v[10:13], off offset:16
	v_pk_add_f32 v[2:3], v[2:3], v[82:83]
	v_mul_f32_e32 v4, 0xbfb8aa3b, v4
	v_rcp_f32_e32 v10, v6
	v_mul_f32_e32 v6, 0xbfb8aa3b, v7
	v_mul_f32_e32 v7, 0xbfb8aa3b, v8
	v_mul_f32_e32 v8, 0xbfb8aa3b, v9
	global_store_dwordx4 v[114:115], v[110:113], off
	v_mul_f32_e32 v94, 0xbfb8aa3b, v94
	v_mul_f32_e32 v95, 0xbfb8aa3b, v95
	v_add_f32_e32 v110, 1.0, v102
	v_mul_f32_e32 v102, 0xbfb8aa3b, v103
	v_mul_f32_e32 v103, 0xbfb8aa3b, v104
	v_mul_f32_e32 v104, 0xbfb8aa3b, v105
	v_mul_f32_e32 v96, 0xbfb8aa3b, v96
	v_mul_f32_e32 v97, 0xbfb8aa3b, v97
	v_exp_f32_e32 v6, v6
	v_exp_f32_e32 v7, v7
	v_exp_f32_e32 v8, v8
	v_mul_f32_e32 v2, 0xbfb8aa3b, v2
	v_mul_f32_e32 v3, 0xbfb8aa3b, v3
	v_exp_f32_e32 v4, v4
	v_mul_f32_e32 v5, 0xbfb8aa3b, v5
	v_exp_f32_e32 v103, v103
	v_exp_f32_e32 v104, v104
	v_exp_f32_e32 v105, v102
	v_exp_f32_e32 v94, v94
	v_exp_f32_e32 v95, v95
	v_exp_f32_e32 v96, v96
	v_exp_f32_e32 v97, v97
	v_exp_f32_e32 v2, v2
	v_exp_f32_e32 v3, v3
	v_exp_f32_e32 v5, v5
	v_add_f32_e32 v9, 1.0, v6
	v_add_f32_e32 v6, 1.0, v7
	v_add_f32_e32 v7, 1.0, v8
	v_add_f32_e32 v4, 1.0, v4
	v_add_f32_e32 v102, 1.0, v103
	v_add_f32_e32 v103, 1.0, v104
	v_add_f32_e32 v104, 1.0, v105
	v_add_f32_e32 v94, 1.0, v94
	v_add_f32_e32 v95, 1.0, v95
	v_add_f32_e32 v96, 1.0, v96
	v_add_f32_e32 v97, 1.0, v97
	v_rcp_f32_e32 v6, v6
	v_rcp_f32_e32 v7, v7
	v_rcp_f32_e32 v11, v9
	v_add_f32_e32 v2, 1.0, v2
	v_add_f32_e32 v3, 1.0, v3
	v_rcp_f32_e32 v8, v4
	v_add_f32_e32 v4, 1.0, v5
	v_rcp_f32_e32 v140, v155
	v_rcp_f32_e32 v141, v162
	v_rcp_f32_e32 v138, v163
	v_rcp_f32_e32 v139, v164
	v_rcp_f32_e32 v102, v102
	v_rcp_f32_e32 v103, v103
	v_rcp_f32_e32 v110, v110
	v_rcp_f32_e32 v111, v104
	v_rcp_f32_e32 v94, v94
	v_rcp_f32_e32 v96, v96
	v_rcp_f32_e32 v97, v97
	v_rcp_f32_e32 v95, v95
	v_rcp_f32_e32 v2, v2
	v_rcp_f32_e32 v9, v4
	v_rcp_f32_e32 v3, v3
	v_pk_mul_f32 v[6:7], v[6:7], s[12:13] op_sel_hi:[1,0]
	v_pk_mul_f32 v[4:5], v[10:11], s[12:13] op_sel_hi:[1,0]
	v_pk_mul_f32 v[138:139], v[138:139], s[12:13] op_sel_hi:[1,0]
	v_pk_mul_f32 v[136:137], v[140:141], s[12:13] op_sel_hi:[1,0]
	v_pk_mul_f32 v[104:105], v[102:103], s[12:13] op_sel_hi:[1,0]
	v_pk_mul_f32 v[102:103], v[110:111], s[12:13] op_sel_hi:[1,0]
	v_pk_mul_f32 v[96:97], v[96:97], s[12:13] op_sel_hi:[1,0]
	v_pk_mul_f32 v[94:95], v[94:95], s[12:13] op_sel_hi:[1,0]
	global_store_dwordx4 v[18:19], v[4:7], off offset:512
	v_pk_mul_f32 v[2:3], v[2:3], s[12:13] op_sel_hi:[1,0]
	s_and_b64 vcc, exec, s[4:5]
	v_pk_mul_f32 v[4:5], v[8:9], s[12:13] op_sel_hi:[1,0]
	s_mov_b64 s[4:5], -1
	global_store_dwordx4 v[150:151], v[136:139], off offset:512
	global_store_dwordx4 v[114:115], v[102:105], off offset:16
	global_store_dwordx4 v[114:115], v[94:97], off offset:512
	global_store_dwordx4 v[18:19], v[2:5], off offset:528
	s_cbranch_vccnz .LBB0_959
	s_andn2_b64 vcc, exec, s[8:9]
	s_cbranch_vccnz .LBB0_958
	s_barrier
	s_branch .LBB0_958

; #define PG8_STAGE(bufoff, goff, voff) do { _Pragma("unroll") for (int _i = 0; _i < 2; ++_i) \
;         __builtin_amdgcn_raw_ptr_buffer_load_lds(rsrc, (PG8_LAS void*)(lds + (bufoff) + ldsw + _i * 8192), 16, (int)(voff), (int)((goff) + _i * p1##voff), 0, 0); } while (0)
; #define PG8_LDA(dst, b, h) do { _Pragma("unroll") for (int m = 0; m < 4; ++m) dst[m] = PG8_LD8(lds + PG8_SA(b, h) + aoff + m * 2048); } while (0)
; #define PG8_LDB(dst, b, h) do { _Pragma("unroll") for (int n = 0; n < 2; ++n) dst[n] = PG8_LD8(lds + PG8_SB(b, h) + boff + n * 2048); } while (0)
; #define PG8_WAIT_V(n) asm volatile("s_waitcnt vmcnt(" #n ")" ::: "memory")
; #define PG8_WAIT_L(n) asm volatile("s_waitcnt lgkmcnt(" #n ")" ::: "memory")
; #define PG8_BAR __builtin_amdgcn_s_barrier()
; #define PG8_SCHED __builtin_amdgcn_sched_barrier(0)
; template <class Epi, class Sched, bool ALIGN_EPI, bool F8 = false, int F8SC = F8_SCALES>
; __device__ __forceinline__ void gemm_phase(PG8_LAS unsigned char* lds, const __amdgpu_buffer_rsrc_t rsrc, const int lda, const int ldb, const int K, const Sched& S, const Epi& E) {
;     ...
;         for (int t = 0; t < nt; t += 2) {
;             const bool last = (t == nt - 2);
;             const unsigned a1 = cA + (unsigned)(t + 1) * kstep;
;             const unsigned a2 = last ? nA : cA + (unsigned)(t + 2) * kstep, b2 = last ? nB : cB + (unsigned)(t + 2) * kstep;
;             const unsigned a3 = a2 + kstep, b3 = b2 + kstep;
;             PG8_LDB(B0, 0, 0); PG8_LDB(B1, 0, 1); PG8_SCHED; PG8_LDA(At, 0, 0); PG8_STAGE(PG8_SA(1, 1), a1 + hsA, voffA);
;             PG8_WAIT_V(8); PG8_WAIT_L(0); PG8_BAR; PG8_MMA(0, 0, At, B0); PG8_MMA(0, 1, At, B1); PG8_BAR; PG8_SCHED;
;             PG8_LDA(At, 0, 1); PG8_STAGE(PG8_SB(0, 0), b2, voffB); PG8_STAGE(PG8_SB(0, 1), b2 + hsB, voffB); PG8_STAGE(PG8_SA(0, 0), a2, voffA);
;             PG8_WAIT_V(8); PG8_WAIT_L(0); PG8_BAR; PG8_MMA(1, 0, At, B0); PG8_MMA(1, 1, At, B1); PG8_BAR; PG8_SCHED;
.LBB0_994:
	s_add_i32 s42, s41, 0x20080
	s_mov_b32 s43, 0
	s_mov_b64 s[6:7], -1
	s_mov_b64 s[12:13], 0
	s_waitcnt vmcnt(23)
	s_waitcnt vmcnt(22)
	ds_read_b128 v[106:109], v157
	ds_read_b128 v[110:113], v157 offset:1024
	ds_read_b128 v[114:117], v157 offset:2048
	ds_read_b128 v[122:125], v157 offset:3072
	ds_read_b128 v[150:153], v158
	ds_read_b128 v[162:165], v158 offset:1024
	ds_read_b128 v[166:169], v158 offset:2048
	ds_read_b128 v[170:173], v158 offset:3072
	s_add_i32 s46, s43, 0x100
	s_add_i32 s47, s46, s41
	s_and_b64 s[44:45], s[12:13], exec
	s_cselect_b32 s49, s36, s47
	s_add_i32 s46, s46, s40
	s_add_i32 s44, s49, 0x80
	s_and_b64 s[12:13], s[12:13], exec
	s_cselect_b32 s52, s37, s46
	s_add_i32 s55, s42, s43
	s_add_i32 s43, s52, 0x10080
	s_add_i32 s13, s52, 0x18080
	s_add_i32 s12, s49, 0x10080
	s_add_i32 s56, s55, 0x10000
	s_add_i32 s54, s52, 0x8000
	s_add_i32 s53, s52, 0x10000
	s_add_i32 s51, s52, 0x18000
	s_add_i32 s50, s49, 0x10000
	s_add_i32 s48, s49, 0x20000
	s_add_i32 s47, s49, 0x30000
	s_add_i32 s46, s52, 0x80
	s_add_i32 s45, s52, 0x8080
	s_mov_b32 s80, s96
	s_mov_b32 m0, s30
	ds_read_b128 v[174:177], v159
	ds_read_b128 v[178:181], v159 offset:1024
	ds_read_b128 v[182:185], v159 offset:2048
	ds_read_b128 v[186:189], v159 offset:3072
	ds_read_b128 v[190:193], v159 offset:4096
	ds_read_b128 v[194:197], v159 offset:5120
	ds_read_b128 v[198:201], v159 offset:6144
	ds_read_b128 v[202:205], v159 offset:7168
	buffer_load_dwordx4 v1, s[80:83], s55 offen lds
	s_mov_b32 m0, s31
	s_nop 0
	buffer_load_dwordx4 v1, s[80:83], s56 offen lds
	s_waitcnt vmcnt(8)
	s_waitcnt lgkmcnt(0)
	s_barrier
	s_setprio 1
	s_waitcnt lgkmcnt(7)
	v_mfma_f32_16x16x32_bf16 v[142:145], v[106:109], v[174:177], 0
	v_mfma_f32_16x16x32_bf16 v[138:141], v[114:117], v[174:177], 0
	s_waitcnt lgkmcnt(5)
	v_mfma_f32_16x16x32_bf16 v[126:129], v[106:109], v[182:185], 0
	v_mfma_f32_16x16x32_bf16 v[118:121], v[114:117], v[182:185], 0
	s_waitcnt lgkmcnt(3)
	v_mfma_f32_16x16x32_bf16 v[94:97], v[106:109], v[190:193], 0
	v_mfma_f32_16x16x32_bf16 v[90:93], v[114:117], v[190:193], 0
	s_waitcnt lgkmcnt(1)
	v_mfma_f32_16x16x32_bf16 v[78:81], v[106:109], v[198:201], 0
	v_mfma_f32_16x16x32_bf16 v[74:77], v[114:117], v[198:201], 0
	v_mfma_f32_16x16x32_bf16 v[142:145], v[110:113], v[178:181], v[142:145]
	v_mfma_f32_16x16x32_bf16 v[138:141], v[122:125], v[178:181], v[138:141]
	v_mfma_f32_16x16x32_bf16 v[126:129], v[110:113], v[186:189], v[126:129]
	v_mfma_f32_16x16x32_bf16 v[118:121], v[122:125], v[186:189], v[118:121]
	v_mfma_f32_16x16x32_bf16 v[94:97], v[110:113], v[194:197], v[94:97]
	v_mfma_f32_16x16x32_bf16 v[90:93], v[122:125], v[194:197], v[90:93]
	s_waitcnt lgkmcnt(0)
	v_mfma_f32_16x16x32_bf16 v[78:81], v[110:113], v[202:205], v[78:81]
	v_mfma_f32_16x16x32_bf16 v[74:77], v[122:125], v[202:205], v[74:77]
	s_setprio 0
	s_setprio 1
	v_mfma_f32_16x16x32_bf16 v[134:137], v[150:153], v[174:177], 0
	v_mfma_f32_16x16x32_bf16 v[130:133], v[166:169], v[174:177], 0
	v_mfma_f32_16x16x32_bf16 v[102:105], v[150:153], v[182:185], 0
	v_mfma_f32_16x16x32_bf16 v[98:101], v[166:169], v[182:185], 0
	v_mfma_f32_16x16x32_bf16 v[86:89], v[150:153], v[190:193], 0
	v_mfma_f32_16x16x32_bf16 v[82:85], v[166:169], v[190:193], 0
	v_mfma_f32_16x16x32_bf16 v[70:73], v[150:153], v[198:201], 0
	v_mfma_f32_16x16x32_bf16 v[66:69], v[166:169], v[198:201], 0
	v_mfma_f32_16x16x32_bf16 v[134:137], v[162:165], v[178:181], v[134:137]
	v_mfma_f32_16x16x32_bf16 v[130:133], v[170:173], v[178:181], v[130:133]
	v_mfma_f32_16x16x32_bf16 v[102:105], v[162:165], v[186:189], v[102:105]
	v_mfma_f32_16x16x32_bf16 v[98:101], v[170:173], v[186:189], v[98:101]
	v_mfma_f32_16x16x32_bf16 v[86:89], v[162:165], v[194:197], v[86:89]
	v_mfma_f32_16x16x32_bf16 v[82:85], v[170:173], v[194:197], v[82:85]
	v_mfma_f32_16x16x32_bf16 v[70:73], v[162:165], v[202:205], v[70:73]
	v_mfma_f32_16x16x32_bf16 v[66:69], v[170:173], v[202:205], v[66:69]
	s_setprio 0
	s_barrier
	s_mov_b32 m0, s16
	ds_read_b128 v[174:177], v159 offset:16384
	ds_read_b128 v[178:181], v159 offset:17408
	ds_read_b128 v[182:185], v159 offset:18432
	ds_read_b128 v[186:189], v159 offset:19456
	ds_read_b128 v[190:193], v159 offset:20480
	ds_read_b128 v[194:197], v159 offset:21504
	ds_read_b128 v[198:201], v159 offset:22528
	ds_read_b128 v[202:205], v159 offset:23552
	buffer_load_dwordx4 v156, s[80:83], s52 offen lds
	s_mov_b32 m0, s17
	s_nop 0
	buffer_load_dwordx4 v156, s[80:83], s54 offen lds
	s_mov_b32 m0, s18
	s_nop 0
	buffer_load_dwordx4 v156, s[80:83], s53 offen lds
	s_mov_b32 m0, s19
	s_nop 0
	buffer_load_dwordx4 v156, s[80:83], s51 offen lds
	s_mov_b32 m0, s15
	s_nop 0
	buffer_load_dwordx4 v1, s[80:83], s49 offen lds
	s_mov_b32 m0, s20
	s_nop 0
	buffer_load_dwordx4 v1, s[80:83], s50 offen lds
	s_waitcnt vmcnt(8)
	s_waitcnt lgkmcnt(0)
	s_barrier
; #define PG8_STAGE(bufoff, goff, voff) do { _Pragma("unroll") for (int _i = 0; _i < 2; ++_i) \
;         __builtin_amdgcn_raw_ptr_buffer_load_lds(rsrc, (PG8_LAS void*)(lds + (bufoff) + ldsw + _i * 8192), 16, (int)(voff), (int)((goff) + _i * p1##voff), 0, 0); } while (0)
; #define PG8_LDA(dst, b, h) do { _Pragma("unroll") for (int m = 0; m < 4; ++m) dst[m] = PG8_LD8(lds + PG8_SA(b, h) + aoff + m * 2048); } while (0)
; #define PG8_LDB(dst, b, h) do { _Pragma("unroll") for (int n = 0; n < 2; ++n) dst[n] = PG8_LD8(lds + PG8_SB(b, h) + boff + n * 2048); } while (0)
; #define PG8_WAIT_V(n) asm volatile("s_waitcnt vmcnt(" #n ")" ::: "memory")
; #define PG8_WAIT_L(n) asm volatile("s_waitcnt lgkmcnt(" #n ")" ::: "memory")
; #define PG8_BAR __builtin_amdgcn_s_barrier()
; #define PG8_SCHED __builtin_amdgcn_sched_barrier(0)
; template <class Epi, class Sched, bool ALIGN_EPI, bool F8 = false, int F8SC = F8_SCALES>
; __device__ __forceinline__ void gemm_phase(PG8_LAS unsigned char* lds, const __amdgpu_buffer_rsrc_t rsrc, const int lda, const int ldb, const int K, const Sched& S, const Epi& E) {
;     ...
;             PG8_WAIT_V(8); PG8_WAIT_L(0); PG8_BAR; PG8_MMA(0, 0, At, B0); PG8_MMA(0, 1, At, B1); PG8_BAR; PG8_SCHED;
;             PG8_LDA(At, 0, 1); PG8_STAGE(PG8_SB(0, 0), b2, voffB); PG8_STAGE(PG8_SB(0, 1), b2 + hsB, voffB); PG8_STAGE(PG8_SA(0, 0), a2, voffA);
;             PG8_WAIT_V(8); PG8_WAIT_L(0); PG8_BAR; PG8_MMA(1, 0, At, B0); PG8_MMA(1, 1, At, B1); PG8_BAR; PG8_SCHED;
;             PG8_LDB(B0, 1, 0); PG8_LDB(B1, 1, 1); PG8_SCHED; PG8_LDA(At, 1, 0); PG8_STAGE(PG8_SA(0, 1), a2 + hsA, voffA);
;             PG8_WAIT_V(8); PG8_WAIT_L(0); PG8_BAR; PG8_MMA(0, 0, At, B0); PG8_MMA(0, 1, At, B1); PG8_BAR; PG8_SCHED;
	s_setprio 1
	s_waitcnt lgkmcnt(7)
	v_mfma_f32_16x16x32_bf16 v[62:65], v[106:109], v[174:177], 0
	v_mfma_f32_16x16x32_bf16 v[58:61], v[114:117], v[174:177], 0
	s_waitcnt lgkmcnt(5)
	v_mfma_f32_16x16x32_bf16 v[46:49], v[106:109], v[182:185], 0
	v_mfma_f32_16x16x32_bf16 v[42:45], v[114:117], v[182:185], 0
	s_waitcnt lgkmcnt(3)
	v_mfma_f32_16x16x32_bf16 v[30:33], v[106:109], v[190:193], 0
	v_mfma_f32_16x16x32_bf16 v[26:29], v[114:117], v[190:193], 0
	s_waitcnt lgkmcnt(1)
	v_mfma_f32_16x16x32_bf16 v[14:17], v[106:109], v[198:201], 0
	v_mfma_f32_16x16x32_bf16 v[10:13], v[114:117], v[198:201], 0
	v_mfma_f32_16x16x32_bf16 v[62:65], v[110:113], v[178:181], v[62:65]
	v_mfma_f32_16x16x32_bf16 v[58:61], v[122:125], v[178:181], v[58:61]
	v_mfma_f32_16x16x32_bf16 v[46:49], v[110:113], v[186:189], v[46:49]
	v_mfma_f32_16x16x32_bf16 v[42:45], v[122:125], v[186:189], v[42:45]
	v_mfma_f32_16x16x32_bf16 v[30:33], v[110:113], v[194:197], v[30:33]
	v_mfma_f32_16x16x32_bf16 v[26:29], v[122:125], v[194:197], v[26:29]
	s_waitcnt lgkmcnt(0)
	v_mfma_f32_16x16x32_bf16 v[14:17], v[110:113], v[202:205], v[14:17]
	v_mfma_f32_16x16x32_bf16 v[10:13], v[122:125], v[202:205], v[10:13]
	s_setprio 0
	s_setprio 1
	v_mfma_f32_16x16x32_bf16 v[54:57], v[150:153], v[174:177], 0
	v_mfma_f32_16x16x32_bf16 v[50:53], v[166:169], v[174:177], 0
	v_mfma_f32_16x16x32_bf16 v[38:41], v[150:153], v[182:185], 0
	v_mfma_f32_16x16x32_bf16 v[34:37], v[166:169], v[182:185], 0
	v_mfma_f32_16x16x32_bf16 v[22:25], v[150:153], v[190:193], 0
	v_mfma_f32_16x16x32_bf16 v[18:21], v[166:169], v[190:193], 0
	v_mfma_f32_16x16x32_bf16 v[6:9], v[150:153], v[198:201], 0
	v_mfma_f32_16x16x32_bf16 v[2:5], v[166:169], v[198:201], 0
	v_mfma_f32_16x16x32_bf16 v[54:57], v[162:165], v[178:181], v[54:57]
	v_mfma_f32_16x16x32_bf16 v[50:53], v[170:173], v[178:181], v[50:53]
	v_mfma_f32_16x16x32_bf16 v[38:41], v[162:165], v[186:189], v[38:41]
	v_mfma_f32_16x16x32_bf16 v[34:37], v[170:173], v[186:189], v[34:37]
	v_mfma_f32_16x16x32_bf16 v[22:25], v[162:165], v[194:197], v[22:25]
	v_mfma_f32_16x16x32_bf16 v[18:21], v[170:173], v[194:197], v[18:21]
	v_mfma_f32_16x16x32_bf16 v[6:9], v[162:165], v[202:205], v[6:9]
	v_mfma_f32_16x16x32_bf16 v[2:5], v[170:173], v[202:205], v[2:5]
	s_setprio 0
	s_barrier
	ds_read_b128 v[106:109], v160
	ds_read_b128 v[110:113], v160 offset:1024
	ds_read_b128 v[114:117], v160 offset:2048
	ds_read_b128 v[122:125], v160 offset:3072
	ds_read_b128 v[150:153], v161
	ds_read_b128 v[162:165], v161 offset:1024
	ds_read_b128 v[166:169], v161 offset:2048
	ds_read_b128 v[170:173], v161 offset:3072
	s_mov_b32 m0, s21
	ds_read_b128 v[174:177], v159 offset:32768
	ds_read_b128 v[178:181], v159 offset:33792
	ds_read_b128 v[182:185], v159 offset:34816
	ds_read_b128 v[186:189], v159 offset:35840
	ds_read_b128 v[190:193], v159 offset:36864
	ds_read_b128 v[194:197], v159 offset:37888
	ds_read_b128 v[198:201], v159 offset:38912
	ds_read_b128 v[202:205], v159 offset:39936
	buffer_load_dwordx4 v1, s[80:83], s48 offen lds
	s_mov_b32 m0, s22
	s_nop 0
	buffer_load_dwordx4 v1, s[80:83], s47 offen lds
	s_waitcnt vmcnt(8)
	s_waitcnt lgkmcnt(0)
	s_barrier
	s_setprio 1
	s_waitcnt lgkmcnt(7)
	v_mfma_f32_16x16x32_bf16 v[142:145], v[106:109], v[174:177], v[142:145]
	v_mfma_f32_16x16x32_bf16 v[138:141], v[114:117], v[174:177], v[138:141]
	s_waitcnt lgkmcnt(5)
	v_mfma_f32_16x16x32_bf16 v[126:129], v[106:109], v[182:185], v[126:129]
	v_mfma_f32_16x16x32_bf16 v[118:121], v[114:117], v[182:185], v[118:121]
	s_waitcnt lgkmcnt(3)
	v_mfma_f32_16x16x32_bf16 v[94:97], v[106:109], v[190:193], v[94:97]
	v_mfma_f32_16x16x32_bf16 v[90:93], v[114:117], v[190:193], v[90:93]
	s_waitcnt lgkmcnt(1)
	v_mfma_f32_16x16x32_bf16 v[78:81], v[106:109], v[198:201], v[78:81]
	v_mfma_f32_16x16x32_bf16 v[74:77], v[114:117], v[198:201], v[74:77]
	v_mfma_f32_16x16x32_bf16 v[142:145], v[110:113], v[178:181], v[142:145]
	v_mfma_f32_16x16x32_bf16 v[138:141], v[122:125], v[178:181], v[138:141]
	v_mfma_f32_16x16x32_bf16 v[126:129], v[110:113], v[186:189], v[126:129]
	v_mfma_f32_16x16x32_bf16 v[118:121], v[122:125], v[186:189], v[118:121]
	v_mfma_f32_16x16x32_bf16 v[94:97], v[110:113], v[194:197], v[94:97]
	v_mfma_f32_16x16x32_bf16 v[90:93], v[122:125], v[194:197], v[90:93]
	s_waitcnt lgkmcnt(0)
	v_mfma_f32_16x16x32_bf16 v[78:81], v[110:113], v[202:205], v[78:81]
	v_mfma_f32_16x16x32_bf16 v[74:77], v[122:125], v[202:205], v[74:77]
	s_setprio 0
	s_setprio 1
	v_mfma_f32_16x16x32_bf16 v[134:137], v[150:153], v[174:177], v[134:137]
	v_mfma_f32_16x16x32_bf16 v[130:133], v[166:169], v[174:177], v[130:133]
	v_mfma_f32_16x16x32_bf16 v[102:105], v[150:153], v[182:185], v[102:105]
	v_mfma_f32_16x16x32_bf16 v[98:101], v[166:169], v[182:185], v[98:101]
	v_mfma_f32_16x16x32_bf16 v[86:89], v[150:153], v[190:193], v[86:89]
	v_mfma_f32_16x16x32_bf16 v[82:85], v[166:169], v[190:193], v[82:85]
	v_mfma_f32_16x16x32_bf16 v[70:73], v[150:153], v[198:201], v[70:73]
	v_mfma_f32_16x16x32_bf16 v[66:69], v[166:169], v[198:201], v[66:69]
	v_mfma_f32_16x16x32_bf16 v[134:137], v[162:165], v[178:181], v[134:137]
	v_mfma_f32_16x16x32_bf16 v[130:133], v[170:173], v[178:181], v[130:133]
	v_mfma_f32_16x16x32_bf16 v[102:105], v[162:165], v[186:189], v[102:105]
	v_mfma_f32_16x16x32_bf16 v[98:101], v[170:173], v[186:189], v[98:101]
	v_mfma_f32_16x16x32_bf16 v[86:89], v[162:165], v[194:197], v[86:89]
	v_mfma_f32_16x16x32_bf16 v[82:85], v[170:173], v[194:197], v[82:85]
	v_mfma_f32_16x16x32_bf16 v[70:73], v[162:165], v[202:205], v[70:73]
	v_mfma_f32_16x16x32_bf16 v[66:69], v[170:173], v[202:205], v[66:69]
	s_setprio 0
	s_barrier
; #define PG8_STAGE(bufoff, goff, voff) do { _Pragma("unroll") for (int _i = 0; _i < 2; ++_i) \
;         __builtin_amdgcn_raw_ptr_buffer_load_lds(rsrc, (PG8_LAS void*)(lds + (bufoff) + ldsw + _i * 8192), 16, (int)(voff), (int)((goff) + _i * p1##voff), 0, 0); } while (0)
; #define PG8_LDA(dst, b, h) do { _Pragma("unroll") for (int m = 0; m < 4; ++m) dst[m] = PG8_LD8(lds + PG8_SA(b, h) + aoff + m * 2048); } while (0)
; #define PG8_WAIT_V(n) asm volatile("s_waitcnt vmcnt(" #n ")" ::: "memory")
; #define PG8_WAIT_L(n) asm volatile("s_waitcnt lgkmcnt(" #n ")" ::: "memory")
; #define PG8_BAR __builtin_amdgcn_s_barrier()
; #define PG8_SCHED __builtin_amdgcn_sched_barrier(0)
; template <class Epi, class Sched, bool ALIGN_EPI, bool F8 = false, int F8SC = F8_SCALES>
; __device__ __forceinline__ void gemm_phase(PG8_LAS unsigned char* lds, const __amdgpu_buffer_rsrc_t rsrc, const int lda, const int ldb, const int K, const Sched& S, const Epi& E) {
;     ...
;             PG8_LDA(At, 1, 1); PG8_STAGE(PG8_SB(1, 0), b3, voffB); PG8_STAGE(PG8_SB(1, 1), b3 + hsB, voffB); PG8_STAGE(PG8_SA(1, 0), a3, voffA);
;             PG8_WAIT_V(8); PG8_WAIT_L(0); PG8_BAR; PG8_MMA(1, 0, At, B0); PG8_MMA(1, 1, At, B1); PG8_BAR; PG8_SCHED;
;         }
	s_mov_b32 m0, s24
	ds_read_b128 v[174:177], v159 offset:49152
	ds_read_b128 v[178:181], v159 offset:50176
	ds_read_b128 v[182:185], v159 offset:51200
	ds_read_b128 v[186:189], v159 offset:52224
	ds_read_b128 v[190:193], v159 offset:53248
	ds_read_b128 v[194:197], v159 offset:54272
	ds_read_b128 v[198:201], v159 offset:55296
	ds_read_b128 v[202:205], v159 offset:56320
	buffer_load_dwordx4 v156, s[80:83], s46 offen lds
	s_mov_b32 m0, s25
	s_nop 0
	buffer_load_dwordx4 v156, s[80:83], s45 offen lds
	s_mov_b32 m0, s28
	s_nop 0
	buffer_load_dwordx4 v156, s[80:83], s43 offen lds
	s_mov_b32 m0, s29
	s_nop 0
	buffer_load_dwordx4 v156, s[80:83], s13 offen lds
	s_mov_b32 m0, s26
	s_nop 0
	buffer_load_dwordx4 v1, s[80:83], s44 offen lds
	s_mov_b32 m0, s27
	s_nop 0
	buffer_load_dwordx4 v1, s[80:83], s12 offen lds
	s_waitcnt vmcnt(8)
	s_waitcnt lgkmcnt(0)
	s_barrier
	s_setprio 1
	s_waitcnt lgkmcnt(7)
	v_mfma_f32_16x16x32_bf16 v[62:65], v[106:109], v[174:177], v[62:65]
	v_mfma_f32_16x16x32_bf16 v[58:61], v[114:117], v[174:177], v[58:61]
	s_waitcnt lgkmcnt(5)
	v_mfma_f32_16x16x32_bf16 v[46:49], v[106:109], v[182:185], v[46:49]
	v_mfma_f32_16x16x32_bf16 v[42:45], v[114:117], v[182:185], v[42:45]
	s_waitcnt lgkmcnt(3)
	v_mfma_f32_16x16x32_bf16 v[30:33], v[106:109], v[190:193], v[30:33]
	v_mfma_f32_16x16x32_bf16 v[26:29], v[114:117], v[190:193], v[26:29]
	s_waitcnt lgkmcnt(1)
	v_mfma_f32_16x16x32_bf16 v[14:17], v[106:109], v[198:201], v[14:17]
	v_mfma_f32_16x16x32_bf16 v[10:13], v[114:117], v[198:201], v[10:13]
	v_mfma_f32_16x16x32_bf16 v[62:65], v[110:113], v[178:181], v[62:65]
	v_mfma_f32_16x16x32_bf16 v[58:61], v[122:125], v[178:181], v[58:61]
	v_mfma_f32_16x16x32_bf16 v[46:49], v[110:113], v[186:189], v[46:49]
	v_mfma_f32_16x16x32_bf16 v[42:45], v[122:125], v[186:189], v[42:45]
	v_mfma_f32_16x16x32_bf16 v[30:33], v[110:113], v[194:197], v[30:33]
	v_mfma_f32_16x16x32_bf16 v[26:29], v[122:125], v[194:197], v[26:29]
	s_waitcnt lgkmcnt(0)
	v_mfma_f32_16x16x32_bf16 v[14:17], v[110:113], v[202:205], v[14:17]
	v_mfma_f32_16x16x32_bf16 v[10:13], v[122:125], v[202:205], v[10:13]
	s_setprio 0
	s_setprio 1
	v_mfma_f32_16x16x32_bf16 v[54:57], v[150:153], v[174:177], v[54:57]
	v_mfma_f32_16x16x32_bf16 v[50:53], v[166:169], v[174:177], v[50:53]
	v_mfma_f32_16x16x32_bf16 v[38:41], v[150:153], v[182:185], v[38:41]
	v_mfma_f32_16x16x32_bf16 v[34:37], v[166:169], v[182:185], v[34:37]
	v_mfma_f32_16x16x32_bf16 v[22:25], v[150:153], v[190:193], v[22:25]
	v_mfma_f32_16x16x32_bf16 v[18:21], v[166:169], v[190:193], v[18:21]
	v_mfma_f32_16x16x32_bf16 v[6:9], v[150:153], v[198:201], v[6:9]
	v_mfma_f32_16x16x32_bf16 v[2:5], v[166:169], v[198:201], v[2:5]
	v_mfma_f32_16x16x32_bf16 v[54:57], v[162:165], v[178:181], v[54:57]
	v_mfma_f32_16x16x32_bf16 v[50:53], v[170:173], v[178:181], v[50:53]
	v_mfma_f32_16x16x32_bf16 v[38:41], v[162:165], v[186:189], v[38:41]
	v_mfma_f32_16x16x32_bf16 v[34:37], v[170:173], v[186:189], v[34:37]
	v_mfma_f32_16x16x32_bf16 v[22:25], v[162:165], v[194:197], v[22:25]
	v_mfma_f32_16x16x32_bf16 v[18:21], v[170:173], v[194:197], v[18:21]
	v_mfma_f32_16x16x32_bf16 v[6:9], v[162:165], v[202:205], v[6:9]
	v_mfma_f32_16x16x32_bf16 v[2:5], v[170:173], v[202:205], v[2:5]
	s_setprio 0
	s_barrier
	s_andn2_b64 vcc, exec, s[6:7]
	s_mov_b64 s[12:13], -1
	s_mov_b64 s[6:7], 0
	s_movk_i32 s43, 0x100
	s_cbranch_vccz .LBB0_995
	s_branch .Lpeel_after_995
.LBB0_995:
	ds_read_b128 v[106:109], v157
	ds_read_b128 v[110:113], v157 offset:1024
	ds_read_b128 v[114:117], v157 offset:2048
	ds_read_b128 v[122:125], v157 offset:3072
	ds_read_b128 v[150:153], v158
	ds_read_b128 v[162:165], v158 offset:1024
	ds_read_b128 v[166:169], v158 offset:2048
	ds_read_b128 v[170:173], v158 offset:3072
	s_add_i32 s46, s43, 0x100
	s_add_i32 s47, s46, s41
	s_and_b64 s[44:45], s[12:13], exec
	s_cselect_b32 s49, s36, s47
	s_add_i32 s46, s46, s40
	s_add_i32 s44, s49, 0x80
	s_and_b64 s[12:13], s[12:13], exec
	s_cselect_b32 s52, s37, s46
	s_add_i32 s55, s42, s43
	s_add_i32 s43, s52, 0x10080
	s_add_i32 s13, s52, 0x18080
	s_add_i32 s12, s49, 0x10080
	s_add_i32 s56, s55, 0x10000
	s_add_i32 s54, s52, 0x8000
	s_add_i32 s53, s52, 0x10000
	s_add_i32 s51, s52, 0x18000
	s_add_i32 s50, s49, 0x10000
	s_add_i32 s48, s49, 0x20000
	s_add_i32 s47, s49, 0x30000
	s_add_i32 s46, s52, 0x80
	s_add_i32 s45, s52, 0x8080
	s_mov_b32 s80, s96
	s_mov_b32 m0, s30
	ds_read_b128 v[174:177], v159
	ds_read_b128 v[178:181], v159 offset:1024
	ds_read_b128 v[182:185], v159 offset:2048
	ds_read_b128 v[186:189], v159 offset:3072
	ds_read_b128 v[190:193], v159 offset:4096
	ds_read_b128 v[194:197], v159 offset:5120
	ds_read_b128 v[198:201], v159 offset:6144
	ds_read_b128 v[202:205], v159 offset:7168
	buffer_load_dwordx4 v1, s[80:83], s55 offen lds
	s_mov_b32 m0, s31
	s_nop 0
	buffer_load_dwordx4 v1, s[80:83], s56 offen lds
	s_waitcnt vmcnt(8)
	s_waitcnt lgkmcnt(0)
	s_barrier
; #define PG8_STAGE(bufoff, goff, voff) do { _Pragma("unroll") for (int _i = 0; _i < 2; ++_i) \
;         __builtin_amdgcn_raw_ptr_buffer_load_lds(rsrc, (PG8_LAS void*)(lds + (bufoff) + ldsw + _i * 8192), 16, (int)(voff), (int)((goff) + _i * p1##voff), 0, 0); } while (0)
; #define PG8_LDA(dst, b, h) do { _Pragma("unroll") for (int m = 0; m < 4; ++m) dst[m] = PG8_LD8(lds + PG8_SA(b, h) + aoff + m * 2048); } while (0)
; #define PG8_LDB(dst, b, h) do { _Pragma("unroll") for (int n = 0; n < 2; ++n) dst[n] = PG8_LD8(lds + PG8_SB(b, h) + boff + n * 2048); } while (0)
; #define PG8_WAIT_V(n) asm volatile("s_waitcnt vmcnt(" #n ")" ::: "memory")
; #define PG8_WAIT_L(n) asm volatile("s_waitcnt lgkmcnt(" #n ")" ::: "memory")
; #define PG8_BAR __builtin_amdgcn_s_barrier()
; #define PG8_SCHED __builtin_amdgcn_sched_barrier(0)
; template <class Epi, class Sched, bool ALIGN_EPI, bool F8 = false, int F8SC = F8_SCALES>
; __device__ __forceinline__ void gemm_phase(PG8_LAS unsigned char* lds, const __amdgpu_buffer_rsrc_t rsrc, const int lda, const int ldb, const int K, const Sched& S, const Epi& E) {
;     ...
;             PG8_WAIT_V(8); PG8_WAIT_L(0); PG8_BAR; PG8_MMA(0, 0, At, B0); PG8_MMA(0, 1, At, B1); PG8_BAR; PG8_SCHED;
;             PG8_LDA(At, 0, 1); PG8_STAGE(PG8_SB(0, 0), b2, voffB); PG8_STAGE(PG8_SB(0, 1), b2 + hsB, voffB); PG8_STAGE(PG8_SA(0, 0), a2, voffA);
;             PG8_WAIT_V(8); PG8_WAIT_L(0); PG8_BAR; PG8_MMA(1, 0, At, B0); PG8_MMA(1, 1, At, B1); PG8_BAR; PG8_SCHED;
;             PG8_LDB(B0, 1, 0); PG8_LDB(B1, 1, 1); PG8_SCHED; PG8_LDA(At, 1, 0); PG8_STAGE(PG8_SA(0, 1), a2 + hsA, voffA);
;             PG8_WAIT_V(8); PG8_WAIT_L(0); PG8_BAR; PG8_MMA(0, 0, At, B0); PG8_MMA(0, 1, At, B1); PG8_BAR; PG8_SCHED;
	s_setprio 1
	s_waitcnt lgkmcnt(7)
	v_mfma_f32_16x16x32_bf16 v[142:145], v[106:109], v[174:177], v[142:145]
	v_mfma_f32_16x16x32_bf16 v[138:141], v[114:117], v[174:177], v[138:141]
	s_waitcnt lgkmcnt(5)
	v_mfma_f32_16x16x32_bf16 v[126:129], v[106:109], v[182:185], v[126:129]
	v_mfma_f32_16x16x32_bf16 v[118:121], v[114:117], v[182:185], v[118:121]
	s_waitcnt lgkmcnt(3)
	v_mfma_f32_16x16x32_bf16 v[94:97], v[106:109], v[190:193], v[94:97]
	v_mfma_f32_16x16x32_bf16 v[90:93], v[114:117], v[190:193], v[90:93]
	s_waitcnt lgkmcnt(1)
	v_mfma_f32_16x16x32_bf16 v[78:81], v[106:109], v[198:201], v[78:81]
	v_mfma_f32_16x16x32_bf16 v[74:77], v[114:117], v[198:201], v[74:77]
	v_mfma_f32_16x16x32_bf16 v[142:145], v[110:113], v[178:181], v[142:145]
	v_mfma_f32_16x16x32_bf16 v[138:141], v[122:125], v[178:181], v[138:141]
	v_mfma_f32_16x16x32_bf16 v[126:129], v[110:113], v[186:189], v[126:129]
	v_mfma_f32_16x16x32_bf16 v[118:121], v[122:125], v[186:189], v[118:121]
	v_mfma_f32_16x16x32_bf16 v[94:97], v[110:113], v[194:197], v[94:97]
	v_mfma_f32_16x16x32_bf16 v[90:93], v[122:125], v[194:197], v[90:93]
	s_waitcnt lgkmcnt(0)
	v_mfma_f32_16x16x32_bf16 v[78:81], v[110:113], v[202:205], v[78:81]
	v_mfma_f32_16x16x32_bf16 v[74:77], v[122:125], v[202:205], v[74:77]
	s_setprio 0
	s_setprio 1
	v_mfma_f32_16x16x32_bf16 v[134:137], v[150:153], v[174:177], v[134:137]
	v_mfma_f32_16x16x32_bf16 v[130:133], v[166:169], v[174:177], v[130:133]
	v_mfma_f32_16x16x32_bf16 v[102:105], v[150:153], v[182:185], v[102:105]
	v_mfma_f32_16x16x32_bf16 v[98:101], v[166:169], v[182:185], v[98:101]
	v_mfma_f32_16x16x32_bf16 v[86:89], v[150:153], v[190:193], v[86:89]
	v_mfma_f32_16x16x32_bf16 v[82:85], v[166:169], v[190:193], v[82:85]
	v_mfma_f32_16x16x32_bf16 v[70:73], v[150:153], v[198:201], v[70:73]
	v_mfma_f32_16x16x32_bf16 v[66:69], v[166:169], v[198:201], v[66:69]
	v_mfma_f32_16x16x32_bf16 v[134:137], v[162:165], v[178:181], v[134:137]
	v_mfma_f32_16x16x32_bf16 v[130:133], v[170:173], v[178:181], v[130:133]
	v_mfma_f32_16x16x32_bf16 v[102:105], v[162:165], v[186:189], v[102:105]
	v_mfma_f32_16x16x32_bf16 v[98:101], v[170:173], v[186:189], v[98:101]
	v_mfma_f32_16x16x32_bf16 v[86:89], v[162:165], v[194:197], v[86:89]
	v_mfma_f32_16x16x32_bf16 v[82:85], v[170:173], v[194:197], v[82:85]
	v_mfma_f32_16x16x32_bf16 v[70:73], v[162:165], v[202:205], v[70:73]
	v_mfma_f32_16x16x32_bf16 v[66:69], v[170:173], v[202:205], v[66:69]
	s_setprio 0
	s_barrier
	s_mov_b32 m0, s16
	ds_read_b128 v[174:177], v159 offset:16384
	ds_read_b128 v[178:181], v159 offset:17408
	ds_read_b128 v[182:185], v159 offset:18432
	ds_read_b128 v[186:189], v159 offset:19456
	ds_read_b128 v[190:193], v159 offset:20480
	ds_read_b128 v[194:197], v159 offset:21504
	ds_read_b128 v[198:201], v159 offset:22528
	ds_read_b128 v[202:205], v159 offset:23552
	buffer_load_dwordx4 v156, s[80:83], s52 offen lds
	s_mov_b32 m0, s17
	s_nop 0
	buffer_load_dwordx4 v156, s[80:83], s54 offen lds
	s_mov_b32 m0, s18
	s_nop 0
	buffer_load_dwordx4 v156, s[80:83], s53 offen lds
	s_mov_b32 m0, s19
	s_nop 0
	buffer_load_dwordx4 v156, s[80:83], s51 offen lds
	s_mov_b32 m0, s15
	s_nop 0
	buffer_load_dwordx4 v1, s[80:83], s49 offen lds
	s_mov_b32 m0, s20
	s_nop 0
	buffer_load_dwordx4 v1, s[80:83], s50 offen lds
	s_waitcnt vmcnt(8)
	s_waitcnt lgkmcnt(0)
	s_barrier
	s_setprio 1
	s_waitcnt lgkmcnt(7)
	v_mfma_f32_16x16x32_bf16 v[62:65], v[106:109], v[174:177], v[62:65]
	v_mfma_f32_16x16x32_bf16 v[58:61], v[114:117], v[174:177], v[58:61]
	s_waitcnt lgkmcnt(5)
	v_mfma_f32_16x16x32_bf16 v[46:49], v[106:109], v[182:185], v[46:49]
	v_mfma_f32_16x16x32_bf16 v[42:45], v[114:117], v[182:185], v[42:45]
	s_waitcnt lgkmcnt(3)
	v_mfma_f32_16x16x32_bf16 v[30:33], v[106:109], v[190:193], v[30:33]
	v_mfma_f32_16x16x32_bf16 v[26:29], v[114:117], v[190:193], v[26:29]
	s_waitcnt lgkmcnt(1)
	v_mfma_f32_16x16x32_bf16 v[14:17], v[106:109], v[198:201], v[14:17]
	v_mfma_f32_16x16x32_bf16 v[10:13], v[114:117], v[198:201], v[10:13]
	v_mfma_f32_16x16x32_bf16 v[62:65], v[110:113], v[178:181], v[62:65]
	v_mfma_f32_16x16x32_bf16 v[58:61], v[122:125], v[178:181], v[58:61]
	v_mfma_f32_16x16x32_bf16 v[46:49], v[110:113], v[186:189], v[46:49]
	v_mfma_f32_16x16x32_bf16 v[42:45], v[122:125], v[186:189], v[42:45]
	v_mfma_f32_16x16x32_bf16 v[30:33], v[110:113], v[194:197], v[30:33]
	v_mfma_f32_16x16x32_bf16 v[26:29], v[122:125], v[194:197], v[26:29]
	s_waitcnt lgkmcnt(0)
	v_mfma_f32_16x16x32_bf16 v[14:17], v[110:113], v[202:205], v[14:17]
	v_mfma_f32_16x16x32_bf16 v[10:13], v[122:125], v[202:205], v[10:13]
	s_setprio 0
	s_setprio 1
	v_mfma_f32_16x16x32_bf16 v[54:57], v[150:153], v[174:177], v[54:57]
	v_mfma_f32_16x16x32_bf16 v[50:53], v[166:169], v[174:177], v[50:53]
	v_mfma_f32_16x16x32_bf16 v[38:41], v[150:153], v[182:185], v[38:41]
	v_mfma_f32_16x16x32_bf16 v[34:37], v[166:169], v[182:185], v[34:37]
	v_mfma_f32_16x16x32_bf16 v[22:25], v[150:153], v[190:193], v[22:25]
	v_mfma_f32_16x16x32_bf16 v[18:21], v[166:169], v[190:193], v[18:21]
	v_mfma_f32_16x16x32_bf16 v[6:9], v[150:153], v[198:201], v[6:9]
	v_mfma_f32_16x16x32_bf16 v[2:5], v[166:169], v[198:201], v[2:5]
	v_mfma_f32_16x16x32_bf16 v[54:57], v[162:165], v[178:181], v[54:57]
	v_mfma_f32_16x16x32_bf16 v[50:53], v[170:173], v[178:181], v[50:53]
	v_mfma_f32_16x16x32_bf16 v[38:41], v[162:165], v[186:189], v[38:41]
	v_mfma_f32_16x16x32_bf16 v[34:37], v[170:173], v[186:189], v[34:37]
	v_mfma_f32_16x16x32_bf16 v[22:25], v[162:165], v[194:197], v[22:25]
	v_mfma_f32_16x16x32_bf16 v[18:21], v[170:173], v[194:197], v[18:21]
	v_mfma_f32_16x16x32_bf16 v[6:9], v[162:165], v[202:205], v[6:9]
	v_mfma_f32_16x16x32_bf16 v[2:5], v[170:173], v[202:205], v[2:5]
	s_setprio 0
	s_barrier
; #define PG8_STAGE(bufoff, goff, voff) do { _Pragma("unroll") for (int _i = 0; _i < 2; ++_i) \
;         __builtin_amdgcn_raw_ptr_buffer_load_lds(rsrc, (PG8_LAS void*)(lds + (bufoff) + ldsw + _i * 8192), 16, (int)(voff), (int)((goff) + _i * p1##voff), 0, 0); } while (0)
; #define PG8_LDA(dst, b, h) do { _Pragma("unroll") for (int m = 0; m < 4; ++m) dst[m] = PG8_LD8(lds + PG8_SA(b, h) + aoff + m * 2048); } while (0)
; #define PG8_LDB(dst, b, h) do { _Pragma("unroll") for (int n = 0; n < 2; ++n) dst[n] = PG8_LD8(lds + PG8_SB(b, h) + boff + n * 2048); } while (0)
; #define PG8_WAIT_V(n) asm volatile("s_waitcnt vmcnt(" #n ")" ::: "memory")
; #define PG8_WAIT_L(n) asm volatile("s_waitcnt lgkmcnt(" #n ")" ::: "memory")
; #define PG8_BAR __builtin_amdgcn_s_barrier()
; #define PG8_SCHED __builtin_amdgcn_sched_barrier(0)
; template <class Epi, class Sched, bool ALIGN_EPI, bool F8 = false, int F8SC = F8_SCALES>
; __device__ __forceinline__ void gemm_phase(PG8_LAS unsigned char* lds, const __amdgpu_buffer_rsrc_t rsrc, const int lda, const int ldb, const int K, const Sched& S, const Epi& E) {
;     ...
;             PG8_LDB(B0, 1, 0); PG8_LDB(B1, 1, 1); PG8_SCHED; PG8_LDA(At, 1, 0); PG8_STAGE(PG8_SA(0, 1), a2 + hsA, voffA);
;             PG8_WAIT_V(8); PG8_WAIT_L(0); PG8_BAR; PG8_MMA(0, 0, At, B0); PG8_MMA(0, 1, At, B1); PG8_BAR; PG8_SCHED;
;             PG8_LDA(At, 1, 1); PG8_STAGE(PG8_SB(1, 0), b3, voffB); PG8_STAGE(PG8_SB(1, 1), b3 + hsB, voffB); PG8_STAGE(PG8_SA(1, 0), a3, voffA);
;             PG8_WAIT_V(8); PG8_WAIT_L(0); PG8_BAR; PG8_MMA(1, 0, At, B0); PG8_MMA(1, 1, At, B1); PG8_BAR; PG8_SCHED;
;         }
	ds_read_b128 v[106:109], v160
	ds_read_b128 v[110:113], v160 offset:1024
	ds_read_b128 v[114:117], v160 offset:2048
	ds_read_b128 v[122:125], v160 offset:3072
	ds_read_b128 v[150:153], v161
	ds_read_b128 v[162:165], v161 offset:1024
	ds_read_b128 v[166:169], v161 offset:2048
	ds_read_b128 v[170:173], v161 offset:3072
	s_mov_b32 m0, s21
	ds_read_b128 v[174:177], v159 offset:32768
	ds_read_b128 v[178:181], v159 offset:33792
	ds_read_b128 v[182:185], v159 offset:34816
	ds_read_b128 v[186:189], v159 offset:35840
	ds_read_b128 v[190:193], v159 offset:36864
	ds_read_b128 v[194:197], v159 offset:37888
	ds_read_b128 v[198:201], v159 offset:38912
	ds_read_b128 v[202:205], v159 offset:39936
	buffer_load_dwordx4 v1, s[80:83], s48 offen lds
	s_mov_b32 m0, s22
	s_nop 0
	buffer_load_dwordx4 v1, s[80:83], s47 offen lds
	s_waitcnt vmcnt(8)
	s_waitcnt lgkmcnt(0)
	s_barrier
	s_setprio 1
	s_waitcnt lgkmcnt(7)
	v_mfma_f32_16x16x32_bf16 v[142:145], v[106:109], v[174:177], v[142:145]
	v_mfma_f32_16x16x32_bf16 v[138:141], v[114:117], v[174:177], v[138:141]
	s_waitcnt lgkmcnt(5)
	v_mfma_f32_16x16x32_bf16 v[126:129], v[106:109], v[182:185], v[126:129]
	v_mfma_f32_16x16x32_bf16 v[118:121], v[114:117], v[182:185], v[118:121]
	s_waitcnt lgkmcnt(3)
	v_mfma_f32_16x16x32_bf16 v[94:97], v[106:109], v[190:193], v[94:97]
	v_mfma_f32_16x16x32_bf16 v[90:93], v[114:117], v[190:193], v[90:93]
	s_waitcnt lgkmcnt(1)
	v_mfma_f32_16x16x32_bf16 v[78:81], v[106:109], v[198:201], v[78:81]
	v_mfma_f32_16x16x32_bf16 v[74:77], v[114:117], v[198:201], v[74:77]
	v_mfma_f32_16x16x32_bf16 v[142:145], v[110:113], v[178:181], v[142:145]
	v_mfma_f32_16x16x32_bf16 v[138:141], v[122:125], v[178:181], v[138:141]
	v_mfma_f32_16x16x32_bf16 v[126:129], v[110:113], v[186:189], v[126:129]
	v_mfma_f32_16x16x32_bf16 v[118:121], v[122:125], v[186:189], v[118:121]
	v_mfma_f32_16x16x32_bf16 v[94:97], v[110:113], v[194:197], v[94:97]
	v_mfma_f32_16x16x32_bf16 v[90:93], v[122:125], v[194:197], v[90:93]
	s_waitcnt lgkmcnt(0)
	v_mfma_f32_16x16x32_bf16 v[78:81], v[110:113], v[202:205], v[78:81]
	v_mfma_f32_16x16x32_bf16 v[74:77], v[122:125], v[202:205], v[74:77]
	s_setprio 0
	s_setprio 1
	v_mfma_f32_16x16x32_bf16 v[134:137], v[150:153], v[174:177], v[134:137]
	v_mfma_f32_16x16x32_bf16 v[130:133], v[166:169], v[174:177], v[130:133]
	v_mfma_f32_16x16x32_bf16 v[102:105], v[150:153], v[182:185], v[102:105]
	v_mfma_f32_16x16x32_bf16 v[98:101], v[166:169], v[182:185], v[98:101]
	v_mfma_f32_16x16x32_bf16 v[86:89], v[150:153], v[190:193], v[86:89]
	v_mfma_f32_16x16x32_bf16 v[82:85], v[166:169], v[190:193], v[82:85]
	v_mfma_f32_16x16x32_bf16 v[70:73], v[150:153], v[198:201], v[70:73]
	v_mfma_f32_16x16x32_bf16 v[66:69], v[166:169], v[198:201], v[66:69]
	v_mfma_f32_16x16x32_bf16 v[134:137], v[162:165], v[178:181], v[134:137]
	v_mfma_f32_16x16x32_bf16 v[130:133], v[170:173], v[178:181], v[130:133]
	v_mfma_f32_16x16x32_bf16 v[102:105], v[162:165], v[186:189], v[102:105]
	v_mfma_f32_16x16x32_bf16 v[98:101], v[170:173], v[186:189], v[98:101]
	v_mfma_f32_16x16x32_bf16 v[86:89], v[162:165], v[194:197], v[86:89]
	v_mfma_f32_16x16x32_bf16 v[82:85], v[170:173], v[194:197], v[82:85]
	v_mfma_f32_16x16x32_bf16 v[70:73], v[162:165], v[202:205], v[70:73]
	v_mfma_f32_16x16x32_bf16 v[66:69], v[170:173], v[202:205], v[66:69]
	s_setprio 0
	s_barrier
	s_mov_b32 m0, s24
	ds_read_b128 v[174:177], v159 offset:49152
	ds_read_b128 v[178:181], v159 offset:50176
	ds_read_b128 v[182:185], v159 offset:51200
	ds_read_b128 v[186:189], v159 offset:52224
	ds_read_b128 v[190:193], v159 offset:53248
	ds_read_b128 v[194:197], v159 offset:54272
	ds_read_b128 v[198:201], v159 offset:55296
	ds_read_b128 v[202:205], v159 offset:56320
	buffer_load_dwordx4 v156, s[80:83], s46 offen lds
	s_mov_b32 m0, s25
	s_nop 0
	buffer_load_dwordx4 v156, s[80:83], s45 offen lds
	s_mov_b32 m0, s28
	s_nop 0
	buffer_load_dwordx4 v156, s[80:83], s43 offen lds
	s_mov_b32 m0, s29
	s_nop 0
	buffer_load_dwordx4 v156, s[80:83], s13 offen lds
	s_mov_b32 m0, s26
	s_nop 0
	buffer_load_dwordx4 v1, s[80:83], s44 offen lds
	s_mov_b32 m0, s27
	s_nop 0
	buffer_load_dwordx4 v1, s[80:83], s12 offen lds
	s_waitcnt vmcnt(8)
	s_waitcnt lgkmcnt(0)
	s_barrier
	s_setprio 1
	s_waitcnt lgkmcnt(7)
	v_mfma_f32_16x16x32_bf16 v[62:65], v[106:109], v[174:177], v[62:65]
	v_mfma_f32_16x16x32_bf16 v[58:61], v[114:117], v[174:177], v[58:61]
	s_waitcnt lgkmcnt(5)
	v_mfma_f32_16x16x32_bf16 v[46:49], v[106:109], v[182:185], v[46:49]
	v_mfma_f32_16x16x32_bf16 v[42:45], v[114:117], v[182:185], v[42:45]
	s_waitcnt lgkmcnt(3)
	v_mfma_f32_16x16x32_bf16 v[30:33], v[106:109], v[190:193], v[30:33]
	v_mfma_f32_16x16x32_bf16 v[26:29], v[114:117], v[190:193], v[26:29]
	s_waitcnt lgkmcnt(1)
	v_mfma_f32_16x16x32_bf16 v[14:17], v[106:109], v[198:201], v[14:17]
	v_mfma_f32_16x16x32_bf16 v[10:13], v[114:117], v[198:201], v[10:13]
	v_mfma_f32_16x16x32_bf16 v[62:65], v[110:113], v[178:181], v[62:65]
	v_mfma_f32_16x16x32_bf16 v[58:61], v[122:125], v[178:181], v[58:61]
	v_mfma_f32_16x16x32_bf16 v[46:49], v[110:113], v[186:189], v[46:49]
	v_mfma_f32_16x16x32_bf16 v[42:45], v[122:125], v[186:189], v[42:45]
	v_mfma_f32_16x16x32_bf16 v[30:33], v[110:113], v[194:197], v[30:33]
	v_mfma_f32_16x16x32_bf16 v[26:29], v[122:125], v[194:197], v[26:29]
	s_waitcnt lgkmcnt(0)
	v_mfma_f32_16x16x32_bf16 v[14:17], v[110:113], v[202:205], v[14:17]
	v_mfma_f32_16x16x32_bf16 v[10:13], v[122:125], v[202:205], v[10:13]
	s_setprio 0
	s_setprio 1
	v_mfma_f32_16x16x32_bf16 v[54:57], v[150:153], v[174:177], v[54:57]
	v_mfma_f32_16x16x32_bf16 v[50:53], v[166:169], v[174:177], v[50:53]
	v_mfma_f32_16x16x32_bf16 v[38:41], v[150:153], v[182:185], v[38:41]
	v_mfma_f32_16x16x32_bf16 v[34:37], v[166:169], v[182:185], v[34:37]
	v_mfma_f32_16x16x32_bf16 v[22:25], v[150:153], v[190:193], v[22:25]
	v_mfma_f32_16x16x32_bf16 v[18:21], v[166:169], v[190:193], v[18:21]
	v_mfma_f32_16x16x32_bf16 v[6:9], v[150:153], v[198:201], v[6:9]
	v_mfma_f32_16x16x32_bf16 v[2:5], v[166:169], v[198:201], v[2:5]
	v_mfma_f32_16x16x32_bf16 v[54:57], v[162:165], v[178:181], v[54:57]
	v_mfma_f32_16x16x32_bf16 v[50:53], v[170:173], v[178:181], v[50:53]
	v_mfma_f32_16x16x32_bf16 v[38:41], v[162:165], v[186:189], v[38:41]
	v_mfma_f32_16x16x32_bf16 v[34:37], v[170:173], v[186:189], v[34:37]
	v_mfma_f32_16x16x32_bf16 v[22:25], v[162:165], v[194:197], v[22:25]
	v_mfma_f32_16x16x32_bf16 v[18:21], v[170:173], v[194:197], v[18:21]
	v_mfma_f32_16x16x32_bf16 v[6:9], v[162:165], v[202:205], v[6:9]
	v_mfma_f32_16x16x32_bf16 v[2:5], v[170:173], v[202:205], v[2:5]
	s_setprio 0
	s_barrier
	s_andn2_b64 vcc, exec, s[6:7]
	s_mov_b64 s[12:13], -1
	s_mov_b64 s[6:7], 0
	s_movk_i32 s43, 0x100
	s_cbranch_vccz .LBB0_995
; __device__ __forceinline__ float fsigmoid(float x) { return __builtin_amdgcn_rcpf(1.0f + __expf(-x)); }
; __device__ __forceinline__ u32x4 pack8(const f32x4& v0, const f32x4& v1) { u32x4 w; w.x = cvt_pk_bf16(v0[0], v0[1]); w.y = cvt_pk_bf16(v0[2], v0[3]); w.z = cvt_pk_bf16(v1[0], v1[1]); w.w = cvt_pk_bf16(v1[2], v1[3]); return w; }
; #define PG8_BAR __builtin_amdgcn_s_barrier()
; #define EPI_ROWLOOP _Pragma("unroll") for (int ai = 0; ai < 2; ++ai) _Pragma("unroll") for (int m = 0; m < 4; ++m)
; template <class Epi, class Sched, bool ALIGN_EPI, bool F8 = false, int F8SC = F8_SCALES>
; __device__ __forceinline__ void gemm_phase(PG8_LAS unsigned char* lds, const __amdgpu_buffer_rsrc_t rsrc, const int lda, const int ldb, const int K, const Sched& S, const Epi& E) {
;     ...
;         if constexpr (ALIGN_EPI) { if (wr == 0) PG8_BAR; }
;     __device__ __forceinline__ bool operator()(f32x4 (&acc)[2][2][4][2], const Unit& u, int wr, int wc, int fr, int fq) const {
;         const int row0 = u.pm * BM + wr * 64 + fr, col0 = u.pn * BM + wc * 32 + 8 * fq;
;         f32x4 pv[2][2];
; #pragma unroll
;         for (int bj = 0; bj < 2; ++bj)
; #pragma unroll
;             for (int n = 0; n < 2; ++n) pv[bj][n] = *(const f32x4*)(par + col0 + bj * HALF + 4 * n);
;         EPI_ROWLOOP { bf16_t* rowp = OUT + (size_t)(row0 + ai * HALF + m * 16) * RW + col0;
; #pragma unroll
;             for (int bj = 0; bj < 2; ++bj) { f32x4 v0 = acc[ai][bj][m][0] + pv[bj][0], v1 = acc[ai][bj][m][1] + pv[bj][1];
; #pragma unroll
;                 for (int j = 0; j < 4; ++j) { v0[j] = fsigmoid(v0[j]); v1[j] = fsigmoid(v1[j]); }
;                 *(u32x4*)(rowp + bj * HALF) = pack8(v0, v1); } }
.Lpeel_after_995:
	s_and_b64 vcc, exec, s[10:11]
	s_cbranch_vccz .LBB0_998
	s_barrier
.LBB0_998:
	v_mov_b32_e32 v152, v0
	s_lshl_b32 s7, s39, 8
	v_readfirstlane_b32 s6, v152
	s_lshr_b32 s12, s6, 1
	s_and_b32 s12, s12, 0x60
	s_or_b32 s7, s12, s7
	v_lshrrev_b32_e32 v106, 1, v152
	v_and_or_b32 v150, v106, 24, s7
	v_readlane_b32 s40, v254, 5
	v_ashrrev_i32_e32 v151, 31, v150
	v_readlane_b32 s52, v254, 17
	v_readlane_b32 s53, v254, 18
	s_ashr_i32 s6, s6, 2
	s_lshl_b32 s7, s38, 8
	v_lshl_add_u64 v[106:107], v[150:151], 2, s[52:53]
	global_load_dwordx4 v[122:125], v[106:107], off
	global_load_dwordx4 v[114:117], v[106:107], off offset:16
	global_load_dwordx4 v[110:113], v[106:107], off offset:512
	s_nop 0
	global_load_dwordx4 v[106:109], v[106:107], off offset:528
	s_andn2_b32 s6, s6, 63
	s_add_i32 s6, s6, s7
	v_and_or_b32 v152, v152, 15, s6
	v_ashrrev_i32_e32 v153, 31, v152
	v_lshlrev_b64 v[162:163], 11, v[152:153]
	v_lshlrev_b64 v[154:155], 1, v[150:151]
	v_lshl_add_u64 v[150:151], s[88:89], 0, v[162:163]
	v_lshl_add_u64 v[150:151], v[150:151], 0, v[154:155]
	s_mov_b64 s[6:7], 0x40000
	v_readlane_b32 s41, v254, 6
	v_readlane_b32 s42, v254, 7
	v_readlane_b32 s43, v254, 8
	v_readlane_b32 s44, v254, 9
	v_readlane_b32 s45, v254, 10
	v_readlane_b32 s46, v254, 11
	v_readlane_b32 s47, v254, 12
	v_readlane_b32 s48, v254, 13
	v_readlane_b32 s49, v254, 14
	v_readlane_b32 s50, v254, 15
	v_readlane_b32 s51, v254, 16
	v_readlane_b32 s54, v254, 19
	v_readlane_b32 s55, v254, 20
	s_waitcnt vmcnt(3)
	v_pk_add_f32 v[144:145], v[144:145], v[124:125]
	v_pk_add_f32 v[142:143], v[142:143], v[122:123]
	s_waitcnt vmcnt(2)
	v_pk_add_f32 v[140:141], v[140:141], v[116:117]
	v_pk_add_f32 v[138:139], v[138:139], v[114:115]
	s_waitcnt vmcnt(1)
	v_pk_add_f32 v[136:137], v[136:137], v[112:113]
	v_pk_add_f32 v[134:135], v[134:135], v[110:111]
	s_waitcnt vmcnt(0)
	v_pk_add_f32 v[132:133], v[132:133], v[108:109]
	v_pk_add_f32 v[130:131], v[130:131], v[106:107]
	v_mul_f32_e32 v142, 0xbfb8aa3b, v142
	v_mul_f32_e32 v138, 0xbfb8aa3b, v138
	v_mul_f32_e32 v143, 0xbfb8aa3b, v143
	v_mul_f32_e32 v139, 0xbfb8aa3b, v139
	v_mul_f32_e32 v144, 0xbfb8aa3b, v144
	v_mul_f32_e32 v140, 0xbfb8aa3b, v140
	v_mul_f32_e32 v145, 0xbfb8aa3b, v145
	v_mul_f32_e32 v141, 0xbfb8aa3b, v141
	v_mul_f32_e32 v134, 0xbfb8aa3b, v134
	v_mul_f32_e32 v130, 0xbfb8aa3b, v130
	v_mul_f32_e32 v135, 0xbfb8aa3b, v135
	v_mul_f32_e32 v131, 0xbfb8aa3b, v131
	v_mul_f32_e32 v136, 0xbfb8aa3b, v136
	v_mul_f32_e32 v132, 0xbfb8aa3b, v132
	v_mul_f32_e32 v137, 0xbfb8aa3b, v137
	v_mul_f32_e32 v133, 0xbfb8aa3b, v133
	v_exp_f32_e32 v142, v142
	v_exp_f32_e32 v138, v138
	v_exp_f32_e32 v143, v143
	v_exp_f32_e32 v139, v139
	v_exp_f32_e32 v144, v144
	v_exp_f32_e32 v140, v140
	v_exp_f32_e32 v145, v145
	v_exp_f32_e32 v141, v141
	v_exp_f32_e32 v134, v134
	v_exp_f32_e32 v130, v130
	v_exp_f32_e32 v135, v135
	v_exp_f32_e32 v131, v131
	v_exp_f32_e32 v136, v136
	v_exp_f32_e32 v132, v132
	v_exp_f32_e32 v137, v137
	v_exp_f32_e32 v133, v133
	v_add_f32_e32 v142, 1.0, v142
	v_add_f32_e32 v138, 1.0, v138
	v_add_f32_e32 v143, 1.0, v143
	v_add_f32_e32 v139, 1.0, v139
	v_add_f32_e32 v144, 1.0, v144
	v_add_f32_e32 v140, 1.0, v140
	v_add_f32_e32 v145, 1.0, v145
	v_add_f32_e32 v141, 1.0, v141
	v_pk_add_f32 v[118:119], v[118:119], v[114:115]
	v_add_f32_e32 v134, 1.0, v134
	v_add_f32_e32 v130, 1.0, v130
	v_add_f32_e32 v135, 1.0, v135
	v_add_f32_e32 v131, 1.0, v131
	v_add_f32_e32 v136, 1.0, v136
	v_add_f32_e32 v132, 1.0, v132
	v_add_f32_e32 v137, 1.0, v137
	v_add_f32_e32 v133, 1.0, v133
	v_rcp_f32_e32 v142, v142
	v_rcp_f32_e32 v138, v138
	v_rcp_f32_e32 v143, v143
	v_rcp_f32_e32 v139, v139
	v_rcp_f32_e32 v144, v144
	v_rcp_f32_e32 v140, v140
	v_rcp_f32_e32 v145, v145
	v_rcp_f32_e32 v141, v141
	v_pk_add_f32 v[126:127], v[126:127], v[122:123]
	v_mul_f32_e32 v118, 0xbfb8aa3b, v118
	v_rcp_f32_e32 v134, v134
	v_rcp_f32_e32 v153, v130
	v_rcp_f32_e32 v135, v135
	v_rcp_f32_e32 v162, v131
	v_rcp_f32_e32 v136, v136
	v_rcp_f32_e32 v163, v132
	v_rcp_f32_e32 v137, v137
	v_rcp_f32_e32 v164, v133
	v_exp_f32_e32 v118, v118
	v_mul_f32_e32 v127, 0xbfb8aa3b, v127
	v_exp_f32_e32 v127, v127
	v_cvt_pk_bf16_f32 v130, v142, v143
	v_cvt_pk_bf16_f32 v131, v144, v145
	v_cvt_pk_bf16_f32 v132, v138, v139
	v_cvt_pk_bf16_f32 v133, v140, v141
	global_store_dwordx4 v[150:151], v[130:133], off
	v_pk_add_f32 v[128:129], v[128:129], v[124:125]
	v_add_f32_e32 v118, 1.0, v118
	v_cvt_pk_bf16_f32 v130, v134, v135
	v_cvt_pk_bf16_f32 v131, v136, v137
	v_cvt_pk_bf16_f32 v132, v153, v162
	v_cvt_pk_bf16_f32 v133, v163, v164
	v_mul_f32_e32 v119, 0xbfb8aa3b, v119
	global_store_dwordx4 v[150:151], v[130:133], off offset:256
	v_exp_f32_e32 v119, v119
	v_pk_add_f32 v[120:121], v[120:121], v[116:117]
	v_rcp_f32_e32 v132, v118
	v_add_f32_e32 v118, 1.0, v127
	v_mul_f32_e32 v127, 0xbfb8aa3b, v128
	v_exp_f32_e32 v127, v127
	v_add_f32_e32 v119, 1.0, v119
	v_mul_f32_e32 v120, 0xbfb8aa3b, v120
	v_mul_f32_e32 v126, 0xbfb8aa3b, v126
	v_exp_f32_e32 v120, v120
	v_rcp_f32_e32 v128, v119
	v_add_f32_e32 v119, 1.0, v127
	v_mul_f32_e32 v127, 0xbfb8aa3b, v129
	v_mul_f32_e32 v121, 0xbfb8aa3b, v121
	v_exp_f32_e32 v126, v126
	v_exp_f32_e32 v127, v127
	v_exp_f32_e32 v121, v121
	v_add_f32_e32 v120, 1.0, v120
	v_pk_add_f32 v[98:99], v[98:99], v[106:107]
	v_add_f32_e32 v126, 1.0, v126
	v_rcp_f32_e32 v129, v120
	v_add_f32_e32 v120, 1.0, v127
	v_add_f32_e32 v121, 1.0, v121
	v_pk_add_f32 v[102:103], v[102:103], v[110:111]
	v_mul_f32_e32 v98, 0xbfb8aa3b, v98
	v_or_b32_e32 v130, 16, v152
	v_rcp_f32_e32 v126, v126
	v_rcp_f32_e32 v118, v118
	v_rcp_f32_e32 v119, v119
	v_rcp_f32_e32 v120, v120
	v_rcp_f32_e32 v121, v121
	v_exp_f32_e32 v98, v98
; __device__ __forceinline__ float fsigmoid(float x) { return __builtin_amdgcn_rcpf(1.0f + __expf(-x)); }
; __device__ __forceinline__ u32x4 pack8(const f32x4& v0, const f32x4& v1) { u32x4 w; w.x = cvt_pk_bf16(v0[0], v0[1]); w.y = cvt_pk_bf16(v0[2], v0[3]); w.z = cvt_pk_bf16(v1[0], v1[1]); w.w = cvt_pk_bf16(v1[2], v1[3]); return w; }
; #define EPI_ROWLOOP _Pragma("unroll") for (int ai = 0; ai < 2; ++ai) _Pragma("unroll") for (int m = 0; m < 4; ++m)
;     __device__ __forceinline__ bool operator()(f32x4 (&acc)[2][2][4][2], const Unit& u, int wr, int wc, int fr, int fq) const {
;     ...
;         EPI_ROWLOOP { bf16_t* rowp = OUT + (size_t)(row0 + ai * HALF + m * 16) * RW + col0;
; #pragma unroll
;             for (int bj = 0; bj < 2; ++bj) { f32x4 v0 = acc[ai][bj][m][0] + pv[bj][0], v1 = acc[ai][bj][m][1] + pv[bj][1];
; #pragma unroll
;                 for (int j = 0; j < 4; ++j) { v0[j] = fsigmoid(v0[j]); v1[j] = fsigmoid(v1[j]); }
;                 *(u32x4*)(rowp + bj * HALF) = pack8(v0, v1); } }
	v_mul_f32_e32 v103, 0xbfb8aa3b, v103
	v_ashrrev_i32_e32 v131, 31, v130
	v_exp_f32_e32 v103, v103
	v_lshlrev_b64 v[130:131], 11, v[130:131]
	v_lshl_add_u64 v[130:131], s[88:89], 0, v[130:131]
	v_lshl_add_u64 v[130:131], v[130:131], 0, v[154:155]
	v_cvt_pk_bf16_f32 v118, v126, v118
	v_cvt_pk_bf16_f32 v119, v119, v120
	v_cvt_pk_bf16_f32 v120, v132, v128
	v_cvt_pk_bf16_f32 v121, v129, v121
	v_pk_add_f32 v[104:105], v[104:105], v[112:113]
	v_add_f32_e32 v98, 1.0, v98
	v_mul_f32_e32 v99, 0xbfb8aa3b, v99
	global_store_dwordx4 v[130:131], v[118:121], off
	v_exp_f32_e32 v99, v99
	v_pk_add_f32 v[100:101], v[100:101], v[108:109]
	v_rcp_f32_e32 v118, v98
	v_add_f32_e32 v98, 1.0, v103
	v_mul_f32_e32 v103, 0xbfb8aa3b, v104
	v_exp_f32_e32 v103, v103
	v_add_f32_e32 v99, 1.0, v99
	v_mul_f32_e32 v100, 0xbfb8aa3b, v100
	v_mul_f32_e32 v102, 0xbfb8aa3b, v102
	v_exp_f32_e32 v100, v100
	v_rcp_f32_e32 v104, v99
	v_add_f32_e32 v99, 1.0, v103
	v_mul_f32_e32 v103, 0xbfb8aa3b, v105
	v_mul_f32_e32 v101, 0xbfb8aa3b, v101
	v_exp_f32_e32 v102, v102
	v_exp_f32_e32 v103, v103
	v_exp_f32_e32 v101, v101
	v_add_f32_e32 v100, 1.0, v100
	v_pk_add_f32 v[90:91], v[90:91], v[114:115]
	v_add_f32_e32 v102, 1.0, v102
	v_rcp_f32_e32 v105, v100
	v_add_f32_e32 v100, 1.0, v103
	v_add_f32_e32 v101, 1.0, v101
	v_pk_add_f32 v[94:95], v[94:95], v[122:123]
	v_mul_f32_e32 v90, 0xbfb8aa3b, v90
	v_rcp_f32_e32 v102, v102
	v_rcp_f32_e32 v98, v98
	v_rcp_f32_e32 v99, v99
	v_rcp_f32_e32 v100, v100
	v_rcp_f32_e32 v101, v101
	v_exp_f32_e32 v90, v90
	v_mul_f32_e32 v95, 0xbfb8aa3b, v95
	v_exp_f32_e32 v95, v95
	v_cvt_pk_bf16_f32 v98, v102, v98
	v_cvt_pk_bf16_f32 v99, v99, v100
	v_cvt_pk_bf16_f32 v100, v118, v104
	v_cvt_pk_bf16_f32 v101, v105, v101
	v_pk_add_f32 v[96:97], v[96:97], v[124:125]
	v_add_f32_e32 v90, 1.0, v90
	v_mul_f32_e32 v91, 0xbfb8aa3b, v91
	global_store_dwordx4 v[130:131], v[98:101], off offset:256
	v_exp_f32_e32 v91, v91
	v_pk_add_f32 v[92:93], v[92:93], v[116:117]
	v_rcp_f32_e32 v100, v90
	v_add_f32_e32 v90, 1.0, v95
	v_mul_f32_e32 v95, 0xbfb8aa3b, v96
	v_exp_f32_e32 v95, v95
	v_add_f32_e32 v91, 1.0, v91
	v_mul_f32_e32 v92, 0xbfb8aa3b, v92
	v_mul_f32_e32 v94, 0xbfb8aa3b, v94
	v_exp_f32_e32 v92, v92
	v_rcp_f32_e32 v96, v91
	v_add_f32_e32 v91, 1.0, v95
	v_mul_f32_e32 v95, 0xbfb8aa3b, v97
	v_mul_f32_e32 v93, 0xbfb8aa3b, v93
	v_exp_f32_e32 v94, v94
	v_exp_f32_e32 v95, v95
	v_exp_f32_e32 v93, v93
	v_add_f32_e32 v92, 1.0, v92
	v_pk_add_f32 v[82:83], v[82:83], v[106:107]
	v_add_f32_e32 v94, 1.0, v94
	v_rcp_f32_e32 v97, v92
	v_add_f32_e32 v92, 1.0, v95
	v_add_f32_e32 v93, 1.0, v93
	v_pk_add_f32 v[86:87], v[86:87], v[110:111]
	v_mul_f32_e32 v82, 0xbfb8aa3b, v82
	v_or_b32_e32 v98, 32, v152
	v_rcp_f32_e32 v94, v94
	v_rcp_f32_e32 v90, v90
	v_rcp_f32_e32 v91, v91
	v_rcp_f32_e32 v92, v92
	v_rcp_f32_e32 v93, v93
	v_exp_f32_e32 v82, v82
	v_mul_f32_e32 v87, 0xbfb8aa3b, v87
	v_ashrrev_i32_e32 v99, 31, v98
	v_exp_f32_e32 v87, v87
	v_lshlrev_b64 v[98:99], 11, v[98:99]
	v_lshl_add_u64 v[98:99], s[88:89], 0, v[98:99]
	v_lshl_add_u64 v[98:99], v[98:99], 0, v[154:155]
	v_cvt_pk_bf16_f32 v90, v94, v90
	v_cvt_pk_bf16_f32 v91, v91, v92
	v_cvt_pk_bf16_f32 v92, v100, v96
	v_cvt_pk_bf16_f32 v93, v97, v93
	v_pk_add_f32 v[88:89], v[88:89], v[112:113]
	v_add_f32_e32 v82, 1.0, v82
	v_mul_f32_e32 v83, 0xbfb8aa3b, v83
	global_store_dwordx4 v[98:99], v[90:93], off
	v_exp_f32_e32 v83, v83
	v_pk_add_f32 v[84:85], v[84:85], v[108:109]
	v_rcp_f32_e32 v90, v82
	v_add_f32_e32 v82, 1.0, v87
	v_mul_f32_e32 v87, 0xbfb8aa3b, v88
	v_exp_f32_e32 v87, v87
	v_add_f32_e32 v83, 1.0, v83
	v_mul_f32_e32 v84, 0xbfb8aa3b, v84
	v_mul_f32_e32 v86, 0xbfb8aa3b, v86
	v_exp_f32_e32 v84, v84
	v_rcp_f32_e32 v88, v83
	v_add_f32_e32 v83, 1.0, v87
	v_mul_f32_e32 v87, 0xbfb8aa3b, v89
	v_mul_f32_e32 v85, 0xbfb8aa3b, v85
	v_exp_f32_e32 v86, v86
	v_exp_f32_e32 v87, v87
	v_exp_f32_e32 v85, v85
	v_add_f32_e32 v84, 1.0, v84
	v_pk_add_f32 v[74:75], v[74:75], v[114:115]
	v_add_f32_e32 v86, 1.0, v86
	v_rcp_f32_e32 v89, v84
	v_add_f32_e32 v84, 1.0, v87
	v_add_f32_e32 v85, 1.0, v85
	v_pk_add_f32 v[78:79], v[78:79], v[122:123]
	v_mul_f32_e32 v74, 0xbfb8aa3b, v74
	v_rcp_f32_e32 v86, v86
	v_rcp_f32_e32 v82, v82
	v_rcp_f32_e32 v83, v83
	v_rcp_f32_e32 v84, v84
	v_rcp_f32_e32 v85, v85
	v_exp_f32_e32 v74, v74
	v_mul_f32_e32 v79, 0xbfb8aa3b, v79
	v_exp_f32_e32 v79, v79
	v_cvt_pk_bf16_f32 v82, v86, v82
	v_cvt_pk_bf16_f32 v83, v83, v84
	v_cvt_pk_bf16_f32 v84, v90, v88
	v_cvt_pk_bf16_f32 v85, v89, v85
	v_pk_add_f32 v[80:81], v[80:81], v[124:125]
	v_add_f32_e32 v74, 1.0, v74
	v_mul_f32_e32 v75, 0xbfb8aa3b, v75
	global_store_dwordx4 v[98:99], v[82:85], off offset:256
	v_exp_f32_e32 v75, v75
	v_pk_add_f32 v[76:77], v[76:77], v[116:117]
	v_rcp_f32_e32 v84, v74
	v_add_f32_e32 v74, 1.0, v79
	v_mul_f32_e32 v79, 0xbfb8aa3b, v80
	v_exp_f32_e32 v79, v79
	v_add_f32_e32 v75, 1.0, v75
	v_mul_f32_e32 v76, 0xbfb8aa3b, v76
	v_mul_f32_e32 v78, 0xbfb8aa3b, v78
	v_exp_f32_e32 v76, v76
	v_rcp_f32_e32 v80, v75
	v_add_f32_e32 v75, 1.0, v79
	v_mul_f32_e32 v79, 0xbfb8aa3b, v81
	v_mul_f32_e32 v77, 0xbfb8aa3b, v77
	v_exp_f32_e32 v78, v78
	v_exp_f32_e32 v79, v79
	v_exp_f32_e32 v77, v77
	v_add_f32_e32 v76, 1.0, v76
	v_pk_add_f32 v[66:67], v[66:67], v[106:107]
	v_add_f32_e32 v78, 1.0, v78
	v_rcp_f32_e32 v81, v76
	v_add_f32_e32 v76, 1.0, v79
	v_add_f32_e32 v77, 1.0, v77
	v_pk_add_f32 v[70:71], v[70:71], v[110:111]
	v_mul_f32_e32 v66, 0xbfb8aa3b, v66
	v_or_b32_e32 v82, 48, v152
	v_rcp_f32_e32 v78, v78
	v_rcp_f32_e32 v74, v74
	v_rcp_f32_e32 v75, v75
	v_rcp_f32_e32 v76, v76
	v_rcp_f32_e32 v77, v77
	v_exp_f32_e32 v66, v66
	v_mul_f32_e32 v71, 0xbfb8aa3b, v71
	v_ashrrev_i32_e32 v83, 31, v82
	v_exp_f32_e32 v71, v71
; __device__ __forceinline__ float fsigmoid(float x) { return __builtin_amdgcn_rcpf(1.0f + __expf(-x)); }
; __device__ __forceinline__ u32x4 pack8(const f32x4& v0, const f32x4& v1) { u32x4 w; w.x = cvt_pk_bf16(v0[0], v0[1]); w.y = cvt_pk_bf16(v0[2], v0[3]); w.z = cvt_pk_bf16(v1[0], v1[1]); w.w = cvt_pk_bf16(v1[2], v1[3]); return w; }
; #define EPI_ROWLOOP _Pragma("unroll") for (int ai = 0; ai < 2; ++ai) _Pragma("unroll") for (int m = 0; m < 4; ++m)
;     __device__ __forceinline__ bool operator()(f32x4 (&acc)[2][2][4][2], const Unit& u, int wr, int wc, int fr, int fq) const {
;     ...
;         EPI_ROWLOOP { bf16_t* rowp = OUT + (size_t)(row0 + ai * HALF + m * 16) * RW + col0;
; #pragma unroll
;             for (int bj = 0; bj < 2; ++bj) { f32x4 v0 = acc[ai][bj][m][0] + pv[bj][0], v1 = acc[ai][bj][m][1] + pv[bj][1];
; #pragma unroll
;                 for (int j = 0; j < 4; ++j) { v0[j] = fsigmoid(v0[j]); v1[j] = fsigmoid(v1[j]); }
;                 *(u32x4*)(rowp + bj * HALF) = pack8(v0, v1); } }
	v_lshlrev_b64 v[82:83], 11, v[82:83]
	v_lshl_add_u64 v[82:83], s[88:89], 0, v[82:83]
	v_lshl_add_u64 v[82:83], v[82:83], 0, v[154:155]
	v_cvt_pk_bf16_f32 v74, v78, v74
	v_cvt_pk_bf16_f32 v75, v75, v76
	v_cvt_pk_bf16_f32 v76, v84, v80
	v_cvt_pk_bf16_f32 v77, v81, v77
	v_pk_add_f32 v[72:73], v[72:73], v[112:113]
	v_add_f32_e32 v66, 1.0, v66
	v_mul_f32_e32 v67, 0xbfb8aa3b, v67
	global_store_dwordx4 v[82:83], v[74:77], off
	v_exp_f32_e32 v67, v67
	v_pk_add_f32 v[68:69], v[68:69], v[108:109]
	v_rcp_f32_e32 v74, v66
	v_add_f32_e32 v66, 1.0, v71
	v_mul_f32_e32 v71, 0xbfb8aa3b, v72
	v_exp_f32_e32 v71, v71
	v_add_f32_e32 v67, 1.0, v67
	v_mul_f32_e32 v68, 0xbfb8aa3b, v68
	v_mul_f32_e32 v70, 0xbfb8aa3b, v70
	v_exp_f32_e32 v68, v68
	v_rcp_f32_e32 v72, v67
	v_add_f32_e32 v67, 1.0, v71
	v_mul_f32_e32 v71, 0xbfb8aa3b, v73
	v_mul_f32_e32 v69, 0xbfb8aa3b, v69
	v_exp_f32_e32 v70, v70
	v_exp_f32_e32 v71, v71
	v_exp_f32_e32 v69, v69
	v_add_f32_e32 v68, 1.0, v68
	v_pk_add_f32 v[58:59], v[58:59], v[114:115]
	v_add_f32_e32 v70, 1.0, v70
	v_rcp_f32_e32 v73, v68
	v_add_f32_e32 v68, 1.0, v71
	v_add_f32_e32 v69, 1.0, v69
	v_pk_add_f32 v[62:63], v[62:63], v[122:123]
	v_mul_f32_e32 v58, 0xbfb8aa3b, v58
	v_rcp_f32_e32 v70, v70
	v_rcp_f32_e32 v66, v66
	v_rcp_f32_e32 v67, v67
	v_rcp_f32_e32 v68, v68
	v_rcp_f32_e32 v69, v69
	v_exp_f32_e32 v58, v58
	v_mul_f32_e32 v63, 0xbfb8aa3b, v63
	v_exp_f32_e32 v63, v63
	v_cvt_pk_bf16_f32 v66, v70, v66
	v_cvt_pk_bf16_f32 v67, v67, v68
	v_cvt_pk_bf16_f32 v68, v74, v72
	v_cvt_pk_bf16_f32 v69, v73, v69
	v_pk_add_f32 v[64:65], v[64:65], v[124:125]
	v_add_f32_e32 v58, 1.0, v58
	v_mul_f32_e32 v59, 0xbfb8aa3b, v59
	global_store_dwordx4 v[82:83], v[66:69], off offset:256
	v_exp_f32_e32 v59, v59
	v_pk_add_f32 v[60:61], v[60:61], v[116:117]
	v_rcp_f32_e32 v68, v58
	v_add_f32_e32 v58, 1.0, v63
	v_mul_f32_e32 v63, 0xbfb8aa3b, v64
	v_exp_f32_e32 v63, v63
	v_mul_f32_e32 v62, 0xbfb8aa3b, v62
	v_add_f32_e32 v59, 1.0, v59
	v_mul_f32_e32 v60, 0xbfb8aa3b, v60
	v_exp_f32_e32 v62, v62
	v_exp_f32_e32 v60, v60
	v_rcp_f32_e32 v64, v59
	v_add_f32_e32 v59, 1.0, v63
	v_mul_f32_e32 v63, 0xbfb8aa3b, v65
	v_mul_f32_e32 v61, 0xbfb8aa3b, v61
	v_exp_f32_e32 v63, v63
	v_exp_f32_e32 v61, v61
	v_add_f32_e32 v62, 1.0, v62
	v_add_f32_e32 v60, 1.0, v60
	v_pk_add_f32 v[50:51], v[50:51], v[106:107]
	v_rcp_f32_e32 v62, v62
	v_rcp_f32_e32 v58, v58
	v_rcp_f32_e32 v65, v60
	v_add_f32_e32 v60, 1.0, v63
	v_add_f32_e32 v61, 1.0, v61
	v_pk_add_f32 v[54:55], v[54:55], v[110:111]
	v_mul_f32_e32 v50, 0xbfb8aa3b, v50
	v_rcp_f32_e32 v59, v59
	v_rcp_f32_e32 v60, v60
	v_rcp_f32_e32 v61, v61
	v_exp_f32_e32 v50, v50
	v_mul_f32_e32 v55, 0xbfb8aa3b, v55
	v_exp_f32_e32 v55, v55
	v_lshl_add_u64 v[66:67], v[150:151], 0, s[6:7]
	s_mov_b32 s6, 0x40000
	v_cvt_pk_bf16_f32 v58, v62, v58
	v_add_co_u32_e32 v62, vcc, s6, v150
	v_cvt_pk_bf16_f32 v59, v59, v60
	v_cvt_pk_bf16_f32 v60, v68, v64
	v_cvt_pk_bf16_f32 v61, v65, v61
	v_addc_co_u32_e32 v63, vcc, 0, v151, vcc
	v_pk_add_f32 v[56:57], v[56:57], v[112:113]
	v_add_f32_e32 v50, 1.0, v50
	v_mul_f32_e32 v51, 0xbfb8aa3b, v51
	global_store_dwordx4 v[62:63], v[58:61], off
	v_exp_f32_e32 v51, v51
	v_pk_add_f32 v[52:53], v[52:53], v[108:109]
	v_rcp_f32_e32 v58, v50
	v_add_f32_e32 v50, 1.0, v55
	v_mul_f32_e32 v55, 0xbfb8aa3b, v56
	v_exp_f32_e32 v55, v55
	v_add_f32_e32 v51, 1.0, v51
	v_mul_f32_e32 v52, 0xbfb8aa3b, v52
	v_mul_f32_e32 v54, 0xbfb8aa3b, v54
	v_exp_f32_e32 v52, v52
	v_rcp_f32_e32 v56, v51
	v_add_f32_e32 v51, 1.0, v55
	v_mul_f32_e32 v55, 0xbfb8aa3b, v57
	v_mul_f32_e32 v53, 0xbfb8aa3b, v53
	v_exp_f32_e32 v54, v54
	v_exp_f32_e32 v55, v55
	v_exp_f32_e32 v53, v53
	v_add_f32_e32 v52, 1.0, v52
	v_pk_add_f32 v[42:43], v[42:43], v[114:115]
	v_add_f32_e32 v54, 1.0, v54
	v_rcp_f32_e32 v57, v52
	v_add_f32_e32 v52, 1.0, v55
	v_add_f32_e32 v53, 1.0, v53
	v_pk_add_f32 v[46:47], v[46:47], v[122:123]
	v_mul_f32_e32 v42, 0xbfb8aa3b, v42
	v_rcp_f32_e32 v54, v54
	v_rcp_f32_e32 v50, v50
	v_rcp_f32_e32 v51, v51
	v_rcp_f32_e32 v52, v52
	v_rcp_f32_e32 v53, v53
	v_exp_f32_e32 v42, v42
	v_mul_f32_e32 v47, 0xbfb8aa3b, v47
	v_exp_f32_e32 v47, v47
	v_cvt_pk_bf16_f32 v50, v54, v50
	v_cvt_pk_bf16_f32 v51, v51, v52
	v_cvt_pk_bf16_f32 v52, v58, v56
	v_cvt_pk_bf16_f32 v53, v57, v53
	v_pk_add_f32 v[48:49], v[48:49], v[124:125]
	v_add_f32_e32 v42, 1.0, v42
	v_mul_f32_e32 v43, 0xbfb8aa3b, v43
	global_store_dwordx4 v[66:67], v[50:53], off offset:256
	v_exp_f32_e32 v43, v43
	v_pk_add_f32 v[44:45], v[44:45], v[116:117]
	v_rcp_f32_e32 v52, v42
	v_add_f32_e32 v42, 1.0, v47
	v_mul_f32_e32 v47, 0xbfb8aa3b, v48
	v_exp_f32_e32 v47, v47
	v_mul_f32_e32 v46, 0xbfb8aa3b, v46
	v_add_f32_e32 v43, 1.0, v43
	v_mul_f32_e32 v44, 0xbfb8aa3b, v44
	v_exp_f32_e32 v46, v46
	v_exp_f32_e32 v44, v44
	v_rcp_f32_e32 v48, v43
	v_add_f32_e32 v43, 1.0, v47
	v_mul_f32_e32 v47, 0xbfb8aa3b, v49
	v_mul_f32_e32 v45, 0xbfb8aa3b, v45
	v_exp_f32_e32 v47, v47
	v_exp_f32_e32 v45, v45
	v_add_f32_e32 v46, 1.0, v46
	v_add_f32_e32 v44, 1.0, v44
	v_pk_add_f32 v[34:35], v[34:35], v[106:107]
	v_rcp_f32_e32 v46, v46
	v_rcp_f32_e32 v42, v42
	v_rcp_f32_e32 v49, v44
	v_add_f32_e32 v44, 1.0, v47
	v_add_f32_e32 v45, 1.0, v45
	v_pk_add_f32 v[38:39], v[38:39], v[110:111]
	v_mul_f32_e32 v34, 0xbfb8aa3b, v34
	v_rcp_f32_e32 v43, v43
	v_rcp_f32_e32 v44, v44
	v_rcp_f32_e32 v45, v45
	v_exp_f32_e32 v34, v34
	v_mul_f32_e32 v39, 0xbfb8aa3b, v39
	s_mov_b64 s[6:7], 0x48000
	v_exp_f32_e32 v39, v39
	v_lshl_add_u64 v[50:51], v[150:151], 0, s[6:7]
	s_mov_b32 s6, 0x48000
	v_cvt_pk_bf16_f32 v42, v46, v42
	v_add_co_u32_e32 v46, vcc, s6, v150
	v_cvt_pk_bf16_f32 v43, v43, v44
	v_cvt_pk_bf16_f32 v44, v52, v48
	v_cvt_pk_bf16_f32 v45, v49, v45
; __device__ __forceinline__ float fsigmoid(float x) { return __builtin_amdgcn_rcpf(1.0f + __expf(-x)); }
; __device__ __forceinline__ u32x4 pack8(const f32x4& v0, const f32x4& v1) { u32x4 w; w.x = cvt_pk_bf16(v0[0], v0[1]); w.y = cvt_pk_bf16(v0[2], v0[3]); w.z = cvt_pk_bf16(v1[0], v1[1]); w.w = cvt_pk_bf16(v1[2], v1[3]); return w; }
; #define EPI_ROWLOOP _Pragma("unroll") for (int ai = 0; ai < 2; ++ai) _Pragma("unroll") for (int m = 0; m < 4; ++m)
;     __device__ __forceinline__ bool operator()(f32x4 (&acc)[2][2][4][2], const Unit& u, int wr, int wc, int fr, int fq) const {
;     ...
;         EPI_ROWLOOP { bf16_t* rowp = OUT + (size_t)(row0 + ai * HALF + m * 16) * RW + col0;
; #pragma unroll
;             for (int bj = 0; bj < 2; ++bj) { f32x4 v0 = acc[ai][bj][m][0] + pv[bj][0], v1 = acc[ai][bj][m][1] + pv[bj][1];
; #pragma unroll
;                 for (int j = 0; j < 4; ++j) { v0[j] = fsigmoid(v0[j]); v1[j] = fsigmoid(v1[j]); }
;                 *(u32x4*)(rowp + bj * HALF) = pack8(v0, v1); } }
	v_addc_co_u32_e32 v47, vcc, 0, v151, vcc
	v_pk_add_f32 v[40:41], v[40:41], v[112:113]
	v_add_f32_e32 v34, 1.0, v34
	v_mul_f32_e32 v35, 0xbfb8aa3b, v35
	global_store_dwordx4 v[46:47], v[42:45], off
	v_exp_f32_e32 v35, v35
	v_pk_add_f32 v[36:37], v[36:37], v[108:109]
	v_rcp_f32_e32 v42, v34
	v_add_f32_e32 v34, 1.0, v39
	v_mul_f32_e32 v39, 0xbfb8aa3b, v40
	v_exp_f32_e32 v39, v39
	v_add_f32_e32 v35, 1.0, v35
	v_mul_f32_e32 v36, 0xbfb8aa3b, v36
	v_mul_f32_e32 v38, 0xbfb8aa3b, v38
	v_exp_f32_e32 v36, v36
	v_rcp_f32_e32 v40, v35
	v_add_f32_e32 v35, 1.0, v39
	v_mul_f32_e32 v39, 0xbfb8aa3b, v41
	v_mul_f32_e32 v37, 0xbfb8aa3b, v37
	v_exp_f32_e32 v38, v38
	v_exp_f32_e32 v39, v39
	v_exp_f32_e32 v37, v37
	v_add_f32_e32 v36, 1.0, v36
	v_pk_add_f32 v[26:27], v[26:27], v[114:115]
	v_add_f32_e32 v38, 1.0, v38
	v_rcp_f32_e32 v41, v36
	v_add_f32_e32 v36, 1.0, v39
	v_add_f32_e32 v37, 1.0, v37
	v_pk_add_f32 v[30:31], v[30:31], v[122:123]
	v_mul_f32_e32 v26, 0xbfb8aa3b, v26
	v_rcp_f32_e32 v38, v38
	v_rcp_f32_e32 v34, v34
	v_rcp_f32_e32 v35, v35
	v_rcp_f32_e32 v36, v36
	v_rcp_f32_e32 v37, v37
	v_exp_f32_e32 v26, v26
	v_mul_f32_e32 v31, 0xbfb8aa3b, v31
	v_exp_f32_e32 v31, v31
	v_cvt_pk_bf16_f32 v34, v38, v34
	v_cvt_pk_bf16_f32 v35, v35, v36
	v_cvt_pk_bf16_f32 v36, v42, v40
	v_cvt_pk_bf16_f32 v37, v41, v37
	v_pk_add_f32 v[32:33], v[32:33], v[124:125]
	v_add_f32_e32 v26, 1.0, v26
	v_mul_f32_e32 v27, 0xbfb8aa3b, v27
	global_store_dwordx4 v[50:51], v[34:37], off offset:256
	v_exp_f32_e32 v27, v27
	v_pk_add_f32 v[28:29], v[28:29], v[116:117]
	v_rcp_f32_e32 v36, v26
	v_add_f32_e32 v26, 1.0, v31
	v_mul_f32_e32 v31, 0xbfb8aa3b, v32
	v_exp_f32_e32 v31, v31
	v_mul_f32_e32 v30, 0xbfb8aa3b, v30
	v_add_f32_e32 v27, 1.0, v27
	v_mul_f32_e32 v28, 0xbfb8aa3b, v28
	v_exp_f32_e32 v30, v30
	v_exp_f32_e32 v28, v28
	v_rcp_f32_e32 v32, v27
	v_add_f32_e32 v27, 1.0, v31
	v_mul_f32_e32 v31, 0xbfb8aa3b, v33
	v_mul_f32_e32 v29, 0xbfb8aa3b, v29
	v_exp_f32_e32 v31, v31
	v_exp_f32_e32 v29, v29
	v_add_f32_e32 v30, 1.0, v30
	v_add_f32_e32 v28, 1.0, v28
	v_pk_add_f32 v[18:19], v[18:19], v[106:107]
	v_rcp_f32_e32 v30, v30
	v_rcp_f32_e32 v26, v26
	v_rcp_f32_e32 v33, v28
	v_add_f32_e32 v28, 1.0, v31
	v_add_f32_e32 v29, 1.0, v29
	v_pk_add_f32 v[22:23], v[22:23], v[110:111]
	v_mul_f32_e32 v18, 0xbfb8aa3b, v18
	v_rcp_f32_e32 v27, v27
	v_rcp_f32_e32 v28, v28
	v_rcp_f32_e32 v29, v29
	v_exp_f32_e32 v18, v18
	v_mul_f32_e32 v23, 0xbfb8aa3b, v23
	s_mov_b64 s[6:7], 0x50000
	v_exp_f32_e32 v23, v23
	v_lshl_add_u64 v[34:35], v[150:151], 0, s[6:7]
	s_mov_b32 s6, 0x50000
	v_cvt_pk_bf16_f32 v26, v30, v26
	v_add_co_u32_e32 v30, vcc, s6, v150
	v_cvt_pk_bf16_f32 v27, v27, v28
	v_cvt_pk_bf16_f32 v28, v36, v32
	v_cvt_pk_bf16_f32 v29, v33, v29
	v_addc_co_u32_e32 v31, vcc, 0, v151, vcc
	v_pk_add_f32 v[24:25], v[24:25], v[112:113]
	v_add_f32_e32 v18, 1.0, v18
	v_mul_f32_e32 v19, 0xbfb8aa3b, v19
	global_store_dwordx4 v[30:31], v[26:29], off
	v_exp_f32_e32 v19, v19
	v_pk_add_f32 v[20:21], v[20:21], v[108:109]
	v_rcp_f32_e32 v26, v18
	v_add_f32_e32 v18, 1.0, v23
	v_mul_f32_e32 v23, 0xbfb8aa3b, v24
	v_exp_f32_e32 v23, v23
	v_add_f32_e32 v19, 1.0, v19
	v_mul_f32_e32 v20, 0xbfb8aa3b, v20
	v_mul_f32_e32 v22, 0xbfb8aa3b, v22
	v_exp_f32_e32 v20, v20
	v_rcp_f32_e32 v24, v19
	v_add_f32_e32 v19, 1.0, v23
	v_mul_f32_e32 v23, 0xbfb8aa3b, v25
	v_mul_f32_e32 v21, 0xbfb8aa3b, v21
	v_exp_f32_e32 v22, v22
	v_exp_f32_e32 v23, v23
	v_exp_f32_e32 v21, v21
	v_add_f32_e32 v20, 1.0, v20
	v_pk_add_f32 v[10:11], v[10:11], v[114:115]
	v_add_f32_e32 v22, 1.0, v22
	v_rcp_f32_e32 v25, v20
	v_add_f32_e32 v20, 1.0, v23
	v_add_f32_e32 v21, 1.0, v21
	v_pk_add_f32 v[14:15], v[14:15], v[122:123]
	v_mul_f32_e32 v10, 0xbfb8aa3b, v10
	v_rcp_f32_e32 v22, v22
	v_rcp_f32_e32 v18, v18
	v_rcp_f32_e32 v19, v19
	v_rcp_f32_e32 v20, v20
	v_rcp_f32_e32 v21, v21
	v_exp_f32_e32 v10, v10
	v_mul_f32_e32 v15, 0xbfb8aa3b, v15
	v_exp_f32_e32 v15, v15
	v_cvt_pk_bf16_f32 v18, v22, v18
	v_cvt_pk_bf16_f32 v19, v19, v20
	v_cvt_pk_bf16_f32 v20, v26, v24
	v_cvt_pk_bf16_f32 v21, v25, v21
	v_pk_add_f32 v[16:17], v[16:17], v[124:125]
	v_add_f32_e32 v10, 1.0, v10
	v_mul_f32_e32 v11, 0xbfb8aa3b, v11
	global_store_dwordx4 v[34:35], v[18:21], off offset:256
	v_exp_f32_e32 v11, v11
	v_pk_add_f32 v[12:13], v[12:13], v[116:117]
	v_rcp_f32_e32 v20, v10
	v_add_f32_e32 v10, 1.0, v15
	v_mul_f32_e32 v15, 0xbfb8aa3b, v16
	v_exp_f32_e32 v15, v15
	v_mul_f32_e32 v14, 0xbfb8aa3b, v14
	v_add_f32_e32 v11, 1.0, v11
	v_mul_f32_e32 v12, 0xbfb8aa3b, v12
	v_exp_f32_e32 v14, v14
	v_exp_f32_e32 v12, v12
	v_rcp_f32_e32 v16, v11
	v_add_f32_e32 v11, 1.0, v15
	v_mul_f32_e32 v15, 0xbfb8aa3b, v17
	v_mul_f32_e32 v13, 0xbfb8aa3b, v13
	v_exp_f32_e32 v15, v15
	v_exp_f32_e32 v13, v13
	v_add_f32_e32 v14, 1.0, v14
	v_add_f32_e32 v12, 1.0, v12
	v_pk_add_f32 v[2:3], v[2:3], v[106:107]
	v_rcp_f32_e32 v14, v14
	v_rcp_f32_e32 v10, v10
	v_rcp_f32_e32 v17, v12
	v_add_f32_e32 v12, 1.0, v15
	v_add_f32_e32 v13, 1.0, v13
	v_pk_add_f32 v[6:7], v[6:7], v[110:111]
	v_mul_f32_e32 v2, 0xbfb8aa3b, v2
	v_rcp_f32_e32 v11, v11
	v_rcp_f32_e32 v12, v12
	v_rcp_f32_e32 v13, v13
	v_exp_f32_e32 v2, v2
	v_mul_f32_e32 v7, 0xbfb8aa3b, v7
	s_mov_b64 s[6:7], 0x58000
	v_exp_f32_e32 v7, v7
	v_lshl_add_u64 v[18:19], v[150:151], 0, s[6:7]
	s_mov_b32 s6, 0x58000
	v_cvt_pk_bf16_f32 v10, v14, v10
	v_add_co_u32_e32 v14, vcc, s6, v150
	v_cvt_pk_bf16_f32 v11, v11, v12
	v_cvt_pk_bf16_f32 v12, v20, v16
	v_cvt_pk_bf16_f32 v13, v17, v13
	v_addc_co_u32_e32 v15, vcc, 0, v151, vcc
	v_pk_add_f32 v[8:9], v[8:9], v[112:113]
	v_add_f32_e32 v2, 1.0, v2
	v_mul_f32_e32 v3, 0xbfb8aa3b, v3
	global_store_dwordx4 v[14:15], v[10:13], off
	v_exp_f32_e32 v3, v3
	v_pk_add_f32 v[4:5], v[4:5], v[108:109]
	v_rcp_f32_e32 v10, v2
	v_add_f32_e32 v2, 1.0, v7
	v_mul_f32_e32 v7, 0xbfb8aa3b, v8
	v_exp_f32_e32 v7, v7
	v_add_f32_e32 v3, 1.0, v3
	v_mul_f32_e32 v4, 0xbfb8aa3b, v4
	v_mul_f32_e32 v6, 0xbfb8aa3b, v6
	v_exp_f32_e32 v4, v4
	v_rcp_f32_e32 v8, v3
	v_add_f32_e32 v3, 1.0, v7
	v_mul_f32_e32 v7, 0xbfb8aa3b, v9
	v_mul_f32_e32 v5, 0xbfb8aa3b, v5
	v_exp_f32_e32 v6, v6
	v_exp_f32_e32 v7, v7
	v_exp_f32_e32 v5, v5
	v_add_f32_e32 v4, 1.0, v4
	v_add_f32_e32 v6, 1.0, v6
	v_rcp_f32_e32 v9, v4
	v_add_f32_e32 v4, 1.0, v7
	v_add_f32_e32 v5, 1.0, v5
	v_rcp_f32_e32 v6, v6
	v_rcp_f32_e32 v2, v2
	v_rcp_f32_e32 v3, v3
	v_rcp_f32_e32 v4, v4
	v_rcp_f32_e32 v5, v5
	v_cvt_pk_bf16_f32 v2, v6, v2
	s_and_b64 vcc, exec, s[4:5]
	v_cvt_pk_bf16_f32 v3, v3, v4
	v_cvt_pk_bf16_f32 v4, v10, v8
	v_cvt_pk_bf16_f32 v5, v9, v5
	s_mov_b64 s[4:5], -1
	global_store_dwordx4 v[18:19], v[2:5], off offset:256
	s_cbranch_vccnz .LBB0_985
	s_andn2_b64 vcc, exec, s[8:9]
	s_cbranch_vccnz .LBB0_984
	s_barrier
	s_branch .LBB0_984

;     __device__ __forceinline__ bool next(int i, Unit& u) const { u.aux = 0; return t.map(i, u.pm, u.pn); }
;     __device__ __forceinline__ bool next(int i, Unit& u) const { u.aux = i & 1; return t.map(i >> 1, u.pm, u.pn); }
; #define PG8_STAGE(bufoff, goff, voff) do { _Pragma("unroll") for (int _i = 0; _i < 2; ++_i) \
;         __builtin_amdgcn_raw_ptr_buffer_load_lds(rsrc, (PG8_LAS void*)(lds + (bufoff) + ldsw + _i * 8192), 16, (int)(voff), (int)((goff) + _i * p1##voff), 0, 0); } while (0)
; #define PG8_LDA(dst, b, h) do { _Pragma("unroll") for (int m = 0; m < 4; ++m) dst[m] = PG8_LD8(lds + PG8_SA(b, h) + aoff + m * 2048); } while (0)
; #define PG8_LDB(dst, b, h) do { _Pragma("unroll") for (int n = 0; n < 2; ++n) dst[n] = PG8_LD8(lds + PG8_SB(b, h) + boff + n * 2048); } while (0)
; #define PG8_WAIT_V(n) asm volatile("s_waitcnt vmcnt(" #n ")" ::: "memory")
; #define PG8_WAIT_L(n) asm volatile("s_waitcnt lgkmcnt(" #n ")" ::: "memory")
; #define PG8_BAR __builtin_amdgcn_s_barrier()
; template <class Epi, class Sched, bool ALIGN_EPI, bool F8 = false, int F8SC = F8_SCALES>
; __device__ __forceinline__ void gemm_phase(PG8_LAS unsigned char* lds, const __amdgpu_buffer_rsrc_t rsrc, const int lda, const int ldb, const int K, const Sched& S, const Epi& E) {
;     ...
;     for (;;) {
;         const bool has_next = S.next(ui + 1, nxt);
;         unsigned nA = cA, nB = cB; if (has_next) { S.bases(nxt, nA, nB); nA = __builtin_amdgcn_readfirstlane(nA); nB = __builtin_amdgcn_readfirstlane(nB); }
; #pragma unroll 1
;         for (int t = 0; t < nt; t += 2) {
;             const bool last = (t == nt - 2);
;             const unsigned a1 = cA + (unsigned)(t + 1) * kstep;
;             const unsigned a2 = last ? nA : cA + (unsigned)(t + 2) * kstep, b2 = last ? nB : cB + (unsigned)(t + 2) * kstep;
;             const unsigned a3 = a2 + kstep, b3 = b2 + kstep;
;             PG8_LDB(B0, 0, 0); PG8_LDB(B1, 0, 1); PG8_SCHED; PG8_LDA(At, 0, 0); PG8_STAGE(PG8_SA(1, 1), a1 + hsA, voffA);
;             PG8_WAIT_V(8); PG8_WAIT_L(0); PG8_BAR; PG8_MMA(0, 0, At, B0); PG8_MMA(0, 1, At, B1); PG8_BAR; PG8_SCHED;
;             PG8_LDA(At, 0, 1); PG8_STAGE(PG8_SB(0, 0), b2, voffB); PG8_STAGE(PG8_SB(0, 1), b2 + hsB, voffB); PG8_STAGE(PG8_SA(0, 0), a2, voffA);
;             PG8_WAIT_V(8); PG8_WAIT_L(0); PG8_BAR; PG8_MMA(1, 0, At, B0); PG8_MMA(1, 1, At, B1); PG8_BAR; PG8_SCHED;
.LBB0_1020:
	s_add_i32 s40, s39, 0x20080
	s_mov_b32 s41, 0
	s_mov_b64 s[4:5], -1
	s_mov_b64 s[10:11], 0
	ds_read_b128 v[140:143], v135
	ds_read_b128 v[144:147], v135 offset:1024
	ds_read_b128 v[148:151], v135 offset:2048
	ds_read_b128 v[152:155], v135 offset:3072
	ds_read_b128 v[156:159], v136
	ds_read_b128 v[160:163], v136 offset:1024
	ds_read_b128 v[164:167], v136 offset:2048
	ds_read_b128 v[168:171], v136 offset:3072
	s_add_i32 s44, s41, 0x100
	s_add_i32 s45, s44, s39
	s_and_b64 s[42:43], s[10:11], exec
	s_cselect_b32 s47, s37, s45
	s_add_i32 s44, s44, s36
	s_add_i32 s42, s47, 0x80
	s_and_b64 s[10:11], s[10:11], exec
	s_cselect_b32 s50, s38, s44
	s_add_i32 s53, s40, s41
	s_add_i32 s41, s50, 0x10080
	s_add_i32 s11, s50, 0x18080
	s_add_i32 s10, s47, 0x10080
	s_add_i32 s54, s53, 0x10000
	s_add_i32 s52, s50, 0x8000
	s_add_i32 s51, s50, 0x10000
	s_add_i32 s49, s50, 0x18000
	s_add_i32 s48, s47, 0x10000
	s_add_i32 s46, s47, 0x20000
	s_add_i32 s45, s47, 0x30000
	s_add_i32 s44, s50, 0x80
	s_add_i32 s43, s50, 0x8080
	s_mov_b32 s80, s96
	s_mov_b32 m0, s28
	ds_read_b128 v[172:175], v137
	ds_read_b128 v[176:179], v137 offset:1024
	ds_read_b128 v[180:183], v137 offset:2048
	ds_read_b128 v[184:187], v137 offset:3072
	ds_read_b128 v[188:191], v137 offset:4096
	ds_read_b128 v[192:195], v137 offset:5120
	ds_read_b128 v[196:199], v137 offset:6144
	ds_read_b128 v[200:203], v137 offset:7168
	buffer_load_dwordx4 v1, s[80:83], s53 offen lds
	s_mov_b32 m0, s29
	s_nop 0
	buffer_load_dwordx4 v1, s[80:83], s54 offen lds
	s_waitcnt vmcnt(8)
	s_waitcnt lgkmcnt(0)
	s_barrier
	s_setprio 1
	s_waitcnt lgkmcnt(7)
	v_mfma_f32_16x16x32_bf16 v[126:129], v[140:143], v[172:175], 0
	v_mfma_f32_16x16x32_bf16 v[122:125], v[148:151], v[172:175], 0
	s_waitcnt lgkmcnt(5)
	v_mfma_f32_16x16x32_bf16 v[118:121], v[140:143], v[180:183], 0
	v_mfma_f32_16x16x32_bf16 v[114:117], v[148:151], v[180:183], 0
	s_waitcnt lgkmcnt(3)
	v_mfma_f32_16x16x32_bf16 v[102:105], v[140:143], v[188:191], 0
	v_mfma_f32_16x16x32_bf16 v[98:101], v[148:151], v[188:191], 0
	s_waitcnt lgkmcnt(1)
	v_mfma_f32_16x16x32_bf16 v[86:89], v[140:143], v[196:199], 0
	v_mfma_f32_16x16x32_bf16 v[82:85], v[148:151], v[196:199], 0
	v_mfma_f32_16x16x32_bf16 v[126:129], v[144:147], v[176:179], v[126:129]
	v_mfma_f32_16x16x32_bf16 v[122:125], v[152:155], v[176:179], v[122:125]
	v_mfma_f32_16x16x32_bf16 v[118:121], v[144:147], v[184:187], v[118:121]
	v_mfma_f32_16x16x32_bf16 v[114:117], v[152:155], v[184:187], v[114:117]
	v_mfma_f32_16x16x32_bf16 v[102:105], v[144:147], v[192:195], v[102:105]
	v_mfma_f32_16x16x32_bf16 v[98:101], v[152:155], v[192:195], v[98:101]
	s_waitcnt lgkmcnt(0)
	v_mfma_f32_16x16x32_bf16 v[86:89], v[144:147], v[200:203], v[86:89]
	v_mfma_f32_16x16x32_bf16 v[82:85], v[152:155], v[200:203], v[82:85]
	s_setprio 0
	s_setprio 1
	v_mfma_f32_16x16x32_bf16 v[110:113], v[156:159], v[172:175], 0
	v_mfma_f32_16x16x32_bf16 v[106:109], v[164:167], v[172:175], 0
	v_mfma_f32_16x16x32_bf16 v[94:97], v[156:159], v[180:183], 0
	v_mfma_f32_16x16x32_bf16 v[90:93], v[164:167], v[180:183], 0
	v_mfma_f32_16x16x32_bf16 v[78:81], v[156:159], v[188:191], 0
	v_mfma_f32_16x16x32_bf16 v[74:77], v[164:167], v[188:191], 0
	v_mfma_f32_16x16x32_bf16 v[70:73], v[156:159], v[196:199], 0
	v_mfma_f32_16x16x32_bf16 v[66:69], v[164:167], v[196:199], 0
	v_mfma_f32_16x16x32_bf16 v[110:113], v[160:163], v[176:179], v[110:113]
	v_mfma_f32_16x16x32_bf16 v[106:109], v[168:171], v[176:179], v[106:109]
	v_mfma_f32_16x16x32_bf16 v[94:97], v[160:163], v[184:187], v[94:97]
	v_mfma_f32_16x16x32_bf16 v[90:93], v[168:171], v[184:187], v[90:93]
	v_mfma_f32_16x16x32_bf16 v[78:81], v[160:163], v[192:195], v[78:81]
	v_mfma_f32_16x16x32_bf16 v[74:77], v[168:171], v[192:195], v[74:77]
	v_mfma_f32_16x16x32_bf16 v[70:73], v[160:163], v[200:203], v[70:73]
	v_mfma_f32_16x16x32_bf16 v[66:69], v[168:171], v[200:203], v[66:69]
	s_setprio 0
	s_barrier
	s_mov_b32 m0, s14
	ds_read_b128 v[172:175], v137 offset:16384
	ds_read_b128 v[176:179], v137 offset:17408
	ds_read_b128 v[180:183], v137 offset:18432
	ds_read_b128 v[184:187], v137 offset:19456
	ds_read_b128 v[188:191], v137 offset:20480
	ds_read_b128 v[192:195], v137 offset:21504
	ds_read_b128 v[196:199], v137 offset:22528
	ds_read_b128 v[200:203], v137 offset:23552
	buffer_load_dwordx4 v134, s[80:83], s50 offen lds
	s_mov_b32 m0, s15
	s_nop 0
	buffer_load_dwordx4 v134, s[80:83], s52 offen lds
	s_mov_b32 m0, s16
	s_nop 0
	buffer_load_dwordx4 v134, s[80:83], s51 offen lds
	s_mov_b32 m0, s17
	s_nop 0
	buffer_load_dwordx4 v134, s[80:83], s49 offen lds
	s_mov_b32 m0, s13
	s_nop 0
	buffer_load_dwordx4 v1, s[80:83], s47 offen lds
	s_mov_b32 m0, s18
	s_nop 0
	buffer_load_dwordx4 v1, s[80:83], s48 offen lds
	s_waitcnt vmcnt(8)
	s_waitcnt lgkmcnt(0)
	s_barrier
; #define PG8_STAGE(bufoff, goff, voff) do { _Pragma("unroll") for (int _i = 0; _i < 2; ++_i) \
;         __builtin_amdgcn_raw_ptr_buffer_load_lds(rsrc, (PG8_LAS void*)(lds + (bufoff) + ldsw + _i * 8192), 16, (int)(voff), (int)((goff) + _i * p1##voff), 0, 0); } while (0)
; #define PG8_LDA(dst, b, h) do { _Pragma("unroll") for (int m = 0; m < 4; ++m) dst[m] = PG8_LD8(lds + PG8_SA(b, h) + aoff + m * 2048); } while (0)
; #define PG8_LDB(dst, b, h) do { _Pragma("unroll") for (int n = 0; n < 2; ++n) dst[n] = PG8_LD8(lds + PG8_SB(b, h) + boff + n * 2048); } while (0)
; #define PG8_WAIT_V(n) asm volatile("s_waitcnt vmcnt(" #n ")" ::: "memory")
; #define PG8_WAIT_L(n) asm volatile("s_waitcnt lgkmcnt(" #n ")" ::: "memory")
; #define PG8_BAR __builtin_amdgcn_s_barrier()
; #define PG8_SCHED __builtin_amdgcn_sched_barrier(0)
; template <class Epi, class Sched, bool ALIGN_EPI, bool F8 = false, int F8SC = F8_SCALES>
; __device__ __forceinline__ void gemm_phase(PG8_LAS unsigned char* lds, const __amdgpu_buffer_rsrc_t rsrc, const int lda, const int ldb, const int K, const Sched& S, const Epi& E) {
;     ...
;             PG8_WAIT_V(8); PG8_WAIT_L(0); PG8_BAR; PG8_MMA(0, 0, At, B0); PG8_MMA(0, 1, At, B1); PG8_BAR; PG8_SCHED;
;             PG8_LDA(At, 0, 1); PG8_STAGE(PG8_SB(0, 0), b2, voffB); PG8_STAGE(PG8_SB(0, 1), b2 + hsB, voffB); PG8_STAGE(PG8_SA(0, 0), a2, voffA);
;             PG8_WAIT_V(8); PG8_WAIT_L(0); PG8_BAR; PG8_MMA(1, 0, At, B0); PG8_MMA(1, 1, At, B1); PG8_BAR; PG8_SCHED;
;             PG8_LDB(B0, 1, 0); PG8_LDB(B1, 1, 1); PG8_SCHED; PG8_LDA(At, 1, 0); PG8_STAGE(PG8_SA(0, 1), a2 + hsA, voffA);
;             PG8_WAIT_V(8); PG8_WAIT_L(0); PG8_BAR; PG8_MMA(0, 0, At, B0); PG8_MMA(0, 1, At, B1); PG8_BAR; PG8_SCHED;
;             PG8_LDA(At, 1, 1); PG8_STAGE(PG8_SB(1, 0), b3, voffB); PG8_STAGE(PG8_SB(1, 1), b3 + hsB, voffB); PG8_STAGE(PG8_SA(1, 0), a3, voffA);
;             PG8_WAIT_V(8); PG8_WAIT_L(0); PG8_BAR; PG8_MMA(1, 0, At, B0); PG8_MMA(1, 1, At, B1); PG8_BAR; PG8_SCHED;
	s_setprio 1
	s_waitcnt lgkmcnt(7)
	v_mfma_f32_16x16x32_bf16 v[62:65], v[140:143], v[172:175], 0
	v_mfma_f32_16x16x32_bf16 v[58:61], v[148:151], v[172:175], 0
	s_waitcnt lgkmcnt(5)
	v_mfma_f32_16x16x32_bf16 v[54:57], v[140:143], v[180:183], 0
	v_mfma_f32_16x16x32_bf16 v[50:53], v[148:151], v[180:183], 0
	s_waitcnt lgkmcnt(3)
	v_mfma_f32_16x16x32_bf16 v[38:41], v[140:143], v[188:191], 0
	v_mfma_f32_16x16x32_bf16 v[34:37], v[148:151], v[188:191], 0
	s_waitcnt lgkmcnt(1)
	v_mfma_f32_16x16x32_bf16 v[22:25], v[140:143], v[196:199], 0
	v_mfma_f32_16x16x32_bf16 v[18:21], v[148:151], v[196:199], 0
	v_mfma_f32_16x16x32_bf16 v[62:65], v[144:147], v[176:179], v[62:65]
	v_mfma_f32_16x16x32_bf16 v[58:61], v[152:155], v[176:179], v[58:61]
	v_mfma_f32_16x16x32_bf16 v[54:57], v[144:147], v[184:187], v[54:57]
	v_mfma_f32_16x16x32_bf16 v[50:53], v[152:155], v[184:187], v[50:53]
	v_mfma_f32_16x16x32_bf16 v[38:41], v[144:147], v[192:195], v[38:41]
	v_mfma_f32_16x16x32_bf16 v[34:37], v[152:155], v[192:195], v[34:37]
	s_waitcnt lgkmcnt(0)
	v_mfma_f32_16x16x32_bf16 v[22:25], v[144:147], v[200:203], v[22:25]
	v_mfma_f32_16x16x32_bf16 v[18:21], v[152:155], v[200:203], v[18:21]
	s_setprio 0
	s_setprio 1
	v_mfma_f32_16x16x32_bf16 v[46:49], v[156:159], v[172:175], 0
	v_mfma_f32_16x16x32_bf16 v[42:45], v[164:167], v[172:175], 0
	v_mfma_f32_16x16x32_bf16 v[30:33], v[156:159], v[180:183], 0
	v_mfma_f32_16x16x32_bf16 v[26:29], v[164:167], v[180:183], 0
	v_mfma_f32_16x16x32_bf16 v[14:17], v[156:159], v[188:191], 0
	v_mfma_f32_16x16x32_bf16 v[10:13], v[164:167], v[188:191], 0
	v_mfma_f32_16x16x32_bf16 v[6:9], v[156:159], v[196:199], 0
	v_mfma_f32_16x16x32_bf16 v[2:5], v[164:167], v[196:199], 0
	v_mfma_f32_16x16x32_bf16 v[46:49], v[160:163], v[176:179], v[46:49]
	v_mfma_f32_16x16x32_bf16 v[42:45], v[168:171], v[176:179], v[42:45]
	v_mfma_f32_16x16x32_bf16 v[30:33], v[160:163], v[184:187], v[30:33]
	v_mfma_f32_16x16x32_bf16 v[26:29], v[168:171], v[184:187], v[26:29]
	v_mfma_f32_16x16x32_bf16 v[14:17], v[160:163], v[192:195], v[14:17]
	v_mfma_f32_16x16x32_bf16 v[10:13], v[168:171], v[192:195], v[10:13]
	v_mfma_f32_16x16x32_bf16 v[6:9], v[160:163], v[200:203], v[6:9]
	v_mfma_f32_16x16x32_bf16 v[2:5], v[168:171], v[200:203], v[2:5]
	s_setprio 0
	s_barrier
	ds_read_b128 v[140:143], v138
	ds_read_b128 v[144:147], v138 offset:1024
	ds_read_b128 v[148:151], v138 offset:2048
	ds_read_b128 v[152:155], v138 offset:3072
	ds_read_b128 v[156:159], v139
	ds_read_b128 v[160:163], v139 offset:1024
	ds_read_b128 v[164:167], v139 offset:2048
	ds_read_b128 v[168:171], v139 offset:3072
	s_mov_b32 m0, s19
	ds_read_b128 v[172:175], v137 offset:32768
	ds_read_b128 v[176:179], v137 offset:33792
	ds_read_b128 v[180:183], v137 offset:34816
	ds_read_b128 v[184:187], v137 offset:35840
	ds_read_b128 v[188:191], v137 offset:36864
	ds_read_b128 v[192:195], v137 offset:37888
	ds_read_b128 v[196:199], v137 offset:38912
	ds_read_b128 v[200:203], v137 offset:39936
	buffer_load_dwordx4 v1, s[80:83], s46 offen lds
	s_mov_b32 m0, s20
	s_nop 0
	buffer_load_dwordx4 v1, s[80:83], s45 offen lds
	s_waitcnt vmcnt(8)
	s_waitcnt lgkmcnt(0)
	s_barrier
	s_setprio 1
	s_waitcnt lgkmcnt(7)
	v_mfma_f32_16x16x32_bf16 v[126:129], v[140:143], v[172:175], v[126:129]
	v_mfma_f32_16x16x32_bf16 v[122:125], v[148:151], v[172:175], v[122:125]
	s_waitcnt lgkmcnt(5)
	v_mfma_f32_16x16x32_bf16 v[118:121], v[140:143], v[180:183], v[118:121]
	v_mfma_f32_16x16x32_bf16 v[114:117], v[148:151], v[180:183], v[114:117]
	s_waitcnt lgkmcnt(3)
	v_mfma_f32_16x16x32_bf16 v[102:105], v[140:143], v[188:191], v[102:105]
	v_mfma_f32_16x16x32_bf16 v[98:101], v[148:151], v[188:191], v[98:101]
	s_waitcnt lgkmcnt(1)
	v_mfma_f32_16x16x32_bf16 v[86:89], v[140:143], v[196:199], v[86:89]
	v_mfma_f32_16x16x32_bf16 v[82:85], v[148:151], v[196:199], v[82:85]
	v_mfma_f32_16x16x32_bf16 v[126:129], v[144:147], v[176:179], v[126:129]
	v_mfma_f32_16x16x32_bf16 v[122:125], v[152:155], v[176:179], v[122:125]
	v_mfma_f32_16x16x32_bf16 v[118:121], v[144:147], v[184:187], v[118:121]
	v_mfma_f32_16x16x32_bf16 v[114:117], v[152:155], v[184:187], v[114:117]
	v_mfma_f32_16x16x32_bf16 v[102:105], v[144:147], v[192:195], v[102:105]
	v_mfma_f32_16x16x32_bf16 v[98:101], v[152:155], v[192:195], v[98:101]
	s_waitcnt lgkmcnt(0)
	v_mfma_f32_16x16x32_bf16 v[86:89], v[144:147], v[200:203], v[86:89]
	v_mfma_f32_16x16x32_bf16 v[82:85], v[152:155], v[200:203], v[82:85]
	s_setprio 0
	s_setprio 1
	v_mfma_f32_16x16x32_bf16 v[110:113], v[156:159], v[172:175], v[110:113]
	v_mfma_f32_16x16x32_bf16 v[106:109], v[164:167], v[172:175], v[106:109]
	v_mfma_f32_16x16x32_bf16 v[94:97], v[156:159], v[180:183], v[94:97]
	v_mfma_f32_16x16x32_bf16 v[90:93], v[164:167], v[180:183], v[90:93]
	v_mfma_f32_16x16x32_bf16 v[78:81], v[156:159], v[188:191], v[78:81]
	v_mfma_f32_16x16x32_bf16 v[74:77], v[164:167], v[188:191], v[74:77]
	v_mfma_f32_16x16x32_bf16 v[70:73], v[156:159], v[196:199], v[70:73]
	v_mfma_f32_16x16x32_bf16 v[66:69], v[164:167], v[196:199], v[66:69]
	v_mfma_f32_16x16x32_bf16 v[110:113], v[160:163], v[176:179], v[110:113]
	v_mfma_f32_16x16x32_bf16 v[106:109], v[168:171], v[176:179], v[106:109]
	v_mfma_f32_16x16x32_bf16 v[94:97], v[160:163], v[184:187], v[94:97]
	v_mfma_f32_16x16x32_bf16 v[90:93], v[168:171], v[184:187], v[90:93]
	v_mfma_f32_16x16x32_bf16 v[78:81], v[160:163], v[192:195], v[78:81]
	v_mfma_f32_16x16x32_bf16 v[74:77], v[168:171], v[192:195], v[74:77]
	v_mfma_f32_16x16x32_bf16 v[70:73], v[160:163], v[200:203], v[70:73]
	v_mfma_f32_16x16x32_bf16 v[66:69], v[168:171], v[200:203], v[66:69]
	s_setprio 0
	s_barrier
; #define PG8_STAGE(bufoff, goff, voff) do { _Pragma("unroll") for (int _i = 0; _i < 2; ++_i) \
;         __builtin_amdgcn_raw_ptr_buffer_load_lds(rsrc, (PG8_LAS void*)(lds + (bufoff) + ldsw + _i * 8192), 16, (int)(voff), (int)((goff) + _i * p1##voff), 0, 0); } while (0)
; #define PG8_LDA(dst, b, h) do { _Pragma("unroll") for (int m = 0; m < 4; ++m) dst[m] = PG8_LD8(lds + PG8_SA(b, h) + aoff + m * 2048); } while (0)
; #define PG8_LDB(dst, b, h) do { _Pragma("unroll") for (int n = 0; n < 2; ++n) dst[n] = PG8_LD8(lds + PG8_SB(b, h) + boff + n * 2048); } while (0)
; #define PG8_WAIT_V(n) asm volatile("s_waitcnt vmcnt(" #n ")" ::: "memory")
; #define PG8_WAIT_L(n) asm volatile("s_waitcnt lgkmcnt(" #n ")" ::: "memory")
; #define PG8_BAR __builtin_amdgcn_s_barrier()
; #define PG8_SCHED __builtin_amdgcn_sched_barrier(0)
; template <class Epi, class Sched, bool ALIGN_EPI, bool F8 = false, int F8SC = F8_SCALES>
; __device__ __forceinline__ void gemm_phase(PG8_LAS unsigned char* lds, const __amdgpu_buffer_rsrc_t rsrc, const int lda, const int ldb, const int K, const Sched& S, const Epi& E) {
;     ...
;         for (int t = 0; t < nt; t += 2) {
;             const bool last = (t == nt - 2);
;             const unsigned a1 = cA + (unsigned)(t + 1) * kstep;
;             const unsigned a2 = last ? nA : cA + (unsigned)(t + 2) * kstep, b2 = last ? nB : cB + (unsigned)(t + 2) * kstep;
;             const unsigned a3 = a2 + kstep, b3 = b2 + kstep;
;             PG8_LDB(B0, 0, 0); PG8_LDB(B1, 0, 1); PG8_SCHED; PG8_LDA(At, 0, 0); PG8_STAGE(PG8_SA(1, 1), a1 + hsA, voffA);
;     ...
;             PG8_WAIT_V(8); PG8_WAIT_L(0); PG8_BAR; PG8_MMA(0, 0, At, B0); PG8_MMA(0, 1, At, B1); PG8_BAR; PG8_SCHED;
;             PG8_LDA(At, 1, 1); PG8_STAGE(PG8_SB(1, 0), b3, voffB); PG8_STAGE(PG8_SB(1, 1), b3 + hsB, voffB); PG8_STAGE(PG8_SA(1, 0), a3, voffA);
;             PG8_WAIT_V(8); PG8_WAIT_L(0); PG8_BAR; PG8_MMA(1, 0, At, B0); PG8_MMA(1, 1, At, B1); PG8_BAR; PG8_SCHED;
	s_mov_b32 m0, s22
	ds_read_b128 v[172:175], v137 offset:49152
	ds_read_b128 v[176:179], v137 offset:50176
	ds_read_b128 v[180:183], v137 offset:51200
	ds_read_b128 v[184:187], v137 offset:52224
	ds_read_b128 v[188:191], v137 offset:53248
	ds_read_b128 v[192:195], v137 offset:54272
	ds_read_b128 v[196:199], v137 offset:55296
	ds_read_b128 v[200:203], v137 offset:56320
	buffer_load_dwordx4 v134, s[80:83], s44 offen lds
	s_mov_b32 m0, s23
	s_nop 0
	buffer_load_dwordx4 v134, s[80:83], s43 offen lds
	s_mov_b32 m0, s26
	s_nop 0
	buffer_load_dwordx4 v134, s[80:83], s41 offen lds
	s_mov_b32 m0, s27
	s_nop 0
	buffer_load_dwordx4 v134, s[80:83], s11 offen lds
	s_mov_b32 m0, s24
	s_nop 0
	buffer_load_dwordx4 v1, s[80:83], s42 offen lds
	s_mov_b32 m0, s25
	s_nop 0
	buffer_load_dwordx4 v1, s[80:83], s10 offen lds
	s_waitcnt vmcnt(8)
	s_waitcnt lgkmcnt(0)
	s_barrier
	s_setprio 1
	s_waitcnt lgkmcnt(7)
	v_mfma_f32_16x16x32_bf16 v[62:65], v[140:143], v[172:175], v[62:65]
	v_mfma_f32_16x16x32_bf16 v[58:61], v[148:151], v[172:175], v[58:61]
	s_waitcnt lgkmcnt(5)
	v_mfma_f32_16x16x32_bf16 v[54:57], v[140:143], v[180:183], v[54:57]
	v_mfma_f32_16x16x32_bf16 v[50:53], v[148:151], v[180:183], v[50:53]
	s_waitcnt lgkmcnt(3)
	v_mfma_f32_16x16x32_bf16 v[38:41], v[140:143], v[188:191], v[38:41]
	v_mfma_f32_16x16x32_bf16 v[34:37], v[148:151], v[188:191], v[34:37]
	s_waitcnt lgkmcnt(1)
	v_mfma_f32_16x16x32_bf16 v[22:25], v[140:143], v[196:199], v[22:25]
	v_mfma_f32_16x16x32_bf16 v[18:21], v[148:151], v[196:199], v[18:21]
	v_mfma_f32_16x16x32_bf16 v[62:65], v[144:147], v[176:179], v[62:65]
	v_mfma_f32_16x16x32_bf16 v[58:61], v[152:155], v[176:179], v[58:61]
	v_mfma_f32_16x16x32_bf16 v[54:57], v[144:147], v[184:187], v[54:57]
	v_mfma_f32_16x16x32_bf16 v[50:53], v[152:155], v[184:187], v[50:53]
	v_mfma_f32_16x16x32_bf16 v[38:41], v[144:147], v[192:195], v[38:41]
	v_mfma_f32_16x16x32_bf16 v[34:37], v[152:155], v[192:195], v[34:37]
	s_waitcnt lgkmcnt(0)
	v_mfma_f32_16x16x32_bf16 v[22:25], v[144:147], v[200:203], v[22:25]
	v_mfma_f32_16x16x32_bf16 v[18:21], v[152:155], v[200:203], v[18:21]
	s_setprio 0
	s_setprio 1
	v_mfma_f32_16x16x32_bf16 v[46:49], v[156:159], v[172:175], v[46:49]
	v_mfma_f32_16x16x32_bf16 v[42:45], v[164:167], v[172:175], v[42:45]
	v_mfma_f32_16x16x32_bf16 v[30:33], v[156:159], v[180:183], v[30:33]
	v_mfma_f32_16x16x32_bf16 v[26:29], v[164:167], v[180:183], v[26:29]
	v_mfma_f32_16x16x32_bf16 v[14:17], v[156:159], v[188:191], v[14:17]
	v_mfma_f32_16x16x32_bf16 v[10:13], v[164:167], v[188:191], v[10:13]
	v_mfma_f32_16x16x32_bf16 v[6:9], v[156:159], v[196:199], v[6:9]
	v_mfma_f32_16x16x32_bf16 v[2:5], v[164:167], v[196:199], v[2:5]
	v_mfma_f32_16x16x32_bf16 v[46:49], v[160:163], v[176:179], v[46:49]
	v_mfma_f32_16x16x32_bf16 v[42:45], v[168:171], v[176:179], v[42:45]
	v_mfma_f32_16x16x32_bf16 v[30:33], v[160:163], v[184:187], v[30:33]
	v_mfma_f32_16x16x32_bf16 v[26:29], v[168:171], v[184:187], v[26:29]
	v_mfma_f32_16x16x32_bf16 v[14:17], v[160:163], v[192:195], v[14:17]
	v_mfma_f32_16x16x32_bf16 v[10:13], v[168:171], v[192:195], v[10:13]
	v_mfma_f32_16x16x32_bf16 v[6:9], v[160:163], v[200:203], v[6:9]
	v_mfma_f32_16x16x32_bf16 v[2:5], v[168:171], v[200:203], v[2:5]
	s_setprio 0
	s_barrier
	s_andn2_b64 vcc, exec, s[4:5]
	s_mov_b64 s[10:11], -1
	s_mov_b64 s[4:5], 0
	s_movk_i32 s41, 0x100
	s_cbranch_vccz .LBB0_1021
	s_branch .Lpeel_after_1021
.LBB0_1021:
	ds_read_b128 v[140:143], v135
	ds_read_b128 v[144:147], v135 offset:1024
	ds_read_b128 v[148:151], v135 offset:2048
	ds_read_b128 v[152:155], v135 offset:3072
	ds_read_b128 v[156:159], v136
	ds_read_b128 v[160:163], v136 offset:1024
	ds_read_b128 v[164:167], v136 offset:2048
	ds_read_b128 v[168:171], v136 offset:3072
	s_add_i32 s44, s41, 0x100
	s_add_i32 s45, s44, s39
	s_and_b64 s[42:43], s[10:11], exec
	s_cselect_b32 s47, s37, s45
	s_add_i32 s44, s44, s36
	s_add_i32 s42, s47, 0x80
	s_and_b64 s[10:11], s[10:11], exec
	s_cselect_b32 s50, s38, s44
	s_add_i32 s53, s40, s41
	s_add_i32 s41, s50, 0x10080
	s_add_i32 s11, s50, 0x18080
	s_add_i32 s10, s47, 0x10080
	s_add_i32 s54, s53, 0x10000
	s_add_i32 s52, s50, 0x8000
	s_add_i32 s51, s50, 0x10000
	s_add_i32 s49, s50, 0x18000
	s_add_i32 s48, s47, 0x10000
	s_add_i32 s46, s47, 0x20000
	s_add_i32 s45, s47, 0x30000
	s_add_i32 s44, s50, 0x80
	s_add_i32 s43, s50, 0x8080
	s_mov_b32 s80, s96
	s_mov_b32 m0, s28
	ds_read_b128 v[172:175], v137
	ds_read_b128 v[176:179], v137 offset:1024
	ds_read_b128 v[180:183], v137 offset:2048
	ds_read_b128 v[184:187], v137 offset:3072
	ds_read_b128 v[188:191], v137 offset:4096
	ds_read_b128 v[192:195], v137 offset:5120
	ds_read_b128 v[196:199], v137 offset:6144
	ds_read_b128 v[200:203], v137 offset:7168
	buffer_load_dwordx4 v1, s[80:83], s53 offen lds
	s_mov_b32 m0, s29
	s_nop 0
	buffer_load_dwordx4 v1, s[80:83], s54 offen lds
	s_waitcnt vmcnt(8)
	s_waitcnt lgkmcnt(0)
	s_barrier
; #define PG8_STAGE(bufoff, goff, voff) do { _Pragma("unroll") for (int _i = 0; _i < 2; ++_i) \
;         __builtin_amdgcn_raw_ptr_buffer_load_lds(rsrc, (PG8_LAS void*)(lds + (bufoff) + ldsw + _i * 8192), 16, (int)(voff), (int)((goff) + _i * p1##voff), 0, 0); } while (0)
; #define PG8_LDA(dst, b, h) do { _Pragma("unroll") for (int m = 0; m < 4; ++m) dst[m] = PG8_LD8(lds + PG8_SA(b, h) + aoff + m * 2048); } while (0)
; #define PG8_LDB(dst, b, h) do { _Pragma("unroll") for (int n = 0; n < 2; ++n) dst[n] = PG8_LD8(lds + PG8_SB(b, h) + boff + n * 2048); } while (0)
; #define PG8_WAIT_V(n) asm volatile("s_waitcnt vmcnt(" #n ")" ::: "memory")
; #define PG8_WAIT_L(n) asm volatile("s_waitcnt lgkmcnt(" #n ")" ::: "memory")
; #define PG8_BAR __builtin_amdgcn_s_barrier()
; #define PG8_SCHED __builtin_amdgcn_sched_barrier(0)
; template <class Epi, class Sched, bool ALIGN_EPI, bool F8 = false, int F8SC = F8_SCALES>
; __device__ __forceinline__ void gemm_phase(PG8_LAS unsigned char* lds, const __amdgpu_buffer_rsrc_t rsrc, const int lda, const int ldb, const int K, const Sched& S, const Epi& E) {
;     ...
;             PG8_LDB(B0, 0, 0); PG8_LDB(B1, 0, 1); PG8_SCHED; PG8_LDA(At, 0, 0); PG8_STAGE(PG8_SA(1, 1), a1 + hsA, voffA);
;             PG8_WAIT_V(8); PG8_WAIT_L(0); PG8_BAR; PG8_MMA(0, 0, At, B0); PG8_MMA(0, 1, At, B1); PG8_BAR; PG8_SCHED;
;             PG8_LDA(At, 0, 1); PG8_STAGE(PG8_SB(0, 0), b2, voffB); PG8_STAGE(PG8_SB(0, 1), b2 + hsB, voffB); PG8_STAGE(PG8_SA(0, 0), a2, voffA);
;             PG8_WAIT_V(8); PG8_WAIT_L(0); PG8_BAR; PG8_MMA(1, 0, At, B0); PG8_MMA(1, 1, At, B1); PG8_BAR; PG8_SCHED;
;             PG8_LDB(B0, 1, 0); PG8_LDB(B1, 1, 1); PG8_SCHED; PG8_LDA(At, 1, 0); PG8_STAGE(PG8_SA(0, 1), a2 + hsA, voffA);
;             PG8_WAIT_V(8); PG8_WAIT_L(0); PG8_BAR; PG8_MMA(0, 0, At, B0); PG8_MMA(0, 1, At, B1); PG8_BAR; PG8_SCHED;
	s_setprio 1
	s_waitcnt lgkmcnt(7)
	v_mfma_f32_16x16x32_bf16 v[126:129], v[140:143], v[172:175], v[126:129]
	v_mfma_f32_16x16x32_bf16 v[122:125], v[148:151], v[172:175], v[122:125]
	s_waitcnt lgkmcnt(5)
	v_mfma_f32_16x16x32_bf16 v[118:121], v[140:143], v[180:183], v[118:121]
	v_mfma_f32_16x16x32_bf16 v[114:117], v[148:151], v[180:183], v[114:117]
	s_waitcnt lgkmcnt(3)
	v_mfma_f32_16x16x32_bf16 v[102:105], v[140:143], v[188:191], v[102:105]
	v_mfma_f32_16x16x32_bf16 v[98:101], v[148:151], v[188:191], v[98:101]
	s_waitcnt lgkmcnt(1)
	v_mfma_f32_16x16x32_bf16 v[86:89], v[140:143], v[196:199], v[86:89]
	v_mfma_f32_16x16x32_bf16 v[82:85], v[148:151], v[196:199], v[82:85]
	v_mfma_f32_16x16x32_bf16 v[126:129], v[144:147], v[176:179], v[126:129]
	v_mfma_f32_16x16x32_bf16 v[122:125], v[152:155], v[176:179], v[122:125]
	v_mfma_f32_16x16x32_bf16 v[118:121], v[144:147], v[184:187], v[118:121]
	v_mfma_f32_16x16x32_bf16 v[114:117], v[152:155], v[184:187], v[114:117]
	v_mfma_f32_16x16x32_bf16 v[102:105], v[144:147], v[192:195], v[102:105]
	v_mfma_f32_16x16x32_bf16 v[98:101], v[152:155], v[192:195], v[98:101]
	s_waitcnt lgkmcnt(0)
	v_mfma_f32_16x16x32_bf16 v[86:89], v[144:147], v[200:203], v[86:89]
	v_mfma_f32_16x16x32_bf16 v[82:85], v[152:155], v[200:203], v[82:85]
	s_setprio 0
	s_setprio 1
	v_mfma_f32_16x16x32_bf16 v[110:113], v[156:159], v[172:175], v[110:113]
	v_mfma_f32_16x16x32_bf16 v[106:109], v[164:167], v[172:175], v[106:109]
	v_mfma_f32_16x16x32_bf16 v[94:97], v[156:159], v[180:183], v[94:97]
	v_mfma_f32_16x16x32_bf16 v[90:93], v[164:167], v[180:183], v[90:93]
	v_mfma_f32_16x16x32_bf16 v[78:81], v[156:159], v[188:191], v[78:81]
	v_mfma_f32_16x16x32_bf16 v[74:77], v[164:167], v[188:191], v[74:77]
	v_mfma_f32_16x16x32_bf16 v[70:73], v[156:159], v[196:199], v[70:73]
	v_mfma_f32_16x16x32_bf16 v[66:69], v[164:167], v[196:199], v[66:69]
	v_mfma_f32_16x16x32_bf16 v[110:113], v[160:163], v[176:179], v[110:113]
	v_mfma_f32_16x16x32_bf16 v[106:109], v[168:171], v[176:179], v[106:109]
	v_mfma_f32_16x16x32_bf16 v[94:97], v[160:163], v[184:187], v[94:97]
	v_mfma_f32_16x16x32_bf16 v[90:93], v[168:171], v[184:187], v[90:93]
	v_mfma_f32_16x16x32_bf16 v[78:81], v[160:163], v[192:195], v[78:81]
	v_mfma_f32_16x16x32_bf16 v[74:77], v[168:171], v[192:195], v[74:77]
	v_mfma_f32_16x16x32_bf16 v[70:73], v[160:163], v[200:203], v[70:73]
	v_mfma_f32_16x16x32_bf16 v[66:69], v[168:171], v[200:203], v[66:69]
	s_setprio 0
	s_barrier
	s_mov_b32 m0, s14
	ds_read_b128 v[172:175], v137 offset:16384
	ds_read_b128 v[176:179], v137 offset:17408
	ds_read_b128 v[180:183], v137 offset:18432
	ds_read_b128 v[184:187], v137 offset:19456
	ds_read_b128 v[188:191], v137 offset:20480
	ds_read_b128 v[192:195], v137 offset:21504
	ds_read_b128 v[196:199], v137 offset:22528
	ds_read_b128 v[200:203], v137 offset:23552
	buffer_load_dwordx4 v134, s[80:83], s50 offen lds
	s_mov_b32 m0, s15
	s_nop 0
	buffer_load_dwordx4 v134, s[80:83], s52 offen lds
	s_mov_b32 m0, s16
	s_nop 0
	buffer_load_dwordx4 v134, s[80:83], s51 offen lds
	s_mov_b32 m0, s17
	s_nop 0
	buffer_load_dwordx4 v134, s[80:83], s49 offen lds
	s_mov_b32 m0, s13
	s_nop 0
	buffer_load_dwordx4 v1, s[80:83], s47 offen lds
	s_mov_b32 m0, s18
	s_nop 0
	buffer_load_dwordx4 v1, s[80:83], s48 offen lds
	s_waitcnt vmcnt(8)
	s_waitcnt lgkmcnt(0)
	s_barrier
	s_setprio 1
	s_waitcnt lgkmcnt(7)
	v_mfma_f32_16x16x32_bf16 v[62:65], v[140:143], v[172:175], v[62:65]
	v_mfma_f32_16x16x32_bf16 v[58:61], v[148:151], v[172:175], v[58:61]
	s_waitcnt lgkmcnt(5)
	v_mfma_f32_16x16x32_bf16 v[54:57], v[140:143], v[180:183], v[54:57]
	v_mfma_f32_16x16x32_bf16 v[50:53], v[148:151], v[180:183], v[50:53]
	s_waitcnt lgkmcnt(3)
	v_mfma_f32_16x16x32_bf16 v[38:41], v[140:143], v[188:191], v[38:41]
	v_mfma_f32_16x16x32_bf16 v[34:37], v[148:151], v[188:191], v[34:37]
	s_waitcnt lgkmcnt(1)
	v_mfma_f32_16x16x32_bf16 v[22:25], v[140:143], v[196:199], v[22:25]
	v_mfma_f32_16x16x32_bf16 v[18:21], v[148:151], v[196:199], v[18:21]
	v_mfma_f32_16x16x32_bf16 v[62:65], v[144:147], v[176:179], v[62:65]
	v_mfma_f32_16x16x32_bf16 v[58:61], v[152:155], v[176:179], v[58:61]
	v_mfma_f32_16x16x32_bf16 v[54:57], v[144:147], v[184:187], v[54:57]
	v_mfma_f32_16x16x32_bf16 v[50:53], v[152:155], v[184:187], v[50:53]
	v_mfma_f32_16x16x32_bf16 v[38:41], v[144:147], v[192:195], v[38:41]
	v_mfma_f32_16x16x32_bf16 v[34:37], v[152:155], v[192:195], v[34:37]
	s_waitcnt lgkmcnt(0)
	v_mfma_f32_16x16x32_bf16 v[22:25], v[144:147], v[200:203], v[22:25]
	v_mfma_f32_16x16x32_bf16 v[18:21], v[152:155], v[200:203], v[18:21]
	s_setprio 0
	s_setprio 1
	v_mfma_f32_16x16x32_bf16 v[46:49], v[156:159], v[172:175], v[46:49]
	v_mfma_f32_16x16x32_bf16 v[42:45], v[164:167], v[172:175], v[42:45]
	v_mfma_f32_16x16x32_bf16 v[30:33], v[156:159], v[180:183], v[30:33]
	v_mfma_f32_16x16x32_bf16 v[26:29], v[164:167], v[180:183], v[26:29]
	v_mfma_f32_16x16x32_bf16 v[14:17], v[156:159], v[188:191], v[14:17]
	v_mfma_f32_16x16x32_bf16 v[10:13], v[164:167], v[188:191], v[10:13]
	v_mfma_f32_16x16x32_bf16 v[6:9], v[156:159], v[196:199], v[6:9]
	v_mfma_f32_16x16x32_bf16 v[2:5], v[164:167], v[196:199], v[2:5]
	v_mfma_f32_16x16x32_bf16 v[46:49], v[160:163], v[176:179], v[46:49]
	v_mfma_f32_16x16x32_bf16 v[42:45], v[168:171], v[176:179], v[42:45]
	v_mfma_f32_16x16x32_bf16 v[30:33], v[160:163], v[184:187], v[30:33]
	v_mfma_f32_16x16x32_bf16 v[26:29], v[168:171], v[184:187], v[26:29]
	v_mfma_f32_16x16x32_bf16 v[14:17], v[160:163], v[192:195], v[14:17]
	v_mfma_f32_16x16x32_bf16 v[10:13], v[168:171], v[192:195], v[10:13]
	v_mfma_f32_16x16x32_bf16 v[6:9], v[160:163], v[200:203], v[6:9]
	v_mfma_f32_16x16x32_bf16 v[2:5], v[168:171], v[200:203], v[2:5]
	s_setprio 0
	s_barrier
; #define PG8_STAGE(bufoff, goff, voff) do { _Pragma("unroll") for (int _i = 0; _i < 2; ++_i) \
;         __builtin_amdgcn_raw_ptr_buffer_load_lds(rsrc, (PG8_LAS void*)(lds + (bufoff) + ldsw + _i * 8192), 16, (int)(voff), (int)((goff) + _i * p1##voff), 0, 0); } while (0)
; #define PG8_LDA(dst, b, h) do { _Pragma("unroll") for (int m = 0; m < 4; ++m) dst[m] = PG8_LD8(lds + PG8_SA(b, h) + aoff + m * 2048); } while (0)
; #define PG8_LDB(dst, b, h) do { _Pragma("unroll") for (int n = 0; n < 2; ++n) dst[n] = PG8_LD8(lds + PG8_SB(b, h) + boff + n * 2048); } while (0)
; #define PG8_WAIT_V(n) asm volatile("s_waitcnt vmcnt(" #n ")" ::: "memory")
; #define PG8_WAIT_L(n) asm volatile("s_waitcnt lgkmcnt(" #n ")" ::: "memory")
; #define PG8_BAR __builtin_amdgcn_s_barrier()
; #define PG8_SCHED __builtin_amdgcn_sched_barrier(0)
; template <class Epi, class Sched, bool ALIGN_EPI, bool F8 = false, int F8SC = F8_SCALES>
; __device__ __forceinline__ void gemm_phase(PG8_LAS unsigned char* lds, const __amdgpu_buffer_rsrc_t rsrc, const int lda, const int ldb, const int K, const Sched& S, const Epi& E) {
;     ...
;             PG8_LDB(B0, 1, 0); PG8_LDB(B1, 1, 1); PG8_SCHED; PG8_LDA(At, 1, 0); PG8_STAGE(PG8_SA(0, 1), a2 + hsA, voffA);
;             PG8_WAIT_V(8); PG8_WAIT_L(0); PG8_BAR; PG8_MMA(0, 0, At, B0); PG8_MMA(0, 1, At, B1); PG8_BAR; PG8_SCHED;
;             PG8_LDA(At, 1, 1); PG8_STAGE(PG8_SB(1, 0), b3, voffB); PG8_STAGE(PG8_SB(1, 1), b3 + hsB, voffB); PG8_STAGE(PG8_SA(1, 0), a3, voffA);
;             PG8_WAIT_V(8); PG8_WAIT_L(0); PG8_BAR; PG8_MMA(1, 0, At, B0); PG8_MMA(1, 1, At, B1); PG8_BAR; PG8_SCHED;
	ds_read_b128 v[140:143], v138
	ds_read_b128 v[144:147], v138 offset:1024
	ds_read_b128 v[148:151], v138 offset:2048
	ds_read_b128 v[152:155], v138 offset:3072
	ds_read_b128 v[156:159], v139
	ds_read_b128 v[160:163], v139 offset:1024
	ds_read_b128 v[164:167], v139 offset:2048
	ds_read_b128 v[168:171], v139 offset:3072
	s_mov_b32 m0, s19
	ds_read_b128 v[172:175], v137 offset:32768
	ds_read_b128 v[176:179], v137 offset:33792
	ds_read_b128 v[180:183], v137 offset:34816
	ds_read_b128 v[184:187], v137 offset:35840
	ds_read_b128 v[188:191], v137 offset:36864
	ds_read_b128 v[192:195], v137 offset:37888
	ds_read_b128 v[196:199], v137 offset:38912
	ds_read_b128 v[200:203], v137 offset:39936
	buffer_load_dwordx4 v1, s[80:83], s46 offen lds
	s_mov_b32 m0, s20
	s_nop 0
	buffer_load_dwordx4 v1, s[80:83], s45 offen lds
	s_waitcnt vmcnt(8)
	s_waitcnt lgkmcnt(0)
	s_barrier
	s_setprio 1
	s_waitcnt lgkmcnt(7)
	v_mfma_f32_16x16x32_bf16 v[126:129], v[140:143], v[172:175], v[126:129]
	v_mfma_f32_16x16x32_bf16 v[122:125], v[148:151], v[172:175], v[122:125]
	s_waitcnt lgkmcnt(5)
	v_mfma_f32_16x16x32_bf16 v[118:121], v[140:143], v[180:183], v[118:121]
	v_mfma_f32_16x16x32_bf16 v[114:117], v[148:151], v[180:183], v[114:117]
	s_waitcnt lgkmcnt(3)
	v_mfma_f32_16x16x32_bf16 v[102:105], v[140:143], v[188:191], v[102:105]
	v_mfma_f32_16x16x32_bf16 v[98:101], v[148:151], v[188:191], v[98:101]
	s_waitcnt lgkmcnt(1)
	v_mfma_f32_16x16x32_bf16 v[86:89], v[140:143], v[196:199], v[86:89]
	v_mfma_f32_16x16x32_bf16 v[82:85], v[148:151], v[196:199], v[82:85]
	v_mfma_f32_16x16x32_bf16 v[126:129], v[144:147], v[176:179], v[126:129]
	v_mfma_f32_16x16x32_bf16 v[122:125], v[152:155], v[176:179], v[122:125]
	v_mfma_f32_16x16x32_bf16 v[118:121], v[144:147], v[184:187], v[118:121]
	v_mfma_f32_16x16x32_bf16 v[114:117], v[152:155], v[184:187], v[114:117]
	v_mfma_f32_16x16x32_bf16 v[102:105], v[144:147], v[192:195], v[102:105]
	v_mfma_f32_16x16x32_bf16 v[98:101], v[152:155], v[192:195], v[98:101]
	s_waitcnt lgkmcnt(0)
	v_mfma_f32_16x16x32_bf16 v[86:89], v[144:147], v[200:203], v[86:89]
	v_mfma_f32_16x16x32_bf16 v[82:85], v[152:155], v[200:203], v[82:85]
	s_setprio 0
	s_setprio 1
	v_mfma_f32_16x16x32_bf16 v[110:113], v[156:159], v[172:175], v[110:113]
	v_mfma_f32_16x16x32_bf16 v[106:109], v[164:167], v[172:175], v[106:109]
	v_mfma_f32_16x16x32_bf16 v[94:97], v[156:159], v[180:183], v[94:97]
	v_mfma_f32_16x16x32_bf16 v[90:93], v[164:167], v[180:183], v[90:93]
	v_mfma_f32_16x16x32_bf16 v[78:81], v[156:159], v[188:191], v[78:81]
	v_mfma_f32_16x16x32_bf16 v[74:77], v[164:167], v[188:191], v[74:77]
	v_mfma_f32_16x16x32_bf16 v[70:73], v[156:159], v[196:199], v[70:73]
	v_mfma_f32_16x16x32_bf16 v[66:69], v[164:167], v[196:199], v[66:69]
	v_mfma_f32_16x16x32_bf16 v[110:113], v[160:163], v[176:179], v[110:113]
	v_mfma_f32_16x16x32_bf16 v[106:109], v[168:171], v[176:179], v[106:109]
	v_mfma_f32_16x16x32_bf16 v[94:97], v[160:163], v[184:187], v[94:97]
	v_mfma_f32_16x16x32_bf16 v[90:93], v[168:171], v[184:187], v[90:93]
	v_mfma_f32_16x16x32_bf16 v[78:81], v[160:163], v[192:195], v[78:81]
	v_mfma_f32_16x16x32_bf16 v[74:77], v[168:171], v[192:195], v[74:77]
	v_mfma_f32_16x16x32_bf16 v[70:73], v[160:163], v[200:203], v[70:73]
	v_mfma_f32_16x16x32_bf16 v[66:69], v[168:171], v[200:203], v[66:69]
	s_setprio 0
	s_barrier
	s_mov_b32 m0, s22
	ds_read_b128 v[172:175], v137 offset:49152
	ds_read_b128 v[176:179], v137 offset:50176
	ds_read_b128 v[180:183], v137 offset:51200
	ds_read_b128 v[184:187], v137 offset:52224
	ds_read_b128 v[188:191], v137 offset:53248
	ds_read_b128 v[192:195], v137 offset:54272
	ds_read_b128 v[196:199], v137 offset:55296
	ds_read_b128 v[200:203], v137 offset:56320
	buffer_load_dwordx4 v134, s[80:83], s44 offen lds
	s_mov_b32 m0, s23
	s_nop 0
	buffer_load_dwordx4 v134, s[80:83], s43 offen lds
	s_mov_b32 m0, s26
	s_nop 0
	buffer_load_dwordx4 v134, s[80:83], s41 offen lds
	s_mov_b32 m0, s27
	s_nop 0
	buffer_load_dwordx4 v134, s[80:83], s11 offen lds
	s_mov_b32 m0, s24
	s_nop 0
	buffer_load_dwordx4 v1, s[80:83], s42 offen lds
	s_mov_b32 m0, s25
	s_nop 0
	buffer_load_dwordx4 v1, s[80:83], s10 offen lds
	s_waitcnt vmcnt(8)
	s_waitcnt lgkmcnt(0)
	s_barrier
	s_setprio 1
	s_waitcnt lgkmcnt(7)
	v_mfma_f32_16x16x32_bf16 v[62:65], v[140:143], v[172:175], v[62:65]
	v_mfma_f32_16x16x32_bf16 v[58:61], v[148:151], v[172:175], v[58:61]
	s_waitcnt lgkmcnt(5)
	v_mfma_f32_16x16x32_bf16 v[54:57], v[140:143], v[180:183], v[54:57]
	v_mfma_f32_16x16x32_bf16 v[50:53], v[148:151], v[180:183], v[50:53]
	s_waitcnt lgkmcnt(3)
	v_mfma_f32_16x16x32_bf16 v[38:41], v[140:143], v[188:191], v[38:41]
	v_mfma_f32_16x16x32_bf16 v[34:37], v[148:151], v[188:191], v[34:37]
	s_waitcnt lgkmcnt(1)
	v_mfma_f32_16x16x32_bf16 v[22:25], v[140:143], v[196:199], v[22:25]
	v_mfma_f32_16x16x32_bf16 v[18:21], v[148:151], v[196:199], v[18:21]
	v_mfma_f32_16x16x32_bf16 v[62:65], v[144:147], v[176:179], v[62:65]
	v_mfma_f32_16x16x32_bf16 v[58:61], v[152:155], v[176:179], v[58:61]
	v_mfma_f32_16x16x32_bf16 v[54:57], v[144:147], v[184:187], v[54:57]
	v_mfma_f32_16x16x32_bf16 v[50:53], v[152:155], v[184:187], v[50:53]
	v_mfma_f32_16x16x32_bf16 v[38:41], v[144:147], v[192:195], v[38:41]
	v_mfma_f32_16x16x32_bf16 v[34:37], v[152:155], v[192:195], v[34:37]
	s_waitcnt lgkmcnt(0)
	v_mfma_f32_16x16x32_bf16 v[22:25], v[144:147], v[200:203], v[22:25]
	v_mfma_f32_16x16x32_bf16 v[18:21], v[152:155], v[200:203], v[18:21]
	s_setprio 0
	s_setprio 1
	v_mfma_f32_16x16x32_bf16 v[46:49], v[156:159], v[172:175], v[46:49]
	v_mfma_f32_16x16x32_bf16 v[42:45], v[164:167], v[172:175], v[42:45]
	v_mfma_f32_16x16x32_bf16 v[30:33], v[156:159], v[180:183], v[30:33]
	v_mfma_f32_16x16x32_bf16 v[26:29], v[164:167], v[180:183], v[26:29]
	v_mfma_f32_16x16x32_bf16 v[14:17], v[156:159], v[188:191], v[14:17]
	v_mfma_f32_16x16x32_bf16 v[10:13], v[164:167], v[188:191], v[10:13]
	v_mfma_f32_16x16x32_bf16 v[6:9], v[156:159], v[196:199], v[6:9]
	v_mfma_f32_16x16x32_bf16 v[2:5], v[164:167], v[196:199], v[2:5]
	v_mfma_f32_16x16x32_bf16 v[46:49], v[160:163], v[176:179], v[46:49]
	v_mfma_f32_16x16x32_bf16 v[42:45], v[168:171], v[176:179], v[42:45]
	v_mfma_f32_16x16x32_bf16 v[30:33], v[160:163], v[184:187], v[30:33]
	v_mfma_f32_16x16x32_bf16 v[26:29], v[168:171], v[184:187], v[26:29]
	v_mfma_f32_16x16x32_bf16 v[14:17], v[160:163], v[192:195], v[14:17]
	v_mfma_f32_16x16x32_bf16 v[10:13], v[168:171], v[192:195], v[10:13]
	v_mfma_f32_16x16x32_bf16 v[6:9], v[160:163], v[200:203], v[6:9]
	v_mfma_f32_16x16x32_bf16 v[2:5], v[168:171], v[200:203], v[2:5]
	s_setprio 0
	s_barrier
	s_andn2_b64 vcc, exec, s[4:5]
	s_mov_b64 s[10:11], -1
	s_mov_b64 s[4:5], 0
	s_movk_i32 s41, 0x100
	s_cbranch_vccz .LBB0_1021
; __device__ __forceinline__ u32x4 pack8(const f32x4& v0, const f32x4& v1) { u32x4 w; w.x = cvt_pk_bf16(v0[0], v0[1]); w.y = cvt_pk_bf16(v0[2], v0[3]); w.z = cvt_pk_bf16(v1[0], v1[1]); w.w = cvt_pk_bf16(v1[2], v1[3]); return w; }
; #define PG8_BAR __builtin_amdgcn_s_barrier()
; #define PG8_ZERO() do { _Pragma("unroll") for (int a = 0; a < 2; ++a) _Pragma("unroll") for (int b = 0; b < 2; ++b) _Pragma("unroll") for (int m = 0; m < 4; ++m) _Pragma("unroll") for (int n = 0; n < 2; ++n) acc[a][b][m][n] = (f32x4){0.f, 0.f, 0.f, 0.f}; } while (0)
; #define EPI_ROWLOOP _Pragma("unroll") for (int ai = 0; ai < 2; ++ai) _Pragma("unroll") for (int m = 0; m < 4; ++m)
; template <class Epi, class Sched, bool ALIGN_EPI, bool F8 = false, int F8SC = F8_SCALES>
; __device__ __forceinline__ void gemm_phase(PG8_LAS unsigned char* lds, const __amdgpu_buffer_rsrc_t rsrc, const int lda, const int ldb, const int K, const Sched& S, const Epi& E) {
;     ...
;         if constexpr (ALIGN_EPI) { if (wr == 0) PG8_BAR; }
;         bool keep; { int t2 = threadIdx.x; asm volatile("" : "+v"(t2)); const int w2 = __builtin_amdgcn_readfirstlane(t2 >> 6), l2 = t2 & 63; keep = E(acc, cur, w2 >> 2, w2 & 3, l2 & 15, l2 >> 4); }
;         if (!has_next) break;
;         if (!keep) PG8_ZERO();
;         cur = nxt; cA = nA; cB = nB; ++ui;
;         if constexpr (ALIGN_EPI) { if (wr == 1) PG8_BAR; }
;     __device__ __forceinline__ bool operator()(f32x4 (&acc)[2][2][4][2], const Unit& u, int wr, int wc, int fr, int fq) const {
;         const int row0 = u.pm * BM + wr * 64 + fr, col0 = u.pn * BM + wc * 32 + 8 * fq;
;         EPI_ROWLOOP { bf16_t* rowp = O + (size_t)(row0 + ai * HALF + m * 16) * ldc + col0;
; #pragma unroll
;             for (int bj = 0; bj < 2; ++bj) *(u32x4*)(rowp + bj * HALF) = pack8(acc[ai][bj][m][0], acc[ai][bj][m][1]); }
;         return false;
;     }
.Lpeel_after_1021:
	s_and_b64 vcc, exec, s[8:9]
	s_cbranch_vccz .LBB0_1024
	s_barrier
.LBB0_1024:
	v_mov_b32_e32 v141, v0
	s_lshl_b32 s5, s35, 8
	v_readfirstlane_b32 s4, v141
	s_ashr_i32 s10, s4, 2
	s_andn2_b32 s10, s10, 63
	s_lshr_b32 s4, s4, 1
	s_add_i32 s10, s10, s5
	s_lshl_b32 s5, s34, 8
	s_and_b32 s4, s4, 0x60
	v_and_or_b32 v140, v141, 15, s10
	s_or_b32 s4, s4, s5
	v_lshrrev_b32_e32 v141, 1, v141
	v_and_or_b32 v142, v141, 24, s4
	v_ashrrev_i32_e32 v141, 31, v140
	v_ashrrev_i32_e32 v143, 31, v142
	v_lshlrev_b64 v[144:145], 11, v[140:141]
	v_lshl_add_u64 v[144:145], s[66:67], 0, v[144:145]
	v_lshlrev_b64 v[142:143], 1, v[142:143]
	v_lshl_add_u64 v[144:145], v[144:145], 0, v[142:143]
	s_mov_b64 s[4:5], 0x40000
	v_cvt_pk_bf16_f32 v70, v70, v71
	v_cvt_pk_bf16_f32 v71, v72, v73
	v_cvt_pk_bf16_f32 v72, v66, v67
	v_lshl_add_u64 v[66:67], v[144:145], 0, s[4:5]
	s_mov_b32 s4, 0x40000
	v_cvt_pk_bf16_f32 v62, v62, v63
	v_cvt_pk_bf16_f32 v63, v64, v65
	v_cvt_pk_bf16_f32 v64, v58, v59
	v_add_co_u32_e32 v58, vcc, s4, v144
	v_cvt_pk_bf16_f32 v46, v46, v47
	v_cvt_pk_bf16_f32 v47, v48, v49
	v_cvt_pk_bf16_f32 v48, v42, v43
	v_cvt_pk_bf16_f32 v49, v44, v45
	s_mov_b64 s[4:5], 0x48000
	v_addc_co_u32_e32 v59, vcc, 0, v145, vcc
	global_store_dwordx4 v[66:67], v[46:49], off offset:256
	v_cvt_pk_bf16_f32 v110, v110, v111
	v_cvt_pk_bf16_f32 v111, v112, v113
	v_lshl_add_u64 v[46:47], v[144:145], 0, s[4:5]
	s_mov_b32 s4, 0x48000
	v_cvt_pk_bf16_f32 v112, v106, v107
	v_or_b32_e32 v106, 16, v140
	v_add_co_u32_e32 v48, vcc, s4, v144
	v_cvt_pk_bf16_f32 v30, v30, v31
	v_cvt_pk_bf16_f32 v31, v32, v33
	v_cvt_pk_bf16_f32 v32, v26, v27
	v_cvt_pk_bf16_f32 v33, v28, v29
	s_mov_b64 s[4:5], 0x50000
	v_ashrrev_i32_e32 v107, 31, v106
	v_cvt_pk_bf16_f32 v94, v94, v95
	v_cvt_pk_bf16_f32 v95, v96, v97
	v_cvt_pk_bf16_f32 v96, v90, v91
	v_or_b32_e32 v90, 32, v140
	v_addc_co_u32_e32 v49, vcc, 0, v145, vcc
	global_store_dwordx4 v[46:47], v[30:33], off offset:256
	v_lshlrev_b64 v[106:107], 11, v[106:107]
	v_ashrrev_i32_e32 v91, 31, v90
	v_lshl_add_u64 v[30:31], v[144:145], 0, s[4:5]
	s_mov_b32 s4, 0x50000
	v_cvt_pk_bf16_f32 v78, v78, v79
	v_cvt_pk_bf16_f32 v79, v80, v81
	v_cvt_pk_bf16_f32 v80, v74, v75
	v_or_b32_e32 v74, 48, v140
	v_add_co_u32_e32 v32, vcc, s4, v144
	v_cvt_pk_bf16_f32 v14, v14, v15
	v_cvt_pk_bf16_f32 v15, v16, v17
	v_cvt_pk_bf16_f32 v16, v10, v11
	v_cvt_pk_bf16_f32 v17, v12, v13
	s_mov_b64 s[4:5], 0x58000
	v_cvt_pk_bf16_f32 v113, v108, v109
	v_lshl_add_u64 v[106:107], s[66:67], 0, v[106:107]
	v_lshlrev_b64 v[90:91], 11, v[90:91]
	v_ashrrev_i32_e32 v75, 31, v74
	v_addc_co_u32_e32 v33, vcc, 0, v145, vcc
	global_store_dwordx4 v[30:31], v[14:17], off offset:256
	global_store_dwordx4 v[144:145], v[110:113], off offset:256
	v_cvt_pk_bf16_f32 v97, v92, v93
	v_lshl_add_u64 v[14:15], v[144:145], 0, s[4:5]
	s_mov_b32 s4, 0x58000
	v_lshl_add_u64 v[110:111], v[106:107], 0, v[142:143]
	v_lshl_add_u64 v[90:91], s[66:67], 0, v[90:91]
	v_lshlrev_b64 v[74:75], 11, v[74:75]
	v_add_co_u32_e32 v16, vcc, s4, v144
	global_store_dwordx4 v[110:111], v[94:97], off offset:256
	v_cvt_pk_bf16_f32 v81, v76, v77
	v_lshl_add_u64 v[74:75], s[66:67], 0, v[74:75]
	v_lshl_add_u64 v[94:95], v[90:91], 0, v[142:143]
	v_addc_co_u32_e32 v17, vcc, 0, v145, vcc
	v_cvt_pk_bf16_f32 v126, v126, v127
	v_cvt_pk_bf16_f32 v127, v128, v129
	v_cvt_pk_bf16_f32 v128, v122, v123
	v_cvt_pk_bf16_f32 v129, v124, v125
	v_cvt_pk_bf16_f32 v106, v118, v119
	v_cvt_pk_bf16_f32 v107, v120, v121
	v_cvt_pk_bf16_f32 v108, v114, v115
	v_cvt_pk_bf16_f32 v109, v116, v117
	v_cvt_pk_bf16_f32 v90, v102, v103
	v_cvt_pk_bf16_f32 v91, v104, v105
	v_cvt_pk_bf16_f32 v92, v98, v99
	v_cvt_pk_bf16_f32 v93, v100, v101
	global_store_dwordx4 v[94:95], v[78:81], off offset:256
	v_cvt_pk_bf16_f32 v76, v82, v83
	v_cvt_pk_bf16_f32 v77, v84, v85
	v_lshl_add_u64 v[78:79], v[74:75], 0, v[142:143]
	v_cvt_pk_bf16_f32 v74, v86, v87
	v_cvt_pk_bf16_f32 v75, v88, v89
	v_cvt_pk_bf16_f32 v73, v68, v69
	v_cvt_pk_bf16_f32 v65, v60, v61
	v_cvt_pk_bf16_f32 v42, v54, v55
	v_cvt_pk_bf16_f32 v43, v56, v57
	v_cvt_pk_bf16_f32 v44, v50, v51
	v_cvt_pk_bf16_f32 v45, v52, v53
	v_cvt_pk_bf16_f32 v26, v38, v39
	v_cvt_pk_bf16_f32 v27, v40, v41
	v_cvt_pk_bf16_f32 v28, v34, v35
	v_cvt_pk_bf16_f32 v29, v36, v37
	v_cvt_pk_bf16_f32 v10, v22, v23
	v_cvt_pk_bf16_f32 v11, v24, v25
	v_cvt_pk_bf16_f32 v12, v18, v19
	v_cvt_pk_bf16_f32 v13, v20, v21
	v_cvt_pk_bf16_f32 v6, v6, v7
	v_cvt_pk_bf16_f32 v7, v8, v9
	v_cvt_pk_bf16_f32 v8, v2, v3
	v_cvt_pk_bf16_f32 v9, v4, v5
	s_and_b64 vcc, exec, s[2:3]
	s_mov_b64 s[2:3], -1
	global_store_dwordx4 v[144:145], v[126:129], off
	global_store_dwordx4 v[110:111], v[106:109], off
	global_store_dwordx4 v[94:95], v[90:93], off
	global_store_dwordx4 v[78:79], v[74:77], off
	global_store_dwordx4 v[78:79], v[70:73], off offset:256
	global_store_dwordx4 v[58:59], v[62:65], off
	global_store_dwordx4 v[48:49], v[42:45], off
	global_store_dwordx4 v[32:33], v[26:29], off
	global_store_dwordx4 v[16:17], v[10:13], off
	global_store_dwordx4 v[14:15], v[6:9], off offset:256
	s_cbranch_vccnz .LBB0_1011
	s_andn2_b64 vcc, exec, s[6:7]
	s_cbranch_vccnz .LBB0_1010
	s_barrier
	s_branch .LBB0_1010
